# speedup vs baseline: 1.1013x; 1.0134x over previous
.LBB0_2:
	s_or_b64 exec, exec, s[14:15]
	s_load_dwordx2 s[0:1], s[0:1], 0x18
	v_lshrrev_b32_e32 v67, 5, v206
	v_or_b32_e32 v132, s11, v67
	s_lshl_b64 s[14:15], s[18:19], 14
	v_ashrrev_i32_e32 v133, 31, v132
	v_and_b32_e32 v124, 31, v0
	s_waitcnt lgkmcnt(0)
	s_add_u32 s14, s0, s14
	v_lshlrev_b64 v[2:3], 12, v[132:133]
	s_addc_u32 s15, s1, s15
	s_add_i32 s0, s7, 0x100
	v_lshl_add_u64 v[2:3], s[8:9], 0, v[2:3]
	v_lshlrev_b32_e32 v190, 4, v124
	v_mov_b32_e32 v191, 0
	s_and_b32 s26, s0, 0x300
	v_lshl_add_u64 v[130:131], v[2:3], 0, v[190:191]
	s_mov_b64 s[0:1], 0x30000
	v_lshl_add_u64 v[126:127], v[130:131], 0, s[0:1]
	s_mov_b64 s[0:1], 0x32000
	v_lshl_add_u64 v[128:129], v[130:131], 0, s[0:1]
	s_mov_b64 s[0:1], 0x34000
	v_lshl_add_u64 v[134:135], v[130:131], 0, s[0:1]
	s_mov_b64 s[0:1], 0x36000
	v_lshl_add_u64 v[136:137], v[130:131], 0, s[0:1]
	s_mov_b64 s[0:1], 0x38000
	v_lshl_add_u64 v[138:139], v[130:131], 0, s[0:1]
	s_mov_b64 s[0:1], 0x3a000
	v_lshl_add_u64 v[140:141], v[130:131], 0, s[0:1]
	s_mov_b64 s[0:1], 0x3c000
	s_or_b32 s24, s7, 0x80
	v_lshl_add_u64 v[142:143], v[130:131], 0, s[0:1]
	s_mov_b64 s[0:1], 0x3e000
	s_lshl_b32 s20, s7, 2
	v_lshl_add_u64 v[144:145], v[130:131], 0, s[0:1]
	s_lshl_b32 s8, s24, 2
	s_mov_b32 s9, s21
	v_lshl_add_u64 v[2:3], v[126:127], 0, s[20:21]
	v_lshl_add_u64 v[4:5], v[128:129], 0, s[20:21]
	v_lshl_add_u64 v[6:7], v[134:135], 0, s[20:21]
	v_lshl_add_u64 v[8:9], v[136:137], 0, s[20:21]
	v_lshl_add_u64 v[10:11], v[138:139], 0, s[20:21]
	v_lshl_add_u64 v[12:13], v[140:141], 0, s[20:21]
	v_lshl_add_u64 v[14:15], v[142:143], 0, s[20:21]
	v_lshl_add_u64 v[16:17], v[144:145], 0, s[20:21]
	v_lshl_add_u64 v[18:19], v[126:127], 0, s[8:9]
	v_lshl_add_u64 v[20:21], v[128:129], 0, s[8:9]
	v_lshl_add_u64 v[22:23], v[134:135], 0, s[8:9]
	v_lshl_add_u64 v[24:25], v[136:137], 0, s[8:9]
	s_lshl_b32 s0, s26, 2
	s_mov_b32 s1, s21
	v_lshl_add_u64 v[72:73], v[138:139], 0, s[8:9]
	v_lshl_add_u64 v[102:103], v[140:141], 0, s[8:9]
	v_lshl_add_u64 v[104:105], v[142:143], 0, s[8:9]
	v_lshl_add_u64 v[106:107], v[144:145], 0, s[8:9]
	v_lshl_add_u64 v[108:109], v[126:127], 0, s[0:1]
	v_lshl_add_u64 v[110:111], v[128:129], 0, s[0:1]
	v_lshl_add_u64 v[112:113], v[134:135], 0, s[0:1]
	v_lshl_add_u64 v[114:115], v[136:137], 0, s[0:1]
	v_lshl_add_u64 v[116:117], v[138:139], 0, s[0:1]
	v_lshl_add_u64 v[118:119], v[140:141], 0, s[0:1]
	v_lshl_add_u64 v[120:121], v[142:143], 0, s[0:1]
	v_lshl_add_u64 v[122:123], v[144:145], 0, s[0:1]
	global_load_dwordx4 v[68:71], v[2:3], off nt
	global_load_dwordx4 v[78:81], v[4:5], off nt
	global_load_dwordx4 v[82:85], v[6:7], off nt
	global_load_dwordx4 v[90:93], v[8:9], off nt
	global_load_dwordx4 v[98:101], v[10:11], off nt
	global_load_dwordx4 v[62:65], v[12:13], off nt
	global_load_dwordx4 v[54:57], v[14:15], off nt
	global_load_dwordx4 v[46:49], v[16:17], off nt
	global_load_dwordx4 v[94:97], v[18:19], off nt
	global_load_dwordx4 v[86:89], v[20:21], off nt
	global_load_dwordx4 v[74:77], v[22:23], off nt
	global_load_dwordx4 v[58:61], v[24:25], off nt
	global_load_dwordx4 v[50:53], v[72:73], off nt
	global_load_dwordx4 v[42:45], v[102:103], off nt
	global_load_dwordx4 v[38:41], v[104:105], off nt
	global_load_dwordx4 v[34:37], v[106:107], off nt
	global_load_dwordx4 v[30:33], v[108:109], off nt
	global_load_dwordx4 v[26:29], v[110:111], off nt
	s_nop 0
	global_load_dwordx4 v[22:25], v[112:113], off nt
	global_load_dwordx4 v[18:21], v[114:115], off nt
	global_load_dwordx4 v[14:17], v[116:117], off nt
	global_load_dwordx4 v[10:13], v[118:119], off nt
	global_load_dwordx4 v[6:9], v[120:121], off nt
	global_load_dwordx4 v[2:5], v[122:123], off nt
	s_waitcnt vmcnt(25)
	v_div_scale_f32 v72, s[22:23], v207, v207, 1.0
	v_rcp_f32_e32 v73, v72
	s_lshl_b32 s11, s10, 2
	s_mul_i32 s19, s35, 0x1100
	s_add_i32 s22, s11, 0x26600
	v_fma_f32 v103, -v72, v73, 1.0
	v_fmac_f32_e32 v73, v103, v73
	v_div_scale_f32 v103, vcc, 1.0, v207, 1.0
	v_mul_f32_e32 v104, v103, v73
	v_fma_f32 v105, -v72, v104, v103
	v_fmac_f32_e32 v104, v105, v73
	v_fma_f32 v72, -v72, v104, v103
	v_div_fmas_f32 v72, v72, v73, v104
	v_div_fixup_f32 v72, v72, v207, 1.0
	s_waitcnt vmcnt(24)
	v_fma_f32 v208, v72, v1, -v66
	v_lshl_add_u32 v1, v206, 2, s22
	s_add_i32 s19, s19, 0x22200
	ds_write_b32 v1, v72
	v_lshl_or_b32 v1, v124, 3, s19
	v_lshl_add_u32 v187, v67, 2, s22
	s_movk_i32 s22, 0x110
	v_mad_u32_u24 v186, v67, s22, v1
	s_add_i32 s22, s7, 0x180
	v_and_b32_e32 v102, 15, v0
	s_lshl_b32 s27, s34, 8
	s_and_b32 s25, s22, 0x380
	s_add_i32 s22, s7, 0x280
	v_lshlrev_b32_e32 v66, 2, v124
	v_mul_u32_u24_e32 v1, 0x110, v102
	v_and_b32_e32 v209, 48, v0
	s_and_b32 s23, s22, 0x380
	s_add_i32 s22, s7, 0x300
	v_mov_b32_e32 v67, 0x200
	s_addk_i32 s27, 0x380
	v_or_b32_e32 v133, s7, v66
	v_add3_u32 v1, s19, v1, v209
	s_lshl_b32 s19, s35, 15
	v_lshlrev_b32_e32 v210, 4, v206
	v_or_b32_e32 v189, s24, v66
	s_xor_b32 s24, s7, 0x200
	s_and_b32 s22, s22, 0x300
	v_bitop3_b32 v197, s7, v66, v67 bitop3:0xde
	s_and_b32 s7, s27, 0x380
	v_lshrrev_b32_e32 v185, 4, v206
	s_ashr_i32 s11, s10, 31
	v_or_b32_e32 v184, s19, v210
	v_or_b32_e32 v188, s26, v66
	v_or_b32_e32 v198, s25, v66
	v_or_b32_e32 v196, s23, v66
	v_or_b32_e32 v195, s22, v66
	v_or_b32_e32 v194, s7, v66
	v_mov_b32_e32 v102, v133
	v_and_b32_e32 v248, 2, v206
	v_cmp_ne_u32_e32 vcc, 0, v248
	v_mov_b32_e32 v249, 0x44444444
	v_mov_b32_e32 v250, 0xeeeeeeee
	s_nop 1
	v_cndmask_b32_e32 v223, v249, v250, vcc
	v_lshrrev_b32_e32 v248, 4, v206
	v_lshl_add_u32 v248, v248, 4, 1
	v_add_u32_e32 v249, 0, v248
	v_cvt_f32_u32_e32 v249, v249
	v_add_u32_e32 v250, 1, v248
	v_cvt_f32_u32_e32 v250, v250
	v_cvt_pk_bf16_f32 v232, v249, v250
	v_add_u32_e32 v249, 2, v248
	v_cvt_f32_u32_e32 v249, v249
	v_add_u32_e32 v250, 3, v248
	v_cvt_f32_u32_e32 v250, v250
	v_cvt_pk_bf16_f32 v233, v249, v250
	v_add_u32_e32 v249, 4, v248
	v_cvt_f32_u32_e32 v249, v249
	v_add_u32_e32 v250, 5, v248
	v_cvt_f32_u32_e32 v250, v250
	v_cvt_pk_bf16_f32 v234, v249, v250
	v_add_u32_e32 v249, 6, v248
	v_cvt_f32_u32_e32 v249, v249
	v_add_u32_e32 v250, 7, v248
	v_cvt_f32_u32_e32 v250, v250
	v_cvt_pk_bf16_f32 v235, v249, v250
	v_add_u32_e32 v249, 8, v248
	v_cvt_f32_u32_e32 v249, v249
	v_add_u32_e32 v250, 9, v248
	v_cvt_f32_u32_e32 v250, v250
	v_cvt_pk_bf16_f32 v236, v249, v250
	v_add_u32_e32 v249, 10, v248
	v_cvt_f32_u32_e32 v249, v249
	v_add_u32_e32 v250, 11, v248
	v_cvt_f32_u32_e32 v250, v250
	v_cvt_pk_bf16_f32 v237, v249, v250
	v_add_u32_e32 v249, 12, v248
	v_cvt_f32_u32_e32 v249, v249
	v_add_u32_e32 v250, 13, v248
	v_cvt_f32_u32_e32 v250, v250
	v_cvt_pk_bf16_f32 v238, v249, v250
	v_add_u32_e32 v249, 14, v248
	v_cvt_f32_u32_e32 v249, v249
	v_add_u32_e32 v250, 15, v248
	v_cvt_f32_u32_e32 v250, v250
	v_cvt_pk_bf16_f32 v239, v249, v250
	v_and_b32_e32 v248, 15, v206
	v_lshrrev_b32_e32 v249, 2, v248
	v_and_b32_e32 v250, 1, v248
	v_lshl_add_u32 v249, v249, 1, v250
	v_and_b32_e32 v250, 3, v249
	v_lshrrev_b32_e32 v251, 4, v206
	v_cmp_eq_u32_e32 vcc, v250, v251
	v_lshrrev_b32_e32 v249, 2, v249
	v_cmp_ne_u32_e64 s[78:79], 0, v249
	v_mov_b32_e32 v250, 0x3f80
	v_mov_b32_e32 v251, 0x3f800000
	s_nop 1
	v_cndmask_b32_e64 v250, v250, v251, s[78:79]
	v_cndmask_b32_e32 v252, 0, v250, vcc
	s_lshr_b32 s77, s19, 15
	s_mulk_i32 s77, 0x1100
	s_add_i32 s77, s77, 0x22200
	v_lshrrev_b32_e32 v248, 4, v206
	v_and_b32_e32 v249, 1, v248
	v_lshrrev_b32_e32 v250, 1, v248
	v_lshlrev_b32_e32 v249, 6, v249
	v_lshl_add_u32 v253, v250, 1, v249
	v_and_b32_e32 v248, 15, v206
	v_cmp_eq_u32_e64 s[78:79], 0, v248
	v_mov_b32_e32 v244, v252
	v_mov_b32_e32 v245, 0
	v_mov_b32_e32 v246, 0
	v_mov_b32_e32 v247, 0
	v_mov_b64_e32 v[240:241], 0
	v_mov_b64_e32 v[242:243], 0
	s_nop 1
	v_smfmac_f32_16x16x64_bf16 v[240:243], v[244:247], v[232:239], v223
	s_nop 15
	s_nop 3
	s_and_saveexec_b64 s[80:81], s[78:79]
	v_cvt_u32_f32_e32 v248, v240
	v_add_u32_e32 v248, -1, v248
	v_lshl_add_u32 v248, v248, 2, s77
	v_add_u32_e32 v249, 0, v253
	ds_write_b32 v248, v249
	v_cvt_u32_f32_e32 v248, v241
	v_add_u32_e32 v248, -1, v248
	v_lshl_add_u32 v248, v248, 2, s77
	v_add_u32_e32 v249, 32, v253
	ds_write_b32 v248, v249
	v_cvt_u32_f32_e32 v248, v242
	v_add_u32_e32 v248, -1, v248
	v_lshl_add_u32 v248, v248, 2, s77
	v_add_u32_e32 v249, 16, v253
	ds_write_b32 v248, v249
	v_cvt_u32_f32_e32 v248, v243
	v_add_u32_e32 v248, -1, v248
	v_lshl_add_u32 v248, v248, 2, s77
	v_add_u32_e32 v249, 48, v253
	ds_write_b32 v248, v249
	s_or_b64 exec, exec, s[80:81]
	v_mov_b32_e32 v244, 0
	v_mov_b32_e32 v245, v252
	v_mov_b32_e32 v246, 0
	v_mov_b32_e32 v247, 0
	v_mov_b64_e32 v[240:241], 0
	v_mov_b64_e32 v[242:243], 0
	s_nop 1
	v_smfmac_f32_16x16x64_bf16 v[240:243], v[244:247], v[232:239], v223
	s_nop 15
	s_nop 3
	s_and_saveexec_b64 s[80:81], s[78:79]
	v_cvt_u32_f32_e32 v248, v240
	v_add_u32_e32 v248, -1, v248
	v_lshl_add_u32 v248, v248, 2, s77
	v_add_u32_e32 v249, 4, v253
	ds_write_b32 v248, v249
	v_cvt_u32_f32_e32 v248, v241
	v_add_u32_e32 v248, -1, v248
	v_lshl_add_u32 v248, v248, 2, s77
	v_add_u32_e32 v249, 36, v253
	ds_write_b32 v248, v249
	v_cvt_u32_f32_e32 v248, v242
	v_add_u32_e32 v248, -1, v248
	v_lshl_add_u32 v248, v248, 2, s77
	v_add_u32_e32 v249, 20, v253
	ds_write_b32 v248, v249
	v_cvt_u32_f32_e32 v248, v243
	v_add_u32_e32 v248, -1, v248
	v_lshl_add_u32 v248, v248, 2, s77
	v_add_u32_e32 v249, 52, v253
	ds_write_b32 v248, v249
	s_or_b64 exec, exec, s[80:81]
	v_mov_b32_e32 v244, 0
	v_mov_b32_e32 v245, 0
	v_mov_b32_e32 v246, v252
	v_mov_b32_e32 v247, 0
	v_mov_b64_e32 v[240:241], 0
	v_mov_b64_e32 v[242:243], 0
	s_nop 1
	v_smfmac_f32_16x16x64_bf16 v[240:243], v[244:247], v[232:239], v223
	s_nop 15
	s_nop 3
	s_and_saveexec_b64 s[80:81], s[78:79]
	v_cvt_u32_f32_e32 v248, v240
	v_add_u32_e32 v248, -1, v248
	v_lshl_add_u32 v248, v248, 2, s77
	v_add_u32_e32 v249, 8, v253
	ds_write_b32 v248, v249
	v_cvt_u32_f32_e32 v248, v241
	v_add_u32_e32 v248, -1, v248
	v_lshl_add_u32 v248, v248, 2, s77
	v_add_u32_e32 v249, 40, v253
	ds_write_b32 v248, v249
	v_cvt_u32_f32_e32 v248, v242
	v_add_u32_e32 v248, -1, v248
	v_lshl_add_u32 v248, v248, 2, s77
	v_add_u32_e32 v249, 24, v253
	ds_write_b32 v248, v249
	v_cvt_u32_f32_e32 v248, v243
	v_add_u32_e32 v248, -1, v248
	v_lshl_add_u32 v248, v248, 2, s77
	v_add_u32_e32 v249, 56, v253
	ds_write_b32 v248, v249
	s_or_b64 exec, exec, s[80:81]
	v_mov_b32_e32 v244, 0
	v_mov_b32_e32 v245, 0
	v_mov_b32_e32 v246, 0
	v_mov_b32_e32 v247, v252
	v_mov_b64_e32 v[240:241], 0
	v_mov_b64_e32 v[242:243], 0
	s_nop 1
	v_smfmac_f32_16x16x64_bf16 v[240:243], v[244:247], v[232:239], v223
	s_nop 15
	s_nop 3
	s_and_saveexec_b64 s[80:81], s[78:79]
	v_cvt_u32_f32_e32 v248, v240
	v_add_u32_e32 v248, -1, v248
	v_lshl_add_u32 v248, v248, 2, s77
	v_add_u32_e32 v249, 12, v253
	ds_write_b32 v248, v249
	v_cvt_u32_f32_e32 v248, v241
	v_add_u32_e32 v248, -1, v248
	v_lshl_add_u32 v248, v248, 2, s77
	v_add_u32_e32 v249, 44, v253
	ds_write_b32 v248, v249
	v_cvt_u32_f32_e32 v248, v242
	v_add_u32_e32 v248, -1, v248
	v_lshl_add_u32 v248, v248, 2, s77
	v_add_u32_e32 v249, 28, v253
	ds_write_b32 v248, v249
	v_cvt_u32_f32_e32 v248, v243
	v_add_u32_e32 v248, -1, v248
	v_lshl_add_u32 v248, v248, 2, s77
	v_add_u32_e32 v249, 60, v253
	ds_write_b32 v248, v249
	s_or_b64 exec, exec, s[80:81]
	v_bfe_u32 v248, v206, 3, 2
	v_lshrrev_b32_e32 v249, 5, v206
	v_lshlrev_b32_e32 v248, 4, v248
	v_lshl_or_b32 v248, v249, 3, v248
	v_and_b32_e32 v249, 7, v206
	v_or_b32_e32 v248, v248, v249
	v_lshl_add_u32 v248, v248, 2, s77
	s_waitcnt lgkmcnt(0)
	ds_read_b32 v254, v248
	v_and_b32_e32 v248, 15, v206
	v_bfe_u32 v249, v248, 1, 2
	v_lshrrev_b32_e32 v250, 3, v248
	v_lshlrev_b32_e32 v249, 4, v249
	v_lshl_or_b32 v249, v250, 3, v249
	v_and_b32_e32 v250, 1, v248
	v_lshl_or_b32 v249, v250, 2, v249
	v_lshl_add_u32 v249, v249, 2, s77
	ds_read_b128 v[248:251], v249
	s_lshr_b32 s76, s19, 6
	s_add_i32 s76, s76, 0x20000
	v_lshrrev_b32_e32 v252, 4, v206
	v_lshl_add_u32 v252, v252, 7, s76
	s_waitcnt lgkmcnt(0)
	v_add_u32_e32 v248, v252, v248
	v_add_u32_e32 v249, v252, v249
	v_add_u32_e32 v250, v252, v250
	v_add_u32_e32 v251, v252, v251
	v_cvt_pk_bf16_f32 v236, v224, v225
	v_cvt_pk_bf16_f32 v237, v226, v227
	v_lshlrev_b32_e32 v238, 16, v236
	v_and_b32_e32 v239, 0xffff0000, v236
	v_lshlrev_b32_e32 v240, 16, v237
	v_and_b32_e32 v241, 0xffff0000, v237
	v_sub_f32_e32 v238, v224, v238
	v_sub_f32_e32 v239, v225, v239
	v_sub_f32_e32 v240, v226, v240
	v_sub_f32_e32 v241, v227, v241
	v_cvt_pk_bf16_f32 v238, v238, v239
	v_cvt_pk_bf16_f32 v239, v240, v241
	ds_write_b16 v248, v236
	ds_write_b16_d16_hi v249, v236
	ds_write_b16 v250, v237
	ds_write_b16_d16_hi v251, v237
	ds_write_b16 v248, v238 offset:2176
	ds_write_b16_d16_hi v249, v238 offset:2176
	ds_write_b16 v250, v239 offset:2176
	ds_write_b16_d16_hi v251, v239 offset:2176
	s_waitcnt vmcnt(23)
	s_waitcnt vmcnt(22)
	s_waitcnt vmcnt(21)
	s_waitcnt vmcnt(20)
	s_waitcnt vmcnt(19)
	s_waitcnt vmcnt(18)
	s_waitcnt vmcnt(17)
	s_waitcnt vmcnt(16)
	ds_read_b32 v66, v187 offset:192
	v_or_b32_e32 v103, 48, v132
	v_add_u32_e32 v104, 1, v102
	v_cmp_eq_u32_e32 vcc, v102, v103
	v_add_u32_e32 v105, 3, v102
	v_add_u32_e32 v106, 2, v102
	v_cndmask_b32_e64 v72, 0, 1.0, vcc
	v_cmp_eq_u32_e32 vcc, v104, v103
	v_or_b32_e32 v107, 50, v132
	v_or_b32_e32 v108, 52, v132
	v_cndmask_b32_e64 v73, 0, 1.0, vcc
	v_cmp_eq_u32_e32 vcc, v105, v103
	s_waitcnt lgkmcnt(0)
	v_pk_fma_f32 v[68:69], v[66:67], v[68:69], v[72:73] op_sel_hi:[0,1,1] neg_lo:[1,0,0] neg_hi:[1,0,0]
	v_cvt_pk_bf16_f32 v68, v68, v69
	v_cndmask_b32_e64 v73, 0, 1.0, vcc
	v_cmp_eq_u32_e32 vcc, v106, v103
	v_or_b32_e32 v109, 54, v132
	v_or_b32_e32 v110, 56, v132
	v_cndmask_b32_e64 v72, 0, 1.0, vcc
	v_pk_fma_f32 v[66:67], v[66:67], v[70:71], v[72:73] op_sel_hi:[0,1,1] neg_lo:[1,0,0] neg_hi:[1,0,0]
	v_cvt_pk_bf16_f32 v69, v66, v67
	ds_write_b64 v186, v[68:69]
	ds_read_b32 v66, v187 offset:200
	v_cmp_eq_u32_e32 vcc, v102, v107
	v_or_b32_e32 v111, 58, v132
	v_or_b32_e32 v112, 60, v132
	v_cndmask_b32_e64 v68, 0, 1.0, vcc
	v_cmp_eq_u32_e32 vcc, v104, v107
	v_or_b32_e32 v113, 62, v132
	v_or_b32_e32 v193, 2, v132
	v_cndmask_b32_e64 v69, 0, 1.0, vcc
	v_cmp_eq_u32_e32 vcc, v105, v107
	s_waitcnt lgkmcnt(0)
	v_pk_fma_f32 v[68:69], v[66:67], v[78:79], v[68:69] op_sel_hi:[0,1,1] neg_lo:[1,0,0] neg_hi:[1,0,0]
	v_cvt_pk_bf16_f32 v68, v68, v69
	v_cndmask_b32_e64 v71, 0, 1.0, vcc
	v_cmp_eq_u32_e32 vcc, v106, v107
	v_or_b32_e32 v192, 4, v132
	v_or_b32_e32 v190, 6, v132
	v_cndmask_b32_e64 v70, 0, 1.0, vcc
	v_pk_fma_f32 v[66:67], v[66:67], v[80:81], v[70:71] op_sel_hi:[0,1,1] neg_lo:[1,0,0] neg_hi:[1,0,0]
	v_cvt_pk_bf16_f32 v69, v66, v67
	ds_write_b64 v186, v[68:69] offset:544
	ds_read_b32 v66, v187 offset:208
	v_cmp_eq_u32_e32 vcc, v102, v108
	v_or_b32_e32 v149, 8, v132
	v_or_b32_e32 v148, 10, v132
	v_cndmask_b32_e64 v68, 0, 1.0, vcc
	v_cmp_eq_u32_e32 vcc, v104, v108
	v_or_b32_e32 v147, 12, v132
	v_or_b32_e32 v146, 14, v132
	v_cndmask_b32_e64 v69, 0, 1.0, vcc
	v_cmp_eq_u32_e32 vcc, v105, v108
	s_waitcnt lgkmcnt(0)
	v_pk_fma_f32 v[68:69], v[66:67], v[82:83], v[68:69] op_sel_hi:[0,1,1] neg_lo:[1,0,0] neg_hi:[1,0,0]
	v_cvt_pk_bf16_f32 v68, v68, v69
	v_cndmask_b32_e64 v71, 0, 1.0, vcc
	v_cmp_eq_u32_e32 vcc, v106, v108
	s_nop 1
	v_cndmask_b32_e64 v70, 0, 1.0, vcc
	v_pk_fma_f32 v[66:67], v[66:67], v[84:85], v[70:71] op_sel_hi:[0,1,1] neg_lo:[1,0,0] neg_hi:[1,0,0]
	v_cvt_pk_bf16_f32 v69, v66, v67
	ds_write_b64 v186, v[68:69] offset:1088
	ds_read_b32 v66, v187 offset:216
	v_cmp_eq_u32_e32 vcc, v102, v109
	s_nop 1
	v_cndmask_b32_e64 v68, 0, 1.0, vcc
	v_cmp_eq_u32_e32 vcc, v104, v109
	s_nop 1
	v_cndmask_b32_e64 v69, 0, 1.0, vcc
	v_cmp_eq_u32_e32 vcc, v105, v109
	s_waitcnt lgkmcnt(0)
	v_pk_fma_f32 v[68:69], v[66:67], v[90:91], v[68:69] op_sel_hi:[0,1,1] neg_lo:[1,0,0] neg_hi:[1,0,0]
	v_cvt_pk_bf16_f32 v68, v68, v69
	v_cndmask_b32_e64 v71, 0, 1.0, vcc
	v_cmp_eq_u32_e32 vcc, v106, v109
	s_nop 1
	v_cndmask_b32_e64 v70, 0, 1.0, vcc
	v_pk_fma_f32 v[66:67], v[66:67], v[92:93], v[70:71] op_sel_hi:[0,1,1] neg_lo:[1,0,0] neg_hi:[1,0,0]
	v_cvt_pk_bf16_f32 v69, v66, v67
	ds_write_b64 v186, v[68:69] offset:1632
	ds_read_b32 v66, v187 offset:224
	v_cmp_eq_u32_e32 vcc, v102, v110
	s_nop 1
	v_cndmask_b32_e64 v68, 0, 1.0, vcc
	v_cmp_eq_u32_e32 vcc, v104, v110
	s_nop 1
	v_cndmask_b32_e64 v69, 0, 1.0, vcc
	v_cmp_eq_u32_e32 vcc, v105, v110
	s_waitcnt lgkmcnt(0)
	v_pk_fma_f32 v[68:69], v[66:67], v[98:99], v[68:69] op_sel_hi:[0,1,1] neg_lo:[1,0,0] neg_hi:[1,0,0]
	v_cvt_pk_bf16_f32 v68, v68, v69
	v_cndmask_b32_e64 v71, 0, 1.0, vcc
	v_cmp_eq_u32_e32 vcc, v106, v110
	s_nop 1
	v_cndmask_b32_e64 v70, 0, 1.0, vcc
	v_pk_fma_f32 v[66:67], v[66:67], v[100:101], v[70:71] op_sel_hi:[0,1,1] neg_lo:[1,0,0] neg_hi:[1,0,0]
	v_cvt_pk_bf16_f32 v69, v66, v67
	ds_write_b64 v186, v[68:69] offset:2176
	ds_read_b32 v66, v187 offset:232
	v_cmp_eq_u32_e32 vcc, v102, v111
	s_nop 1
	v_cndmask_b32_e64 v68, 0, 1.0, vcc
	v_cmp_eq_u32_e32 vcc, v104, v111
	s_nop 1
	v_cndmask_b32_e64 v69, 0, 1.0, vcc
	v_cmp_eq_u32_e32 vcc, v105, v111
	s_waitcnt lgkmcnt(0)
	v_pk_fma_f32 v[62:63], v[66:67], v[62:63], v[68:69] op_sel_hi:[0,1,1] neg_lo:[1,0,0] neg_hi:[1,0,0]
	v_cvt_pk_bf16_f32 v62, v62, v63
	v_cndmask_b32_e64 v69, 0, 1.0, vcc
	v_cmp_eq_u32_e32 vcc, v106, v111
	s_nop 1
	v_cndmask_b32_e64 v68, 0, 1.0, vcc
	v_pk_fma_f32 v[64:65], v[66:67], v[64:65], v[68:69] op_sel_hi:[0,1,1] neg_lo:[1,0,0] neg_hi:[1,0,0]
	v_cvt_pk_bf16_f32 v63, v64, v65
	ds_write_b64 v186, v[62:63] offset:2720
	ds_read_b32 v62, v187 offset:240
	v_cmp_eq_u32_e32 vcc, v102, v112
	s_nop 1
	v_cndmask_b32_e64 v64, 0, 1.0, vcc
	v_cmp_eq_u32_e32 vcc, v104, v112
	s_nop 1
	v_cndmask_b32_e64 v65, 0, 1.0, vcc
	v_cmp_eq_u32_e32 vcc, v105, v112
	s_waitcnt lgkmcnt(0)
	v_pk_fma_f32 v[54:55], v[62:63], v[54:55], v[64:65] op_sel_hi:[0,1,1] neg_lo:[1,0,0] neg_hi:[1,0,0]
	v_cvt_pk_bf16_f32 v54, v54, v55
	v_cndmask_b32_e64 v65, 0, 1.0, vcc
	v_cmp_eq_u32_e32 vcc, v106, v112
	s_nop 1
	v_cndmask_b32_e64 v64, 0, 1.0, vcc
	v_pk_fma_f32 v[56:57], v[62:63], v[56:57], v[64:65] op_sel_hi:[0,1,1] neg_lo:[1,0,0] neg_hi:[1,0,0]
	v_cvt_pk_bf16_f32 v55, v56, v57
	ds_write_b64 v186, v[54:55] offset:3264
	ds_read_b32 v54, v187 offset:248
	v_cmp_eq_u32_e32 vcc, v102, v113
	s_nop 1
	v_cndmask_b32_e64 v56, 0, 1.0, vcc
	v_cmp_eq_u32_e32 vcc, v104, v113
	s_nop 1
	v_cndmask_b32_e64 v57, 0, 1.0, vcc
	v_cmp_eq_u32_e32 vcc, v105, v113
	s_waitcnt lgkmcnt(0)
	v_pk_fma_f32 v[46:47], v[54:55], v[46:47], v[56:57] op_sel_hi:[0,1,1] neg_lo:[1,0,0] neg_hi:[1,0,0]
	v_cvt_pk_bf16_f32 v46, v46, v47
	v_cndmask_b32_e64 v57, 0, 1.0, vcc
	v_cmp_eq_u32_e32 vcc, v106, v113
	s_nop 1
	v_cndmask_b32_e64 v56, 0, 1.0, vcc
	v_pk_fma_f32 v[48:49], v[54:55], v[48:49], v[56:57] op_sel_hi:[0,1,1] neg_lo:[1,0,0] neg_hi:[1,0,0]
	v_cvt_pk_bf16_f32 v47, v48, v49
	ds_write_b64 v186, v[46:47] offset:3808
	ds_read_b128 v[46:49], v1
	s_waitcnt lgkmcnt(0)
	ds_write_b128 v184, v[46:49]
	ds_read_b128 v[46:49], v1 offset:64
	s_waitcnt lgkmcnt(0)
	ds_write_b128 v184, v[46:49] offset:1024
	ds_read_b128 v[46:49], v1 offset:128
	s_waitcnt lgkmcnt(0)
	ds_write_b128 v184, v[46:49] offset:2048
	ds_read_b128 v[46:49], v1 offset:192
	s_waitcnt lgkmcnt(0)
	ds_write_b128 v184, v[46:49] offset:3072
	s_lshl_b32 s30, s25, 2
	s_mov_b32 s31, s21
	v_lshl_add_u64 v[46:47], v[126:127], 0, s[30:31]
	v_lshl_add_u64 v[48:49], v[128:129], 0, s[30:31]
	v_lshl_add_u64 v[54:55], v[134:135], 0, s[30:31]
	v_lshl_add_u64 v[56:57], v[136:137], 0, s[30:31]
	v_lshl_add_u64 v[62:63], v[138:139], 0, s[30:31]
	v_lshl_add_u64 v[64:65], v[140:141], 0, s[30:31]
	v_lshl_add_u64 v[98:99], v[142:143], 0, s[30:31]
	v_lshl_add_u64 v[100:101], v[144:145], 0, s[30:31]
	global_load_dwordx4 v[90:93], v[46:47], off nt
	global_load_dwordx4 v[82:85], v[48:49], off nt
	global_load_dwordx4 v[78:81], v[54:55], off nt
	global_load_dwordx4 v[70:73], v[56:57], off nt
	global_load_dwordx4 v[66:69], v[62:63], off nt
	s_nop 0
	global_load_dwordx4 v[62:65], v[64:65], off nt
	s_nop 0
	global_load_dwordx4 v[54:57], v[98:99], off nt
	global_load_dwordx4 v[46:49], v[100:101], off nt
	v_mov_b32_e32 v99, v189
	s_waitcnt vmcnt(23)
	s_waitcnt vmcnt(22)
	s_waitcnt vmcnt(21)
	s_waitcnt vmcnt(20)
	s_waitcnt vmcnt(19)
	s_waitcnt vmcnt(18)
	s_waitcnt vmcnt(17)
	s_waitcnt vmcnt(16)
	ds_read_b32 v98, v187 offset:192
	v_add_u32_e32 v102, 1, v99
	v_cmp_eq_u32_e32 vcc, v99, v103
	v_add_u32_e32 v104, 3, v99
	v_add_u32_e32 v105, 2, v99
	v_cndmask_b32_e64 v100, 0, 1.0, vcc
	v_cmp_eq_u32_e32 vcc, v102, v103
	s_nop 1
	v_cndmask_b32_e64 v101, 0, 1.0, vcc
	v_cmp_eq_u32_e32 vcc, v104, v103
	s_waitcnt lgkmcnt(0)
	v_pk_fma_f32 v[94:95], v[98:99], v[94:95], v[100:101] op_sel_hi:[0,1,1] neg_lo:[1,0,0] neg_hi:[1,0,0]
	v_cvt_pk_bf16_f32 v94, v94, v95
	v_cndmask_b32_e64 v101, 0, 1.0, vcc
	v_cmp_eq_u32_e32 vcc, v105, v103
	s_nop 1
	v_cndmask_b32_e64 v100, 0, 1.0, vcc
	v_pk_fma_f32 v[96:97], v[98:99], v[96:97], v[100:101] op_sel_hi:[0,1,1] neg_lo:[1,0,0] neg_hi:[1,0,0]
	v_cvt_pk_bf16_f32 v95, v96, v97
	ds_write_b64 v186, v[94:95]
	ds_read_b32 v94, v187 offset:200
	v_cmp_eq_u32_e32 vcc, v99, v107
	s_nop 1
	v_cndmask_b32_e64 v96, 0, 1.0, vcc
	v_cmp_eq_u32_e32 vcc, v102, v107
	s_nop 1
	v_cndmask_b32_e64 v97, 0, 1.0, vcc
	v_cmp_eq_u32_e32 vcc, v104, v107
	s_waitcnt lgkmcnt(0)
	v_pk_fma_f32 v[86:87], v[94:95], v[86:87], v[96:97] op_sel_hi:[0,1,1] neg_lo:[1,0,0] neg_hi:[1,0,0]
	v_cvt_pk_bf16_f32 v86, v86, v87
	v_cndmask_b32_e64 v97, 0, 1.0, vcc
	v_cmp_eq_u32_e32 vcc, v105, v107
	s_nop 1
	v_cndmask_b32_e64 v96, 0, 1.0, vcc
	v_pk_fma_f32 v[88:89], v[94:95], v[88:89], v[96:97] op_sel_hi:[0,1,1] neg_lo:[1,0,0] neg_hi:[1,0,0]
	v_cvt_pk_bf16_f32 v87, v88, v89
	ds_write_b64 v186, v[86:87] offset:544
	ds_read_b32 v86, v187 offset:208
	v_cmp_eq_u32_e32 vcc, v99, v108
	s_nop 1
	v_cndmask_b32_e64 v88, 0, 1.0, vcc
	v_cmp_eq_u32_e32 vcc, v102, v108
	s_nop 1
	v_cndmask_b32_e64 v89, 0, 1.0, vcc
	v_cmp_eq_u32_e32 vcc, v104, v108
	s_waitcnt lgkmcnt(0)
	v_pk_fma_f32 v[74:75], v[86:87], v[74:75], v[88:89] op_sel_hi:[0,1,1] neg_lo:[1,0,0] neg_hi:[1,0,0]
	v_cvt_pk_bf16_f32 v74, v74, v75
	v_cndmask_b32_e64 v89, 0, 1.0, vcc
	v_cmp_eq_u32_e32 vcc, v105, v108
	s_nop 1
	v_cndmask_b32_e64 v88, 0, 1.0, vcc
	v_pk_fma_f32 v[76:77], v[86:87], v[76:77], v[88:89] op_sel_hi:[0,1,1] neg_lo:[1,0,0] neg_hi:[1,0,0]
	v_cvt_pk_bf16_f32 v75, v76, v77
	ds_write_b64 v186, v[74:75] offset:1088
	ds_read_b32 v74, v187 offset:216
	v_cmp_eq_u32_e32 vcc, v99, v109
	s_nop 1
	v_cndmask_b32_e64 v76, 0, 1.0, vcc
	v_cmp_eq_u32_e32 vcc, v102, v109
	s_nop 1
	v_cndmask_b32_e64 v77, 0, 1.0, vcc
	v_cmp_eq_u32_e32 vcc, v104, v109
	s_waitcnt lgkmcnt(0)
	v_pk_fma_f32 v[58:59], v[74:75], v[58:59], v[76:77] op_sel_hi:[0,1,1] neg_lo:[1,0,0] neg_hi:[1,0,0]
	v_cvt_pk_bf16_f32 v58, v58, v59
	v_cndmask_b32_e64 v77, 0, 1.0, vcc
	v_cmp_eq_u32_e32 vcc, v105, v109
	s_nop 1
	v_cndmask_b32_e64 v76, 0, 1.0, vcc
	v_pk_fma_f32 v[60:61], v[74:75], v[60:61], v[76:77] op_sel_hi:[0,1,1] neg_lo:[1,0,0] neg_hi:[1,0,0]
	v_cvt_pk_bf16_f32 v59, v60, v61
	ds_write_b64 v186, v[58:59] offset:1632
	ds_read_b32 v58, v187 offset:224
	v_cmp_eq_u32_e32 vcc, v99, v110
	s_nop 1
	v_cndmask_b32_e64 v60, 0, 1.0, vcc
	v_cmp_eq_u32_e32 vcc, v102, v110
	s_nop 1
	v_cndmask_b32_e64 v61, 0, 1.0, vcc
	v_cmp_eq_u32_e32 vcc, v104, v110
	s_waitcnt lgkmcnt(0)
	v_pk_fma_f32 v[50:51], v[58:59], v[50:51], v[60:61] op_sel_hi:[0,1,1] neg_lo:[1,0,0] neg_hi:[1,0,0]
	v_cvt_pk_bf16_f32 v50, v50, v51
	v_cndmask_b32_e64 v61, 0, 1.0, vcc
	v_cmp_eq_u32_e32 vcc, v105, v110
	s_nop 1
	v_cndmask_b32_e64 v60, 0, 1.0, vcc
	v_pk_fma_f32 v[52:53], v[58:59], v[52:53], v[60:61] op_sel_hi:[0,1,1] neg_lo:[1,0,0] neg_hi:[1,0,0]
	v_cvt_pk_bf16_f32 v51, v52, v53
	ds_write_b64 v186, v[50:51] offset:2176
	ds_read_b32 v50, v187 offset:232
	v_cmp_eq_u32_e32 vcc, v99, v111
	s_nop 1
	v_cndmask_b32_e64 v52, 0, 1.0, vcc
	v_cmp_eq_u32_e32 vcc, v102, v111
	s_nop 1
	v_cndmask_b32_e64 v53, 0, 1.0, vcc
	v_cmp_eq_u32_e32 vcc, v104, v111
	s_waitcnt lgkmcnt(0)
	v_pk_fma_f32 v[42:43], v[50:51], v[42:43], v[52:53] op_sel_hi:[0,1,1] neg_lo:[1,0,0] neg_hi:[1,0,0]
	v_cvt_pk_bf16_f32 v42, v42, v43
	v_cndmask_b32_e64 v53, 0, 1.0, vcc
	v_cmp_eq_u32_e32 vcc, v105, v111
	s_nop 1
	v_cndmask_b32_e64 v52, 0, 1.0, vcc
	v_pk_fma_f32 v[44:45], v[50:51], v[44:45], v[52:53] op_sel_hi:[0,1,1] neg_lo:[1,0,0] neg_hi:[1,0,0]
	v_cvt_pk_bf16_f32 v43, v44, v45
	ds_write_b64 v186, v[42:43] offset:2720
	ds_read_b32 v42, v187 offset:240
	v_cmp_eq_u32_e32 vcc, v99, v112
	s_nop 1
	v_cndmask_b32_e64 v44, 0, 1.0, vcc
	v_cmp_eq_u32_e32 vcc, v102, v112
	s_nop 1
	v_cndmask_b32_e64 v45, 0, 1.0, vcc
	v_cmp_eq_u32_e32 vcc, v104, v112
	s_waitcnt lgkmcnt(0)
	v_pk_fma_f32 v[38:39], v[42:43], v[38:39], v[44:45] op_sel_hi:[0,1,1] neg_lo:[1,0,0] neg_hi:[1,0,0]
	v_cvt_pk_bf16_f32 v38, v38, v39
	v_cndmask_b32_e64 v45, 0, 1.0, vcc
	v_cmp_eq_u32_e32 vcc, v105, v112
	s_nop 1
	v_cndmask_b32_e64 v44, 0, 1.0, vcc
	v_pk_fma_f32 v[40:41], v[42:43], v[40:41], v[44:45] op_sel_hi:[0,1,1] neg_lo:[1,0,0] neg_hi:[1,0,0]
	v_cvt_pk_bf16_f32 v39, v40, v41
	ds_write_b64 v186, v[38:39] offset:3264
	ds_read_b32 v38, v187 offset:248
	v_cmp_eq_u32_e32 vcc, v99, v113
	s_nop 1
	v_cndmask_b32_e64 v40, 0, 1.0, vcc
	v_cmp_eq_u32_e32 vcc, v102, v113
	s_nop 1
	v_cndmask_b32_e64 v41, 0, 1.0, vcc
	v_cmp_eq_u32_e32 vcc, v104, v113
	s_waitcnt lgkmcnt(0)
	v_pk_fma_f32 v[34:35], v[38:39], v[34:35], v[40:41] op_sel_hi:[0,1,1] neg_lo:[1,0,0] neg_hi:[1,0,0]
	v_cvt_pk_bf16_f32 v34, v34, v35
	v_cndmask_b32_e64 v41, 0, 1.0, vcc
	v_cmp_eq_u32_e32 vcc, v105, v113
	s_nop 1
	v_cndmask_b32_e64 v40, 0, 1.0, vcc
	v_pk_fma_f32 v[36:37], v[38:39], v[36:37], v[40:41] op_sel_hi:[0,1,1] neg_lo:[1,0,0] neg_hi:[1,0,0]
	v_cvt_pk_bf16_f32 v35, v36, v37
	ds_write_b64 v186, v[34:35] offset:3808
	ds_read_b128 v[34:37], v1
	s_waitcnt lgkmcnt(0)
	ds_write_b128 v184, v[34:37] offset:4096
	ds_read_b128 v[34:37], v1 offset:64
	s_waitcnt lgkmcnt(0)
	ds_write_b128 v184, v[34:37] offset:5120
	ds_read_b128 v[34:37], v1 offset:128
	s_waitcnt lgkmcnt(0)
	ds_write_b128 v184, v[34:37] offset:6144
	ds_read_b128 v[34:37], v1 offset:192
	s_waitcnt lgkmcnt(0)
	ds_write_b128 v184, v[34:37] offset:7168
	s_lshl_b32 s28, s24, 2
	s_mov_b32 s29, s21
	v_lshl_add_u64 v[34:35], v[126:127], 0, s[28:29]
	v_lshl_add_u64 v[36:37], v[128:129], 0, s[28:29]
	v_lshl_add_u64 v[38:39], v[134:135], 0, s[28:29]
	v_lshl_add_u64 v[40:41], v[136:137], 0, s[28:29]
	v_lshl_add_u64 v[42:43], v[138:139], 0, s[28:29]
	v_lshl_add_u64 v[44:45], v[140:141], 0, s[28:29]
	v_lshl_add_u64 v[50:51], v[142:143], 0, s[28:29]
	v_lshl_add_u64 v[52:53], v[144:145], 0, s[28:29]
	global_load_dwordx4 v[122:125], v[34:35], off nt
	global_load_dwordx4 v[114:117], v[36:37], off nt
	global_load_dwordx4 v[106:109], v[38:39], off nt
	global_load_dwordx4 v[86:89], v[40:41], off nt
	global_load_dwordx4 v[74:77], v[42:43], off nt
	s_nop 0
	global_load_dwordx4 v[42:45], v[44:45], off nt
	s_nop 0
	global_load_dwordx4 v[38:41], v[50:51], off nt
	global_load_dwordx4 v[34:37], v[52:53], off nt
	v_mov_b32_e32 v50, v188
	s_waitcnt vmcnt(23)
	s_waitcnt vmcnt(22)
	s_waitcnt vmcnt(21)
	s_waitcnt vmcnt(20)
	s_waitcnt vmcnt(19)
	s_waitcnt vmcnt(18)
	s_waitcnt vmcnt(17)
	s_waitcnt vmcnt(16)
	ds_read_b32 v50, v187 offset:192
	s_waitcnt lgkmcnt(0)
	v_pk_fma_f32 v[30:31], v[50:51], v[30:31], 0 op_sel_hi:[0,1,0] neg_lo:[1,0,0] neg_hi:[1,0,0]
	v_pk_fma_f32 v[32:33], v[50:51], v[32:33], 0 op_sel_hi:[0,1,0] neg_lo:[1,0,0] neg_hi:[1,0,0]
	v_cvt_pk_bf16_f32 v30, v30, v31
	v_cvt_pk_bf16_f32 v31, v32, v33
	ds_write_b64 v186, v[30:31]
	ds_read_b32 v30, v187 offset:200
	s_waitcnt lgkmcnt(0)
	v_pk_fma_f32 v[26:27], v[30:31], v[26:27], 0 op_sel_hi:[0,1,0] neg_lo:[1,0,0] neg_hi:[1,0,0]
	v_pk_fma_f32 v[28:29], v[30:31], v[28:29], 0 op_sel_hi:[0,1,0] neg_lo:[1,0,0] neg_hi:[1,0,0]
	v_cvt_pk_bf16_f32 v26, v26, v27
	v_cvt_pk_bf16_f32 v27, v28, v29
	ds_write_b64 v186, v[26:27] offset:544
	ds_read_b32 v26, v187 offset:208
	s_waitcnt lgkmcnt(0)
	v_pk_fma_f32 v[22:23], v[26:27], v[22:23], 0 op_sel_hi:[0,1,0] neg_lo:[1,0,0] neg_hi:[1,0,0]
	v_pk_fma_f32 v[24:25], v[26:27], v[24:25], 0 op_sel_hi:[0,1,0] neg_lo:[1,0,0] neg_hi:[1,0,0]
	v_cvt_pk_bf16_f32 v22, v22, v23
	v_cvt_pk_bf16_f32 v23, v24, v25
	ds_write_b64 v186, v[22:23] offset:1088
	ds_read_b32 v22, v187 offset:216
	s_waitcnt lgkmcnt(0)
	v_pk_fma_f32 v[18:19], v[22:23], v[18:19], 0 op_sel_hi:[0,1,0] neg_lo:[1,0,0] neg_hi:[1,0,0]
	v_pk_fma_f32 v[20:21], v[22:23], v[20:21], 0 op_sel_hi:[0,1,0] neg_lo:[1,0,0] neg_hi:[1,0,0]
	v_cvt_pk_bf16_f32 v18, v18, v19
	v_cvt_pk_bf16_f32 v19, v20, v21
	ds_write_b64 v186, v[18:19] offset:1632
	ds_read_b32 v18, v187 offset:224
	s_waitcnt lgkmcnt(0)
	v_pk_fma_f32 v[14:15], v[18:19], v[14:15], 0 op_sel_hi:[0,1,0] neg_lo:[1,0,0] neg_hi:[1,0,0]
	v_pk_fma_f32 v[16:17], v[18:19], v[16:17], 0 op_sel_hi:[0,1,0] neg_lo:[1,0,0] neg_hi:[1,0,0]
	v_cvt_pk_bf16_f32 v14, v14, v15
	v_cvt_pk_bf16_f32 v15, v16, v17
	ds_write_b64 v186, v[14:15] offset:2176
	ds_read_b32 v14, v187 offset:232
	s_waitcnt lgkmcnt(0)
	v_pk_fma_f32 v[10:11], v[14:15], v[10:11], 0 op_sel_hi:[0,1,0] neg_lo:[1,0,0] neg_hi:[1,0,0]
	v_pk_fma_f32 v[12:13], v[14:15], v[12:13], 0 op_sel_hi:[0,1,0] neg_lo:[1,0,0] neg_hi:[1,0,0]
	v_cvt_pk_bf16_f32 v10, v10, v11
	v_cvt_pk_bf16_f32 v11, v12, v13
	ds_write_b64 v186, v[10:11] offset:2720
	ds_read_b32 v10, v187 offset:240
	s_waitcnt lgkmcnt(0)
	v_pk_fma_f32 v[6:7], v[10:11], v[6:7], 0 op_sel_hi:[0,1,0] neg_lo:[1,0,0] neg_hi:[1,0,0]
	v_pk_fma_f32 v[8:9], v[10:11], v[8:9], 0 op_sel_hi:[0,1,0] neg_lo:[1,0,0] neg_hi:[1,0,0]
	v_cvt_pk_bf16_f32 v6, v6, v7
	v_cvt_pk_bf16_f32 v7, v8, v9
	ds_write_b64 v186, v[6:7] offset:3264
	ds_read_b32 v6, v187 offset:248
	s_waitcnt lgkmcnt(0)
	v_pk_fma_f32 v[2:3], v[6:7], v[2:3], 0 op_sel_hi:[0,1,0] neg_lo:[1,0,0] neg_hi:[1,0,0]
	v_pk_fma_f32 v[4:5], v[6:7], v[4:5], 0 op_sel_hi:[0,1,0] neg_lo:[1,0,0] neg_hi:[1,0,0]
	v_cvt_pk_bf16_f32 v2, v2, v3
	v_cvt_pk_bf16_f32 v3, v4, v5
	ds_write_b64 v186, v[2:3] offset:3808
	ds_read_b128 v[2:5], v1
	s_waitcnt lgkmcnt(0)
	ds_write_b128 v184, v[2:5] offset:8192
	ds_read_b128 v[2:5], v1 offset:64
	s_waitcnt lgkmcnt(0)
	ds_write_b128 v184, v[2:5] offset:9216
	ds_read_b128 v[2:5], v1 offset:128
	s_waitcnt lgkmcnt(0)
	ds_write_b128 v184, v[2:5] offset:10240
	ds_read_b128 v[2:5], v1 offset:192
	s_waitcnt lgkmcnt(0)
	ds_write_b128 v184, v[2:5] offset:11264
	s_lshl_b32 s26, s23, 2
	s_mov_b32 s27, s21
	v_lshl_add_u64 v[2:3], v[126:127], 0, s[26:27]
	v_lshl_add_u64 v[4:5], v[128:129], 0, s[26:27]
	v_lshl_add_u64 v[6:7], v[134:135], 0, s[26:27]
	v_lshl_add_u64 v[8:9], v[136:137], 0, s[26:27]
	v_lshl_add_u64 v[10:11], v[138:139], 0, s[26:27]
	v_lshl_add_u64 v[12:13], v[140:141], 0, s[26:27]
	v_lshl_add_u64 v[14:15], v[142:143], 0, s[26:27]
	v_lshl_add_u64 v[16:17], v[144:145], 0, s[26:27]
	global_load_dwordx4 v[118:121], v[2:3], off nt
	global_load_dwordx4 v[110:113], v[4:5], off nt
	global_load_dwordx4 v[102:105], v[6:7], off nt
	global_load_dwordx4 v[98:101], v[8:9], off nt
	global_load_dwordx4 v[58:61], v[10:11], off nt
	global_load_dwordx4 v[50:53], v[12:13], off nt
	global_load_dwordx4 v[30:33], v[14:15], off nt
	global_load_dwordx4 v[22:25], v[16:17], off nt
	v_mov_b32_e32 v2, v198
	s_waitcnt vmcnt(23)
	s_waitcnt vmcnt(22)
	s_waitcnt vmcnt(21)
	s_waitcnt vmcnt(20)
	s_waitcnt vmcnt(19)
	s_waitcnt vmcnt(18)
	s_waitcnt vmcnt(17)
	s_waitcnt vmcnt(16)
	ds_read_b32 v2, v187 offset:192
	s_waitcnt lgkmcnt(0)
	v_pk_fma_f32 v[4:5], v[2:3], v[90:91], 0 op_sel_hi:[0,1,0] neg_lo:[1,0,0] neg_hi:[1,0,0]
	v_pk_fma_f32 v[2:3], v[2:3], v[92:93], 0 op_sel_hi:[0,1,0] neg_lo:[1,0,0] neg_hi:[1,0,0]
	v_cvt_pk_bf16_f32 v4, v4, v5
	v_cvt_pk_bf16_f32 v5, v2, v3
	ds_write_b64 v186, v[4:5]
	ds_read_b32 v2, v187 offset:200
	s_waitcnt lgkmcnt(0)
	v_pk_fma_f32 v[4:5], v[2:3], v[82:83], 0 op_sel_hi:[0,1,0] neg_lo:[1,0,0] neg_hi:[1,0,0]
	v_pk_fma_f32 v[2:3], v[2:3], v[84:85], 0 op_sel_hi:[0,1,0] neg_lo:[1,0,0] neg_hi:[1,0,0]
	v_cvt_pk_bf16_f32 v4, v4, v5
	v_cvt_pk_bf16_f32 v5, v2, v3
	ds_write_b64 v186, v[4:5] offset:544
	ds_read_b32 v2, v187 offset:208
	s_waitcnt lgkmcnt(0)
	v_pk_fma_f32 v[4:5], v[2:3], v[78:79], 0 op_sel_hi:[0,1,0] neg_lo:[1,0,0] neg_hi:[1,0,0]
	v_pk_fma_f32 v[2:3], v[2:3], v[80:81], 0 op_sel_hi:[0,1,0] neg_lo:[1,0,0] neg_hi:[1,0,0]
	v_cvt_pk_bf16_f32 v4, v4, v5
	v_cvt_pk_bf16_f32 v5, v2, v3
	ds_write_b64 v186, v[4:5] offset:1088
	ds_read_b32 v2, v187 offset:216
	s_waitcnt lgkmcnt(0)
	v_pk_fma_f32 v[4:5], v[2:3], v[70:71], 0 op_sel_hi:[0,1,0] neg_lo:[1,0,0] neg_hi:[1,0,0]
	v_pk_fma_f32 v[2:3], v[2:3], v[72:73], 0 op_sel_hi:[0,1,0] neg_lo:[1,0,0] neg_hi:[1,0,0]
	v_cvt_pk_bf16_f32 v4, v4, v5
	v_cvt_pk_bf16_f32 v5, v2, v3
	ds_write_b64 v186, v[4:5] offset:1632
	ds_read_b32 v2, v187 offset:224
	s_waitcnt lgkmcnt(0)
	v_pk_fma_f32 v[4:5], v[2:3], v[66:67], 0 op_sel_hi:[0,1,0] neg_lo:[1,0,0] neg_hi:[1,0,0]
	v_pk_fma_f32 v[2:3], v[2:3], v[68:69], 0 op_sel_hi:[0,1,0] neg_lo:[1,0,0] neg_hi:[1,0,0]
	v_cvt_pk_bf16_f32 v4, v4, v5
	v_cvt_pk_bf16_f32 v5, v2, v3
	ds_write_b64 v186, v[4:5] offset:2176
	ds_read_b32 v2, v187 offset:232
	s_waitcnt lgkmcnt(0)
	v_pk_fma_f32 v[4:5], v[2:3], v[62:63], 0 op_sel_hi:[0,1,0] neg_lo:[1,0,0] neg_hi:[1,0,0]
	v_pk_fma_f32 v[2:3], v[2:3], v[64:65], 0 op_sel_hi:[0,1,0] neg_lo:[1,0,0] neg_hi:[1,0,0]
	v_cvt_pk_bf16_f32 v4, v4, v5
	v_cvt_pk_bf16_f32 v5, v2, v3
	ds_write_b64 v186, v[4:5] offset:2720
	ds_read_b32 v2, v187 offset:240
	s_waitcnt lgkmcnt(0)
	v_pk_fma_f32 v[4:5], v[2:3], v[54:55], 0 op_sel_hi:[0,1,0] neg_lo:[1,0,0] neg_hi:[1,0,0]
	v_pk_fma_f32 v[2:3], v[2:3], v[56:57], 0 op_sel_hi:[0,1,0] neg_lo:[1,0,0] neg_hi:[1,0,0]
	v_cvt_pk_bf16_f32 v4, v4, v5
	v_cvt_pk_bf16_f32 v5, v2, v3
	ds_write_b64 v186, v[4:5] offset:3264
	ds_read_b32 v2, v187 offset:248
	s_waitcnt lgkmcnt(0)
	v_pk_fma_f32 v[4:5], v[2:3], v[46:47], 0 op_sel_hi:[0,1,0] neg_lo:[1,0,0] neg_hi:[1,0,0]
	v_pk_fma_f32 v[2:3], v[2:3], v[48:49], 0 op_sel_hi:[0,1,0] neg_lo:[1,0,0] neg_hi:[1,0,0]
	v_cvt_pk_bf16_f32 v4, v4, v5
	v_cvt_pk_bf16_f32 v5, v2, v3
	ds_write_b64 v186, v[4:5] offset:3808
	ds_read_b128 v[2:5], v1
	s_waitcnt lgkmcnt(0)
	ds_write_b128 v184, v[2:5] offset:12288
	ds_read_b128 v[2:5], v1 offset:64
	s_waitcnt lgkmcnt(0)
	ds_write_b128 v184, v[2:5] offset:13312
	ds_read_b128 v[2:5], v1 offset:128
	s_waitcnt lgkmcnt(0)
	ds_write_b128 v184, v[2:5] offset:14336
	ds_read_b128 v[2:5], v1 offset:192
	s_waitcnt lgkmcnt(0)
	ds_write_b128 v184, v[2:5] offset:15360
	s_lshl_b32 s24, s22, 2
	s_mov_b32 s25, s21
	v_lshl_add_u64 v[2:3], v[126:127], 0, s[24:25]
	v_lshl_add_u64 v[6:7], v[134:135], 0, s[24:25]
	v_lshl_add_u64 v[8:9], v[136:137], 0, s[24:25]
	v_lshl_add_u64 v[14:15], v[142:143], 0, s[24:25]
	v_lshl_add_u64 v[4:5], v[128:129], 0, s[24:25]
	v_lshl_add_u64 v[10:11], v[138:139], 0, s[24:25]
	v_lshl_add_u64 v[12:13], v[140:141], 0, s[24:25]
	v_lshl_add_u64 v[18:19], v[144:145], 0, s[24:25]
	global_load_dwordx4 v[94:97], v[2:3], off nt
	global_load_dwordx4 v[90:93], v[4:5], off nt
	global_load_dwordx4 v[82:85], v[6:7], off nt
	global_load_dwordx4 v[70:73], v[8:9], off nt
	global_load_dwordx4 v[54:57], v[10:11], off nt
	global_load_dwordx4 v[26:29], v[12:13], off nt
	s_nop 0
	global_load_dwordx4 v[14:17], v[14:15], off nt
	s_nop 0
	global_load_dwordx4 v[6:9], v[18:19], off nt
	v_mov_b32_e32 v2, v197
	s_waitcnt vmcnt(23)
	s_waitcnt vmcnt(22)
	s_waitcnt vmcnt(21)
	s_waitcnt vmcnt(20)
	s_waitcnt vmcnt(19)
	s_waitcnt vmcnt(18)
	s_waitcnt vmcnt(17)
	s_waitcnt vmcnt(16)
	ds_read_b32 v2, v187 offset:192
	s_waitcnt lgkmcnt(0)
	v_pk_fma_f32 v[4:5], v[2:3], v[122:123], 0 op_sel_hi:[0,1,0] neg_lo:[1,0,0] neg_hi:[1,0,0]
	v_pk_fma_f32 v[2:3], v[2:3], v[124:125], 0 op_sel_hi:[0,1,0] neg_lo:[1,0,0] neg_hi:[1,0,0]
	v_cvt_pk_bf16_f32 v4, v4, v5
	v_cvt_pk_bf16_f32 v5, v2, v3
	ds_write_b64 v186, v[4:5]
	ds_read_b32 v2, v187 offset:200
	s_waitcnt lgkmcnt(0)
	v_pk_fma_f32 v[4:5], v[2:3], v[114:115], 0 op_sel_hi:[0,1,0] neg_lo:[1,0,0] neg_hi:[1,0,0]
	v_pk_fma_f32 v[2:3], v[2:3], v[116:117], 0 op_sel_hi:[0,1,0] neg_lo:[1,0,0] neg_hi:[1,0,0]
	v_cvt_pk_bf16_f32 v4, v4, v5
	v_cvt_pk_bf16_f32 v5, v2, v3
	ds_write_b64 v186, v[4:5] offset:544
	ds_read_b32 v2, v187 offset:208
	s_waitcnt lgkmcnt(0)
	v_pk_fma_f32 v[4:5], v[2:3], v[106:107], 0 op_sel_hi:[0,1,0] neg_lo:[1,0,0] neg_hi:[1,0,0]
	v_pk_fma_f32 v[2:3], v[2:3], v[108:109], 0 op_sel_hi:[0,1,0] neg_lo:[1,0,0] neg_hi:[1,0,0]
	v_cvt_pk_bf16_f32 v4, v4, v5
	v_cvt_pk_bf16_f32 v5, v2, v3
	ds_write_b64 v186, v[4:5] offset:1088
	ds_read_b32 v2, v187 offset:216
	s_waitcnt lgkmcnt(0)
	v_pk_fma_f32 v[4:5], v[2:3], v[86:87], 0 op_sel_hi:[0,1,0] neg_lo:[1,0,0] neg_hi:[1,0,0]
	v_pk_fma_f32 v[2:3], v[2:3], v[88:89], 0 op_sel_hi:[0,1,0] neg_lo:[1,0,0] neg_hi:[1,0,0]
	v_cvt_pk_bf16_f32 v4, v4, v5
	v_cvt_pk_bf16_f32 v5, v2, v3
	ds_write_b64 v186, v[4:5] offset:1632
	ds_read_b32 v2, v187 offset:224
	s_waitcnt lgkmcnt(0)
	v_pk_fma_f32 v[4:5], v[2:3], v[74:75], 0 op_sel_hi:[0,1,0] neg_lo:[1,0,0] neg_hi:[1,0,0]
	v_pk_fma_f32 v[2:3], v[2:3], v[76:77], 0 op_sel_hi:[0,1,0] neg_lo:[1,0,0] neg_hi:[1,0,0]
	v_cvt_pk_bf16_f32 v4, v4, v5
	v_cvt_pk_bf16_f32 v5, v2, v3
	ds_write_b64 v186, v[4:5] offset:2176
	ds_read_b32 v2, v187 offset:232
	s_waitcnt lgkmcnt(0)
	v_pk_fma_f32 v[4:5], v[2:3], v[42:43], 0 op_sel_hi:[0,1,0] neg_lo:[1,0,0] neg_hi:[1,0,0]
	v_pk_fma_f32 v[2:3], v[2:3], v[44:45], 0 op_sel_hi:[0,1,0] neg_lo:[1,0,0] neg_hi:[1,0,0]
	v_cvt_pk_bf16_f32 v4, v4, v5
	v_cvt_pk_bf16_f32 v5, v2, v3
	ds_write_b64 v186, v[4:5] offset:2720
	ds_read_b32 v2, v187 offset:240
	s_waitcnt lgkmcnt(0)
	v_pk_fma_f32 v[4:5], v[2:3], v[38:39], 0 op_sel_hi:[0,1,0] neg_lo:[1,0,0] neg_hi:[1,0,0]
	v_pk_fma_f32 v[2:3], v[2:3], v[40:41], 0 op_sel_hi:[0,1,0] neg_lo:[1,0,0] neg_hi:[1,0,0]
	v_cvt_pk_bf16_f32 v4, v4, v5
	v_cvt_pk_bf16_f32 v5, v2, v3
	ds_write_b64 v186, v[4:5] offset:3264
	ds_read_b32 v2, v187 offset:248
	s_waitcnt lgkmcnt(0)
	v_pk_fma_f32 v[4:5], v[2:3], v[34:35], 0 op_sel_hi:[0,1,0] neg_lo:[1,0,0] neg_hi:[1,0,0]
	v_pk_fma_f32 v[2:3], v[2:3], v[36:37], 0 op_sel_hi:[0,1,0] neg_lo:[1,0,0] neg_hi:[1,0,0]
	v_cvt_pk_bf16_f32 v4, v4, v5
	v_cvt_pk_bf16_f32 v5, v2, v3
	ds_write_b64 v186, v[4:5] offset:3808
	ds_read_b128 v[2:5], v1
	s_waitcnt lgkmcnt(0)
	ds_write_b128 v184, v[2:5] offset:16384
	ds_read_b128 v[2:5], v1 offset:64
	s_waitcnt lgkmcnt(0)
	ds_write_b128 v184, v[2:5] offset:17408
	ds_read_b128 v[2:5], v1 offset:128
	s_waitcnt lgkmcnt(0)
	ds_write_b128 v184, v[2:5] offset:18432
	ds_read_b128 v[2:5], v1 offset:192
	s_waitcnt lgkmcnt(0)
	ds_write_b128 v184, v[2:5] offset:19456
	s_lshl_b32 s22, s7, 2
	s_mov_b32 s23, s21
	v_lshl_add_u64 v[2:3], v[126:127], 0, s[22:23]
	v_lshl_add_u64 v[4:5], v[128:129], 0, s[22:23]
	v_lshl_add_u64 v[10:11], v[134:135], 0, s[22:23]
	v_lshl_add_u64 v[12:13], v[136:137], 0, s[22:23]
	v_lshl_add_u64 v[34:35], v[138:139], 0, s[22:23]
	v_lshl_add_u64 v[36:37], v[140:141], 0, s[22:23]
	v_lshl_add_u64 v[46:47], v[142:143], 0, s[22:23]
	v_lshl_add_u64 v[48:49], v[144:145], 0, s[22:23]
	global_load_dwordx4 v[86:89], v[2:3], off nt
	global_load_dwordx4 v[78:81], v[4:5], off nt
	global_load_dwordx4 v[66:69], v[10:11], off nt
	global_load_dwordx4 v[42:45], v[12:13], off nt
	global_load_dwordx4 v[38:41], v[34:35], off nt
	global_load_dwordx4 v[18:21], v[36:37], off nt
	s_nop 0
	global_load_dwordx4 v[10:13], v[46:47], off nt
	global_load_dwordx4 v[2:5], v[48:49], off nt
	v_mov_b32_e32 v34, v196
	s_waitcnt vmcnt(23)
	s_waitcnt vmcnt(22)
	s_waitcnt vmcnt(21)
	s_waitcnt vmcnt(20)
	s_waitcnt vmcnt(19)
	s_waitcnt vmcnt(18)
	s_waitcnt vmcnt(17)
	s_waitcnt vmcnt(16)
	ds_read_b32 v34, v187 offset:192
	s_waitcnt lgkmcnt(0)
	v_pk_fma_f32 v[36:37], v[34:35], v[118:119], 0 op_sel_hi:[0,1,0] neg_lo:[1,0,0] neg_hi:[1,0,0]
	v_pk_fma_f32 v[34:35], v[34:35], v[120:121], 0 op_sel_hi:[0,1,0] neg_lo:[1,0,0] neg_hi:[1,0,0]
	v_cvt_pk_bf16_f32 v36, v36, v37
	v_cvt_pk_bf16_f32 v37, v34, v35
	ds_write_b64 v186, v[36:37]
	ds_read_b32 v34, v187 offset:200
	s_waitcnt lgkmcnt(0)
	v_pk_fma_f32 v[36:37], v[34:35], v[110:111], 0 op_sel_hi:[0,1,0] neg_lo:[1,0,0] neg_hi:[1,0,0]
	v_pk_fma_f32 v[34:35], v[34:35], v[112:113], 0 op_sel_hi:[0,1,0] neg_lo:[1,0,0] neg_hi:[1,0,0]
	v_cvt_pk_bf16_f32 v36, v36, v37
	v_cvt_pk_bf16_f32 v37, v34, v35
	ds_write_b64 v186, v[36:37] offset:544
	ds_read_b32 v34, v187 offset:208
	s_waitcnt lgkmcnt(0)
	v_pk_fma_f32 v[36:37], v[34:35], v[102:103], 0 op_sel_hi:[0,1,0] neg_lo:[1,0,0] neg_hi:[1,0,0]
	v_pk_fma_f32 v[34:35], v[34:35], v[104:105], 0 op_sel_hi:[0,1,0] neg_lo:[1,0,0] neg_hi:[1,0,0]
	v_cvt_pk_bf16_f32 v36, v36, v37
	v_cvt_pk_bf16_f32 v37, v34, v35
	ds_write_b64 v186, v[36:37] offset:1088
	ds_read_b32 v34, v187 offset:216
	s_waitcnt lgkmcnt(0)
	v_pk_fma_f32 v[36:37], v[34:35], v[98:99], 0 op_sel_hi:[0,1,0] neg_lo:[1,0,0] neg_hi:[1,0,0]
	v_pk_fma_f32 v[34:35], v[34:35], v[100:101], 0 op_sel_hi:[0,1,0] neg_lo:[1,0,0] neg_hi:[1,0,0]
	v_cvt_pk_bf16_f32 v36, v36, v37
	v_cvt_pk_bf16_f32 v37, v34, v35
	ds_write_b64 v186, v[36:37] offset:1632
	ds_read_b32 v34, v187 offset:224
	s_waitcnt lgkmcnt(0)
	v_pk_fma_f32 v[36:37], v[34:35], v[58:59], 0 op_sel_hi:[0,1,0] neg_lo:[1,0,0] neg_hi:[1,0,0]
	v_pk_fma_f32 v[34:35], v[34:35], v[60:61], 0 op_sel_hi:[0,1,0] neg_lo:[1,0,0] neg_hi:[1,0,0]
	v_cvt_pk_bf16_f32 v36, v36, v37
	v_cvt_pk_bf16_f32 v37, v34, v35
	ds_write_b64 v186, v[36:37] offset:2176
	ds_read_b32 v34, v187 offset:232
	s_waitcnt lgkmcnt(0)
	v_pk_fma_f32 v[36:37], v[34:35], v[50:51], 0 op_sel_hi:[0,1,0] neg_lo:[1,0,0] neg_hi:[1,0,0]
	v_pk_fma_f32 v[34:35], v[34:35], v[52:53], 0 op_sel_hi:[0,1,0] neg_lo:[1,0,0] neg_hi:[1,0,0]
	v_cvt_pk_bf16_f32 v36, v36, v37
	v_cvt_pk_bf16_f32 v37, v34, v35
	ds_write_b64 v186, v[36:37] offset:2720
	ds_read_b32 v34, v187 offset:240
	s_waitcnt lgkmcnt(0)
	v_pk_fma_f32 v[30:31], v[34:35], v[30:31], 0 op_sel_hi:[0,1,0] neg_lo:[1,0,0] neg_hi:[1,0,0]
	v_pk_fma_f32 v[32:33], v[34:35], v[32:33], 0 op_sel_hi:[0,1,0] neg_lo:[1,0,0] neg_hi:[1,0,0]
	v_cvt_pk_bf16_f32 v30, v30, v31
	v_cvt_pk_bf16_f32 v31, v32, v33
	ds_write_b64 v186, v[30:31] offset:3264
	ds_read_b32 v30, v187 offset:248
	s_waitcnt lgkmcnt(0)
	v_pk_fma_f32 v[22:23], v[30:31], v[22:23], 0 op_sel_hi:[0,1,0] neg_lo:[1,0,0] neg_hi:[1,0,0]
	v_pk_fma_f32 v[24:25], v[30:31], v[24:25], 0 op_sel_hi:[0,1,0] neg_lo:[1,0,0] neg_hi:[1,0,0]
	v_cvt_pk_bf16_f32 v22, v22, v23
	v_cvt_pk_bf16_f32 v23, v24, v25
	ds_write_b64 v186, v[22:23] offset:3808
	ds_read_b128 v[22:25], v1
	s_waitcnt lgkmcnt(0)
	ds_write_b128 v184, v[22:25] offset:20480
	ds_read_b128 v[22:25], v1 offset:64
	s_waitcnt lgkmcnt(0)
	ds_write_b128 v184, v[22:25] offset:21504
	ds_read_b128 v[22:25], v1 offset:128
	s_waitcnt lgkmcnt(0)
	ds_write_b128 v184, v[22:25] offset:22528
	ds_read_b128 v[22:25], v1 offset:192
	s_waitcnt lgkmcnt(0)
	ds_write_b128 v184, v[22:25] offset:23552
	v_lshl_add_u64 v[22:23], v[130:131], 0, s[30:31]
	s_movk_i32 s7, 0x2000
	v_add_co_u32_e32 v24, vcc, s7, v22
	s_movk_i32 s36, 0x4000
	s_nop 0
	v_addc_co_u32_e32 v25, vcc, 0, v23, vcc
	global_load_dwordx4 v[74:77], v[22:23], off nt
	global_load_dwordx4 v[62:65], v[24:25], off nt
	v_add_co_u32_e32 v24, vcc, s36, v22
	s_movk_i32 s37, 0x6000
	s_nop 0
	v_addc_co_u32_e32 v25, vcc, 0, v23, vcc
	v_add_co_u32_e32 v30, vcc, s37, v22
	s_mov_b32 s38, 0x8000
	s_nop 0
	v_addc_co_u32_e32 v31, vcc, 0, v23, vcc
	global_load_dwordx4 v[58:61], v[24:25], off nt
	global_load_dwordx4 v[46:49], v[30:31], off nt
	v_add_co_u32_e32 v24, vcc, s38, v22
	s_mov_b32 s39, 0xa000
	s_nop 0
	v_addc_co_u32_e32 v25, vcc, 0, v23, vcc
	v_add_co_u32_e32 v34, vcc, s39, v22
	s_mov_b32 s41, 0xc000
	s_nop 0
	v_addc_co_u32_e32 v35, vcc, 0, v23, vcc
	global_load_dwordx4 v[50:53], v[24:25], off nt
	global_load_dwordx4 v[30:33], v[34:35], off nt
	v_add_co_u32_e32 v24, vcc, s41, v22
	s_mov_b32 s42, 0xe000
	s_nop 0
	v_addc_co_u32_e32 v25, vcc, 0, v23, vcc
	v_add_co_u32_e32 v22, vcc, s42, v22
	s_nop 1
	v_addc_co_u32_e32 v23, vcc, 0, v23, vcc
	global_load_dwordx4 v[34:37], v[24:25], off nt
	s_nop 0
	global_load_dwordx4 v[22:25], v[22:23], off nt
	v_mov_b32_e32 v98, v195
	s_waitcnt vmcnt(23)
	s_waitcnt vmcnt(22)
	s_waitcnt vmcnt(21)
	s_waitcnt vmcnt(20)
	s_waitcnt vmcnt(19)
	s_waitcnt vmcnt(18)
	s_waitcnt vmcnt(17)
	s_waitcnt vmcnt(16)
	ds_read_b32 v98, v187 offset:192
	s_waitcnt lgkmcnt(0)
	v_pk_fma_f32 v[94:95], v[98:99], v[94:95], 0 op_sel_hi:[0,1,0] neg_lo:[1,0,0] neg_hi:[1,0,0]
	v_pk_fma_f32 v[96:97], v[98:99], v[96:97], 0 op_sel_hi:[0,1,0] neg_lo:[1,0,0] neg_hi:[1,0,0]
	v_cvt_pk_bf16_f32 v94, v94, v95
	v_cvt_pk_bf16_f32 v95, v96, v97
	ds_write_b64 v186, v[94:95]
	ds_read_b32 v94, v187 offset:200
	s_waitcnt lgkmcnt(0)
	v_pk_fma_f32 v[90:91], v[94:95], v[90:91], 0 op_sel_hi:[0,1,0] neg_lo:[1,0,0] neg_hi:[1,0,0]
	v_pk_fma_f32 v[92:93], v[94:95], v[92:93], 0 op_sel_hi:[0,1,0] neg_lo:[1,0,0] neg_hi:[1,0,0]
	v_cvt_pk_bf16_f32 v90, v90, v91
	v_cvt_pk_bf16_f32 v91, v92, v93
	ds_write_b64 v186, v[90:91] offset:544
	ds_read_b32 v90, v187 offset:208
	s_waitcnt lgkmcnt(0)
	v_pk_fma_f32 v[82:83], v[90:91], v[82:83], 0 op_sel_hi:[0,1,0] neg_lo:[1,0,0] neg_hi:[1,0,0]
	v_pk_fma_f32 v[84:85], v[90:91], v[84:85], 0 op_sel_hi:[0,1,0] neg_lo:[1,0,0] neg_hi:[1,0,0]
	v_cvt_pk_bf16_f32 v82, v82, v83
	v_cvt_pk_bf16_f32 v83, v84, v85
	ds_write_b64 v186, v[82:83] offset:1088
	ds_read_b32 v82, v187 offset:216
	s_waitcnt lgkmcnt(0)
	v_pk_fma_f32 v[70:71], v[82:83], v[70:71], 0 op_sel_hi:[0,1,0] neg_lo:[1,0,0] neg_hi:[1,0,0]
	v_pk_fma_f32 v[72:73], v[82:83], v[72:73], 0 op_sel_hi:[0,1,0] neg_lo:[1,0,0] neg_hi:[1,0,0]
	v_cvt_pk_bf16_f32 v70, v70, v71
	v_cvt_pk_bf16_f32 v71, v72, v73
	ds_write_b64 v186, v[70:71] offset:1632
	ds_read_b32 v70, v187 offset:224
	s_waitcnt lgkmcnt(0)
	v_pk_fma_f32 v[54:55], v[70:71], v[54:55], 0 op_sel_hi:[0,1,0] neg_lo:[1,0,0] neg_hi:[1,0,0]
	v_pk_fma_f32 v[56:57], v[70:71], v[56:57], 0 op_sel_hi:[0,1,0] neg_lo:[1,0,0] neg_hi:[1,0,0]
	v_cvt_pk_bf16_f32 v54, v54, v55
	v_cvt_pk_bf16_f32 v55, v56, v57
	ds_write_b64 v186, v[54:55] offset:2176
	ds_read_b32 v54, v187 offset:232
	s_waitcnt lgkmcnt(0)
	v_pk_fma_f32 v[26:27], v[54:55], v[26:27], 0 op_sel_hi:[0,1,0] neg_lo:[1,0,0] neg_hi:[1,0,0]
	v_pk_fma_f32 v[28:29], v[54:55], v[28:29], 0 op_sel_hi:[0,1,0] neg_lo:[1,0,0] neg_hi:[1,0,0]
	v_cvt_pk_bf16_f32 v26, v26, v27
	v_cvt_pk_bf16_f32 v27, v28, v29
	ds_write_b64 v186, v[26:27] offset:2720
	ds_read_b32 v26, v187 offset:240
	s_waitcnt lgkmcnt(0)
	v_pk_fma_f32 v[14:15], v[26:27], v[14:15], 0 op_sel_hi:[0,1,0] neg_lo:[1,0,0] neg_hi:[1,0,0]
	v_pk_fma_f32 v[16:17], v[26:27], v[16:17], 0 op_sel_hi:[0,1,0] neg_lo:[1,0,0] neg_hi:[1,0,0]
	v_cvt_pk_bf16_f32 v14, v14, v15
	v_cvt_pk_bf16_f32 v15, v16, v17
	ds_write_b64 v186, v[14:15] offset:3264
	ds_read_b32 v14, v187 offset:248
	s_waitcnt lgkmcnt(0)
	v_pk_fma_f32 v[6:7], v[14:15], v[6:7], 0 op_sel_hi:[0,1,0] neg_lo:[1,0,0] neg_hi:[1,0,0]
	v_pk_fma_f32 v[8:9], v[14:15], v[8:9], 0 op_sel_hi:[0,1,0] neg_lo:[1,0,0] neg_hi:[1,0,0]
	v_cvt_pk_bf16_f32 v6, v6, v7
	v_cvt_pk_bf16_f32 v7, v8, v9
	ds_write_b64 v186, v[6:7] offset:3808
	ds_read_b128 v[6:9], v1
	s_waitcnt lgkmcnt(0)
	ds_write_b128 v184, v[6:9] offset:24576
	ds_read_b128 v[6:9], v1 offset:64
	s_waitcnt lgkmcnt(0)
	ds_write_b128 v184, v[6:9] offset:25600
	ds_read_b128 v[6:9], v1 offset:128
	s_waitcnt lgkmcnt(0)
	ds_write_b128 v184, v[6:9] offset:26624
	ds_read_b128 v[6:9], v1 offset:192
	s_waitcnt lgkmcnt(0)
	ds_write_b128 v184, v[6:9] offset:27648
	s_mov_b64 s[44:45], 0x10000
	v_lshl_add_u64 v[150:151], v[130:131], 0, s[44:45]
	s_mov_b64 s[44:45], 0x12000
	v_lshl_add_u64 v[152:153], v[130:131], 0, s[44:45]
	s_mov_b64 s[44:45], 0x14000
	v_lshl_add_u64 v[156:157], v[130:131], 0, s[44:45]
	s_mov_b64 s[44:45], 0x16000
	v_lshl_add_u64 v[158:159], v[130:131], 0, s[44:45]
	s_mov_b64 s[44:45], 0x18000
	v_lshl_add_u64 v[160:161], v[130:131], 0, s[44:45]
	s_mov_b64 s[44:45], 0x1a000
	v_lshl_add_u64 v[162:163], v[130:131], 0, s[44:45]
	s_mov_b64 s[44:45], 0x1c000
	v_lshl_add_u64 v[164:165], v[130:131], 0, s[44:45]
	s_mov_b64 s[44:45], 0x1e000
	v_lshl_add_u64 v[6:7], v[150:151], 0, s[30:31]
	v_lshl_add_u64 v[8:9], v[152:153], 0, s[30:31]
	v_lshl_add_u64 v[14:15], v[156:157], 0, s[30:31]
	v_lshl_add_u64 v[16:17], v[158:159], 0, s[30:31]
	v_lshl_add_u64 v[26:27], v[160:161], 0, s[30:31]
	v_lshl_add_u64 v[28:29], v[162:163], 0, s[30:31]
	v_lshl_add_u64 v[166:167], v[130:131], 0, s[44:45]
	v_lshl_add_u64 v[98:99], v[164:165], 0, s[30:31]
	v_lshl_add_u64 v[100:101], v[166:167], 0, s[30:31]
	global_load_dwordx4 v[94:97], v[6:7], off nt
	global_load_dwordx4 v[90:93], v[8:9], off nt
	global_load_dwordx4 v[82:85], v[14:15], off nt
	global_load_dwordx4 v[70:73], v[16:17], off nt
	global_load_dwordx4 v[54:57], v[26:27], off nt
	s_nop 0
	global_load_dwordx4 v[26:29], v[28:29], off nt
	s_nop 0
	global_load_dwordx4 v[14:17], v[98:99], off nt
	global_load_dwordx4 v[6:9], v[100:101], off nt
	v_mov_b32_e32 v98, v194
	s_waitcnt vmcnt(23)
	s_waitcnt vmcnt(22)
	s_waitcnt vmcnt(21)
	s_waitcnt vmcnt(20)
	s_waitcnt vmcnt(19)
	s_waitcnt vmcnt(18)
	s_waitcnt vmcnt(17)
	s_waitcnt vmcnt(16)
	ds_read_b32 v98, v187 offset:192
	s_waitcnt lgkmcnt(0)
	v_pk_fma_f32 v[86:87], v[98:99], v[86:87], 0 op_sel_hi:[0,1,0] neg_lo:[1,0,0] neg_hi:[1,0,0]
	v_pk_fma_f32 v[88:89], v[98:99], v[88:89], 0 op_sel_hi:[0,1,0] neg_lo:[1,0,0] neg_hi:[1,0,0]
	v_cvt_pk_bf16_f32 v86, v86, v87
	v_cvt_pk_bf16_f32 v87, v88, v89
	ds_write_b64 v186, v[86:87]
	ds_read_b32 v86, v187 offset:200
	s_waitcnt lgkmcnt(0)
	v_pk_fma_f32 v[78:79], v[86:87], v[78:79], 0 op_sel_hi:[0,1,0] neg_lo:[1,0,0] neg_hi:[1,0,0]
	v_pk_fma_f32 v[80:81], v[86:87], v[80:81], 0 op_sel_hi:[0,1,0] neg_lo:[1,0,0] neg_hi:[1,0,0]
	v_cvt_pk_bf16_f32 v78, v78, v79
	v_cvt_pk_bf16_f32 v79, v80, v81
	ds_write_b64 v186, v[78:79] offset:544
	ds_read_b32 v78, v187 offset:208
	s_waitcnt lgkmcnt(0)
	v_pk_fma_f32 v[66:67], v[78:79], v[66:67], 0 op_sel_hi:[0,1,0] neg_lo:[1,0,0] neg_hi:[1,0,0]
	v_pk_fma_f32 v[68:69], v[78:79], v[68:69], 0 op_sel_hi:[0,1,0] neg_lo:[1,0,0] neg_hi:[1,0,0]
	v_cvt_pk_bf16_f32 v66, v66, v67
	v_cvt_pk_bf16_f32 v67, v68, v69
	ds_write_b64 v186, v[66:67] offset:1088
	ds_read_b32 v66, v187 offset:216
	s_waitcnt lgkmcnt(0)
	v_pk_fma_f32 v[42:43], v[66:67], v[42:43], 0 op_sel_hi:[0,1,0] neg_lo:[1,0,0] neg_hi:[1,0,0]
	v_pk_fma_f32 v[44:45], v[66:67], v[44:45], 0 op_sel_hi:[0,1,0] neg_lo:[1,0,0] neg_hi:[1,0,0]
	v_cvt_pk_bf16_f32 v42, v42, v43
	v_cvt_pk_bf16_f32 v43, v44, v45
	ds_write_b64 v186, v[42:43] offset:1632
	ds_read_b32 v42, v187 offset:224
	s_waitcnt lgkmcnt(0)
	v_pk_fma_f32 v[38:39], v[42:43], v[38:39], 0 op_sel_hi:[0,1,0] neg_lo:[1,0,0] neg_hi:[1,0,0]
	v_pk_fma_f32 v[40:41], v[42:43], v[40:41], 0 op_sel_hi:[0,1,0] neg_lo:[1,0,0] neg_hi:[1,0,0]
	v_cvt_pk_bf16_f32 v38, v38, v39
	v_cvt_pk_bf16_f32 v39, v40, v41
	ds_write_b64 v186, v[38:39] offset:2176
	ds_read_b32 v38, v187 offset:232
	s_waitcnt lgkmcnt(0)
	v_pk_fma_f32 v[18:19], v[38:39], v[18:19], 0 op_sel_hi:[0,1,0] neg_lo:[1,0,0] neg_hi:[1,0,0]
	v_pk_fma_f32 v[20:21], v[38:39], v[20:21], 0 op_sel_hi:[0,1,0] neg_lo:[1,0,0] neg_hi:[1,0,0]
	v_cvt_pk_bf16_f32 v18, v18, v19
	v_cvt_pk_bf16_f32 v19, v20, v21
	ds_write_b64 v186, v[18:19] offset:2720
	ds_read_b32 v18, v187 offset:240
	s_waitcnt lgkmcnt(0)
	v_pk_fma_f32 v[10:11], v[18:19], v[10:11], 0 op_sel_hi:[0,1,0] neg_lo:[1,0,0] neg_hi:[1,0,0]
	v_pk_fma_f32 v[12:13], v[18:19], v[12:13], 0 op_sel_hi:[0,1,0] neg_lo:[1,0,0] neg_hi:[1,0,0]
	v_cvt_pk_bf16_f32 v10, v10, v11
	v_cvt_pk_bf16_f32 v11, v12, v13
	ds_write_b64 v186, v[10:11] offset:3264
	ds_read_b32 v10, v187 offset:248
	s_waitcnt lgkmcnt(0)
	v_pk_fma_f32 v[2:3], v[10:11], v[2:3], 0 op_sel_hi:[0,1,0] neg_lo:[1,0,0] neg_hi:[1,0,0]
	v_pk_fma_f32 v[4:5], v[10:11], v[4:5], 0 op_sel_hi:[0,1,0] neg_lo:[1,0,0] neg_hi:[1,0,0]
	v_cvt_pk_bf16_f32 v2, v2, v3
	v_cvt_pk_bf16_f32 v3, v4, v5
	ds_write_b64 v186, v[2:3] offset:3808
	ds_read_b128 v[2:5], v1
	s_waitcnt lgkmcnt(0)
	ds_write_b128 v184, v[2:5] offset:28672
	ds_read_b128 v[2:5], v1 offset:64
	s_waitcnt lgkmcnt(0)
	ds_write_b128 v184, v[2:5] offset:29696
	ds_read_b128 v[2:5], v1 offset:128
	s_waitcnt lgkmcnt(0)
	ds_write_b128 v184, v[2:5] offset:30720
	ds_read_b128 v[2:5], v1 offset:192
	s_waitcnt lgkmcnt(0)
	ds_write_b128 v184, v[2:5] offset:31744
	s_mov_b64 s[44:45], 0x20000
	v_lshl_add_u64 v[168:169], v[130:131], 0, s[44:45]
	s_mov_b64 s[44:45], 0x22000
	v_lshl_add_u64 v[170:171], v[130:131], 0, s[44:45]
	s_mov_b64 s[44:45], 0x24000
	v_lshl_add_u64 v[172:173], v[130:131], 0, s[44:45]
	s_mov_b64 s[44:45], 0x26000
	v_lshl_add_u64 v[174:175], v[130:131], 0, s[44:45]
	s_mov_b64 s[44:45], 0x28000
	v_lshl_add_u64 v[176:177], v[130:131], 0, s[44:45]
	s_mov_b64 s[44:45], 0x2a000
	v_lshl_add_u64 v[178:179], v[130:131], 0, s[44:45]
	s_mov_b64 s[44:45], 0x2c000
	v_lshl_add_u64 v[180:181], v[130:131], 0, s[44:45]
	s_mov_b64 s[44:45], 0x2e000
	v_lshl_add_u64 v[2:3], v[168:169], 0, s[30:31]
	v_lshl_add_u64 v[4:5], v[170:171], 0, s[30:31]
	v_lshl_add_u64 v[10:11], v[172:173], 0, s[30:31]
	v_lshl_add_u64 v[12:13], v[174:175], 0, s[30:31]
	v_lshl_add_u64 v[18:19], v[176:177], 0, s[30:31]
	v_lshl_add_u64 v[20:21], v[178:179], 0, s[30:31]
	v_lshl_add_u64 v[182:183], v[130:131], 0, s[44:45]
	v_lshl_add_u64 v[42:43], v[180:181], 0, s[30:31]
	v_lshl_add_u64 v[44:45], v[182:183], 0, s[30:31]
	global_load_dwordx4 v[106:109], v[2:3], off nt
	global_load_dwordx4 v[98:101], v[4:5], off nt
	global_load_dwordx4 v[78:81], v[10:11], off nt
	global_load_dwordx4 v[66:69], v[12:13], off nt
	global_load_dwordx4 v[38:41], v[18:19], off nt
	s_nop 0
	global_load_dwordx4 v[18:21], v[20:21], off nt
	s_nop 0
	global_load_dwordx4 v[10:13], v[42:43], off nt
	global_load_dwordx4 v[2:5], v[44:45], off nt
	v_mov_b32_e32 v42, v198
	s_waitcnt vmcnt(23)
	s_waitcnt vmcnt(22)
	s_waitcnt vmcnt(21)
	s_waitcnt vmcnt(20)
	s_waitcnt vmcnt(19)
	s_waitcnt vmcnt(18)
	s_waitcnt vmcnt(17)
	s_waitcnt vmcnt(16)
	ds_read_b32 v42, v187
	s_waitcnt lgkmcnt(0)
	v_pk_fma_f32 v[44:45], v[42:43], v[74:75], 0 op_sel_hi:[0,1,0] neg_lo:[1,0,0] neg_hi:[1,0,0]
	v_pk_fma_f32 v[42:43], v[42:43], v[76:77], 0 op_sel_hi:[0,1,0] neg_lo:[1,0,0] neg_hi:[1,0,0]
	v_cvt_pk_bf16_f32 v44, v44, v45
	v_cvt_pk_bf16_f32 v45, v42, v43
	ds_write_b64 v186, v[44:45]
	ds_read_b32 v42, v187 offset:8
	s_waitcnt lgkmcnt(0)
	v_pk_fma_f32 v[44:45], v[42:43], v[62:63], 0 op_sel_hi:[0,1,0] neg_lo:[1,0,0] neg_hi:[1,0,0]
	v_pk_fma_f32 v[42:43], v[42:43], v[64:65], 0 op_sel_hi:[0,1,0] neg_lo:[1,0,0] neg_hi:[1,0,0]
	v_cvt_pk_bf16_f32 v44, v44, v45
	v_cvt_pk_bf16_f32 v45, v42, v43
	ds_write_b64 v186, v[44:45] offset:544
	ds_read_b32 v42, v187 offset:16
	s_waitcnt lgkmcnt(0)
	v_pk_fma_f32 v[44:45], v[42:43], v[58:59], 0 op_sel_hi:[0,1,0] neg_lo:[1,0,0] neg_hi:[1,0,0]
	v_pk_fma_f32 v[42:43], v[42:43], v[60:61], 0 op_sel_hi:[0,1,0] neg_lo:[1,0,0] neg_hi:[1,0,0]
	v_cvt_pk_bf16_f32 v44, v44, v45
	v_cvt_pk_bf16_f32 v45, v42, v43
	ds_write_b64 v186, v[44:45] offset:1088
	ds_read_b32 v42, v187 offset:24
	s_waitcnt lgkmcnt(0)
	v_pk_fma_f32 v[44:45], v[42:43], v[46:47], 0 op_sel_hi:[0,1,0] neg_lo:[1,0,0] neg_hi:[1,0,0]
	v_pk_fma_f32 v[42:43], v[42:43], v[48:49], 0 op_sel_hi:[0,1,0] neg_lo:[1,0,0] neg_hi:[1,0,0]
	v_cvt_pk_bf16_f32 v44, v44, v45
	v_cvt_pk_bf16_f32 v45, v42, v43
	ds_write_b64 v186, v[44:45] offset:1632
	ds_read_b32 v42, v187 offset:32
	s_waitcnt lgkmcnt(0)
	v_pk_fma_f32 v[44:45], v[42:43], v[50:51], 0 op_sel_hi:[0,1,0] neg_lo:[1,0,0] neg_hi:[1,0,0]
	v_pk_fma_f32 v[42:43], v[42:43], v[52:53], 0 op_sel_hi:[0,1,0] neg_lo:[1,0,0] neg_hi:[1,0,0]
	v_cvt_pk_bf16_f32 v44, v44, v45
	v_cvt_pk_bf16_f32 v45, v42, v43
	ds_write_b64 v186, v[44:45] offset:2176
	ds_read_b32 v42, v187 offset:40
	s_waitcnt lgkmcnt(0)
	v_pk_fma_f32 v[30:31], v[42:43], v[30:31], 0 op_sel_hi:[0,1,0] neg_lo:[1,0,0] neg_hi:[1,0,0]
	v_pk_fma_f32 v[32:33], v[42:43], v[32:33], 0 op_sel_hi:[0,1,0] neg_lo:[1,0,0] neg_hi:[1,0,0]
	v_cvt_pk_bf16_f32 v30, v30, v31
	v_cvt_pk_bf16_f32 v31, v32, v33
	ds_write_b64 v186, v[30:31] offset:2720
	ds_read_b32 v30, v187 offset:48
	s_waitcnt lgkmcnt(0)
	v_pk_fma_f32 v[32:33], v[30:31], v[34:35], 0 op_sel_hi:[0,1,0] neg_lo:[1,0,0] neg_hi:[1,0,0]
	v_pk_fma_f32 v[30:31], v[30:31], v[36:37], 0 op_sel_hi:[0,1,0] neg_lo:[1,0,0] neg_hi:[1,0,0]
	v_cvt_pk_bf16_f32 v32, v32, v33
	v_cvt_pk_bf16_f32 v33, v30, v31
	ds_write_b64 v186, v[32:33] offset:3264
	ds_read_b32 v30, v187 offset:56
	s_waitcnt lgkmcnt(0)
	v_pk_fma_f32 v[22:23], v[30:31], v[22:23], 0 op_sel_hi:[0,1,0] neg_lo:[1,0,0] neg_hi:[1,0,0]
	v_pk_fma_f32 v[24:25], v[30:31], v[24:25], 0 op_sel_hi:[0,1,0] neg_lo:[1,0,0] neg_hi:[1,0,0]
	v_cvt_pk_bf16_f32 v22, v22, v23
	v_cvt_pk_bf16_f32 v23, v24, v25
	ds_write_b64 v186, v[22:23] offset:3808
	ds_read_b128 a[0:3], v1
	ds_read_b128 a[4:7], v1 offset:64
	ds_read_b128 a[8:11], v1 offset:128
	ds_read_b128 a[12:15], v1 offset:192
	v_lshl_add_u64 v[22:23], v[130:131], 0, s[28:29]
	v_add_co_u32_e32 v24, vcc, s7, v22
	s_nop 1
	v_addc_co_u32_e32 v25, vcc, 0, v23, vcc
	global_load_dwordx4 v[102:105], v[22:23], off nt
	global_load_dwordx4 v[86:89], v[24:25], off nt
	v_add_co_u32_e32 v24, vcc, s36, v22
	s_nop 1
	v_addc_co_u32_e32 v25, vcc, 0, v23, vcc
	v_add_co_u32_e32 v30, vcc, s37, v22
	s_nop 1
	v_addc_co_u32_e32 v31, vcc, 0, v23, vcc
	global_load_dwordx4 v[74:77], v[24:25], off nt
	global_load_dwordx4 v[62:65], v[30:31], off nt
	v_add_co_u32_e32 v24, vcc, s38, v22
	s_nop 1
	v_addc_co_u32_e32 v25, vcc, 0, v23, vcc
	v_add_co_u32_e32 v30, vcc, s39, v22
	s_nop 1
	v_addc_co_u32_e32 v31, vcc, 0, v23, vcc
	global_load_dwordx4 v[58:61], v[24:25], off nt
	global_load_dwordx4 v[46:49], v[30:31], off nt
	v_add_co_u32_e32 v24, vcc, s41, v22
	s_nop 1
	v_addc_co_u32_e32 v25, vcc, 0, v23, vcc
	v_add_co_u32_e32 v22, vcc, s42, v22
	s_nop 1
	v_addc_co_u32_e32 v23, vcc, 0, v23, vcc
	global_load_dwordx4 v[42:45], v[24:25], off nt
	global_load_dwordx4 v[30:33], v[22:23], off nt
	v_mov_b32_e32 v22, v198
	s_waitcnt vmcnt(23)
	s_waitcnt vmcnt(22)
	s_waitcnt vmcnt(21)
	s_waitcnt vmcnt(20)
	s_waitcnt vmcnt(19)
	s_waitcnt vmcnt(18)
	s_waitcnt vmcnt(17)
	s_waitcnt vmcnt(16)
	ds_read_b32 v22, v187 offset:64
	s_waitcnt lgkmcnt(0)
	v_pk_fma_f32 v[24:25], v[22:23], v[94:95], 0 op_sel_hi:[0,1,0] neg_lo:[1,0,0] neg_hi:[1,0,0]
	v_pk_fma_f32 v[22:23], v[22:23], v[96:97], 0 op_sel_hi:[0,1,0] neg_lo:[1,0,0] neg_hi:[1,0,0]
	v_cvt_pk_bf16_f32 v24, v24, v25
	v_cvt_pk_bf16_f32 v25, v22, v23
	ds_write_b64 v186, v[24:25]
	ds_read_b32 v22, v187 offset:72
	s_waitcnt lgkmcnt(0)
	v_pk_fma_f32 v[24:25], v[22:23], v[90:91], 0 op_sel_hi:[0,1,0] neg_lo:[1,0,0] neg_hi:[1,0,0]
	v_pk_fma_f32 v[22:23], v[22:23], v[92:93], 0 op_sel_hi:[0,1,0] neg_lo:[1,0,0] neg_hi:[1,0,0]
	v_cvt_pk_bf16_f32 v24, v24, v25
	v_cvt_pk_bf16_f32 v25, v22, v23
	ds_write_b64 v186, v[24:25] offset:544
	ds_read_b32 v22, v187 offset:80
	s_waitcnt lgkmcnt(0)
	v_pk_fma_f32 v[24:25], v[22:23], v[82:83], 0 op_sel_hi:[0,1,0] neg_lo:[1,0,0] neg_hi:[1,0,0]
	v_pk_fma_f32 v[22:23], v[22:23], v[84:85], 0 op_sel_hi:[0,1,0] neg_lo:[1,0,0] neg_hi:[1,0,0]
	v_cvt_pk_bf16_f32 v24, v24, v25
	v_cvt_pk_bf16_f32 v25, v22, v23
	ds_write_b64 v186, v[24:25] offset:1088
	ds_read_b32 v22, v187 offset:88
	s_waitcnt lgkmcnt(0)
	v_pk_fma_f32 v[24:25], v[22:23], v[70:71], 0 op_sel_hi:[0,1,0] neg_lo:[1,0,0] neg_hi:[1,0,0]
	v_pk_fma_f32 v[22:23], v[22:23], v[72:73], 0 op_sel_hi:[0,1,0] neg_lo:[1,0,0] neg_hi:[1,0,0]
	v_cvt_pk_bf16_f32 v24, v24, v25
	v_cvt_pk_bf16_f32 v25, v22, v23
	ds_write_b64 v186, v[24:25] offset:1632
	ds_read_b32 v22, v187 offset:96
	s_waitcnt lgkmcnt(0)
	v_pk_fma_f32 v[24:25], v[22:23], v[54:55], 0 op_sel_hi:[0,1,0] neg_lo:[1,0,0] neg_hi:[1,0,0]
	v_pk_fma_f32 v[22:23], v[22:23], v[56:57], 0 op_sel_hi:[0,1,0] neg_lo:[1,0,0] neg_hi:[1,0,0]
	v_cvt_pk_bf16_f32 v24, v24, v25
	v_cvt_pk_bf16_f32 v25, v22, v23
	ds_write_b64 v186, v[24:25] offset:2176
	ds_read_b32 v22, v187 offset:104
	s_waitcnt lgkmcnt(0)
	v_pk_fma_f32 v[24:25], v[22:23], v[26:27], 0 op_sel_hi:[0,1,0] neg_lo:[1,0,0] neg_hi:[1,0,0]
	v_pk_fma_f32 v[22:23], v[22:23], v[28:29], 0 op_sel_hi:[0,1,0] neg_lo:[1,0,0] neg_hi:[1,0,0]
	v_cvt_pk_bf16_f32 v24, v24, v25
	v_cvt_pk_bf16_f32 v25, v22, v23
	ds_write_b64 v186, v[24:25] offset:2720
	ds_read_b32 v22, v187 offset:112
	s_waitcnt lgkmcnt(0)
	v_pk_fma_f32 v[14:15], v[22:23], v[14:15], 0 op_sel_hi:[0,1,0] neg_lo:[1,0,0] neg_hi:[1,0,0]
	v_pk_fma_f32 v[16:17], v[22:23], v[16:17], 0 op_sel_hi:[0,1,0] neg_lo:[1,0,0] neg_hi:[1,0,0]
	v_cvt_pk_bf16_f32 v14, v14, v15
	v_cvt_pk_bf16_f32 v15, v16, v17
	ds_write_b64 v186, v[14:15] offset:3264
	ds_read_b32 v14, v187 offset:120
	s_waitcnt lgkmcnt(0)
	v_pk_fma_f32 v[6:7], v[14:15], v[6:7], 0 op_sel_hi:[0,1,0] neg_lo:[1,0,0] neg_hi:[1,0,0]
	v_pk_fma_f32 v[8:9], v[14:15], v[8:9], 0 op_sel_hi:[0,1,0] neg_lo:[1,0,0] neg_hi:[1,0,0]
	v_cvt_pk_bf16_f32 v6, v6, v7
	v_cvt_pk_bf16_f32 v7, v8, v9
	ds_write_b64 v186, v[6:7] offset:3808
	ds_read_b128 a[16:19], v1
	ds_read_b128 a[20:23], v1 offset:64
	ds_read_b128 a[24:27], v1 offset:128
	ds_read_b128 a[28:31], v1 offset:192
	v_lshl_add_u64 v[6:7], v[150:151], 0, s[28:29]
	v_lshl_add_u64 v[8:9], v[152:153], 0, s[28:29]
	v_lshl_add_u64 v[14:15], v[156:157], 0, s[28:29]
	v_lshl_add_u64 v[16:17], v[158:159], 0, s[28:29]
	v_lshl_add_u64 v[22:23], v[160:161], 0, s[28:29]
	v_lshl_add_u64 v[24:25], v[162:163], 0, s[28:29]
	v_lshl_add_u64 v[26:27], v[164:165], 0, s[28:29]
	v_lshl_add_u64 v[28:29], v[166:167], 0, s[28:29]
	global_load_dwordx4 v[110:113], v[6:7], off nt
	global_load_dwordx4 v[90:93], v[8:9], off nt
	global_load_dwordx4 v[70:73], v[14:15], off nt
	global_load_dwordx4 v[50:53], v[16:17], off nt
	global_load_dwordx4 v[34:37], v[22:23], off nt
	s_nop 0
	global_load_dwordx4 v[22:25], v[24:25], off nt
	s_nop 0
	global_load_dwordx4 v[14:17], v[26:27], off nt
	global_load_dwordx4 v[6:9], v[28:29], off nt
	s_waitcnt vmcnt(23)
	s_waitcnt vmcnt(22)
	s_waitcnt vmcnt(21)
	s_waitcnt vmcnt(20)
	s_waitcnt vmcnt(19)
	s_waitcnt vmcnt(18)
	s_waitcnt vmcnt(17)
	s_waitcnt vmcnt(16)
	ds_read_b32 v26, v187 offset:128
	s_waitcnt lgkmcnt(0)
	v_pk_fma_f32 v[28:29], v[26:27], v[106:107], 0 op_sel_hi:[0,1,0] neg_lo:[1,0,0] neg_hi:[1,0,0]
	v_pk_fma_f32 v[26:27], v[26:27], v[108:109], 0 op_sel_hi:[0,1,0] neg_lo:[1,0,0] neg_hi:[1,0,0]
	v_cvt_pk_bf16_f32 v28, v28, v29
	v_cvt_pk_bf16_f32 v29, v26, v27
	ds_write_b64 v186, v[28:29]
	ds_read_b32 v26, v187 offset:136
	s_waitcnt lgkmcnt(0)
	v_pk_fma_f32 v[28:29], v[26:27], v[98:99], 0 op_sel_hi:[0,1,0] neg_lo:[1,0,0] neg_hi:[1,0,0]
	v_pk_fma_f32 v[26:27], v[26:27], v[100:101], 0 op_sel_hi:[0,1,0] neg_lo:[1,0,0] neg_hi:[1,0,0]
	v_cvt_pk_bf16_f32 v28, v28, v29
	v_cvt_pk_bf16_f32 v29, v26, v27
	ds_write_b64 v186, v[28:29] offset:544
	ds_read_b32 v26, v187 offset:144
	s_waitcnt lgkmcnt(0)
	v_pk_fma_f32 v[28:29], v[26:27], v[78:79], 0 op_sel_hi:[0,1,0] neg_lo:[1,0,0] neg_hi:[1,0,0]
	v_pk_fma_f32 v[26:27], v[26:27], v[80:81], 0 op_sel_hi:[0,1,0] neg_lo:[1,0,0] neg_hi:[1,0,0]
	v_cvt_pk_bf16_f32 v28, v28, v29
	v_cvt_pk_bf16_f32 v29, v26, v27
	ds_write_b64 v186, v[28:29] offset:1088
	ds_read_b32 v26, v187 offset:152
	s_waitcnt lgkmcnt(0)
	v_pk_fma_f32 v[28:29], v[26:27], v[66:67], 0 op_sel_hi:[0,1,0] neg_lo:[1,0,0] neg_hi:[1,0,0]
	v_pk_fma_f32 v[26:27], v[26:27], v[68:69], 0 op_sel_hi:[0,1,0] neg_lo:[1,0,0] neg_hi:[1,0,0]
	v_cvt_pk_bf16_f32 v28, v28, v29
	v_cvt_pk_bf16_f32 v29, v26, v27
	ds_write_b64 v186, v[28:29] offset:1632
	ds_read_b32 v26, v187 offset:160
	s_waitcnt lgkmcnt(0)
	v_pk_fma_f32 v[28:29], v[26:27], v[38:39], 0 op_sel_hi:[0,1,0] neg_lo:[1,0,0] neg_hi:[1,0,0]
	v_pk_fma_f32 v[26:27], v[26:27], v[40:41], 0 op_sel_hi:[0,1,0] neg_lo:[1,0,0] neg_hi:[1,0,0]
	v_cvt_pk_bf16_f32 v28, v28, v29
	v_cvt_pk_bf16_f32 v29, v26, v27
	ds_write_b64 v186, v[28:29] offset:2176
	ds_read_b32 v26, v187 offset:168
	s_waitcnt lgkmcnt(0)
	v_pk_fma_f32 v[18:19], v[26:27], v[18:19], 0 op_sel_hi:[0,1,0] neg_lo:[1,0,0] neg_hi:[1,0,0]
	v_pk_fma_f32 v[20:21], v[26:27], v[20:21], 0 op_sel_hi:[0,1,0] neg_lo:[1,0,0] neg_hi:[1,0,0]
	v_cvt_pk_bf16_f32 v18, v18, v19
	v_cvt_pk_bf16_f32 v19, v20, v21
	ds_write_b64 v186, v[18:19] offset:2720
	ds_read_b32 v18, v187 offset:176
	s_waitcnt lgkmcnt(0)
	v_pk_fma_f32 v[10:11], v[18:19], v[10:11], 0 op_sel_hi:[0,1,0] neg_lo:[1,0,0] neg_hi:[1,0,0]
	v_pk_fma_f32 v[12:13], v[18:19], v[12:13], 0 op_sel_hi:[0,1,0] neg_lo:[1,0,0] neg_hi:[1,0,0]
	v_cvt_pk_bf16_f32 v10, v10, v11
	v_cvt_pk_bf16_f32 v11, v12, v13
	ds_write_b64 v186, v[10:11] offset:3264
	ds_read_b32 v10, v187 offset:184
	s_waitcnt lgkmcnt(0)
	v_pk_fma_f32 v[2:3], v[10:11], v[2:3], 0 op_sel_hi:[0,1,0] neg_lo:[1,0,0] neg_hi:[1,0,0]
	v_pk_fma_f32 v[4:5], v[10:11], v[4:5], 0 op_sel_hi:[0,1,0] neg_lo:[1,0,0] neg_hi:[1,0,0]
	v_cvt_pk_bf16_f32 v2, v2, v3
	v_cvt_pk_bf16_f32 v3, v4, v5
	ds_write_b64 v186, v[2:3] offset:3808
	ds_read_b128 a[32:35], v1
	ds_read_b128 a[36:39], v1 offset:64
	ds_read_b128 a[40:43], v1 offset:128
	ds_read_b128 a[44:47], v1 offset:192
	v_lshl_add_u64 v[2:3], v[168:169], 0, s[28:29]
	v_lshl_add_u64 v[4:5], v[170:171], 0, s[28:29]
	v_lshl_add_u64 v[10:11], v[172:173], 0, s[28:29]
	v_lshl_add_u64 v[12:13], v[174:175], 0, s[28:29]
	v_lshl_add_u64 v[18:19], v[176:177], 0, s[28:29]
	v_lshl_add_u64 v[20:21], v[178:179], 0, s[28:29]
	v_lshl_add_u64 v[26:27], v[180:181], 0, s[28:29]
	v_lshl_add_u64 v[28:29], v[182:183], 0, s[28:29]
	global_load_dwordx4 v[106:109], v[2:3], off nt
	global_load_dwordx4 v[94:97], v[4:5], off nt
	global_load_dwordx4 v[66:69], v[10:11], off nt
	global_load_dwordx4 v[54:57], v[12:13], off nt
	global_load_dwordx4 v[38:41], v[18:19], off nt
	s_nop 0
	global_load_dwordx4 v[18:21], v[20:21], off nt
	s_nop 0
	global_load_dwordx4 v[10:13], v[26:27], off nt
	global_load_dwordx4 v[2:5], v[28:29], off nt
	v_mov_b32_e32 v26, v197
	s_waitcnt vmcnt(23)
	s_waitcnt vmcnt(22)
	s_waitcnt vmcnt(21)
	s_waitcnt vmcnt(20)
	s_waitcnt vmcnt(19)
	s_waitcnt vmcnt(18)
	s_waitcnt vmcnt(17)
	s_waitcnt vmcnt(16)
	ds_read_b32 v26, v187
	s_waitcnt lgkmcnt(0)
	v_pk_fma_f32 v[28:29], v[26:27], v[102:103], 0 op_sel_hi:[0,1,0] neg_lo:[1,0,0] neg_hi:[1,0,0]
	v_pk_fma_f32 v[26:27], v[26:27], v[104:105], 0 op_sel_hi:[0,1,0] neg_lo:[1,0,0] neg_hi:[1,0,0]
	v_cvt_pk_bf16_f32 v28, v28, v29
	v_cvt_pk_bf16_f32 v29, v26, v27
	ds_write_b64 v186, v[28:29]
	ds_read_b32 v26, v187 offset:8
	s_waitcnt lgkmcnt(0)
	v_pk_fma_f32 v[28:29], v[26:27], v[86:87], 0 op_sel_hi:[0,1,0] neg_lo:[1,0,0] neg_hi:[1,0,0]
	v_pk_fma_f32 v[26:27], v[26:27], v[88:89], 0 op_sel_hi:[0,1,0] neg_lo:[1,0,0] neg_hi:[1,0,0]
	v_cvt_pk_bf16_f32 v28, v28, v29
	v_cvt_pk_bf16_f32 v29, v26, v27
	ds_write_b64 v186, v[28:29] offset:544
	ds_read_b32 v26, v187 offset:16
	s_waitcnt lgkmcnt(0)
	v_pk_fma_f32 v[28:29], v[26:27], v[74:75], 0 op_sel_hi:[0,1,0] neg_lo:[1,0,0] neg_hi:[1,0,0]
	v_pk_fma_f32 v[26:27], v[26:27], v[76:77], 0 op_sel_hi:[0,1,0] neg_lo:[1,0,0] neg_hi:[1,0,0]
	v_cvt_pk_bf16_f32 v28, v28, v29
	v_cvt_pk_bf16_f32 v29, v26, v27
	ds_write_b64 v186, v[28:29] offset:1088
	ds_read_b32 v26, v187 offset:24
	s_waitcnt lgkmcnt(0)
	v_pk_fma_f32 v[28:29], v[26:27], v[62:63], 0 op_sel_hi:[0,1,0] neg_lo:[1,0,0] neg_hi:[1,0,0]
	v_pk_fma_f32 v[26:27], v[26:27], v[64:65], 0 op_sel_hi:[0,1,0] neg_lo:[1,0,0] neg_hi:[1,0,0]
	v_cvt_pk_bf16_f32 v28, v28, v29
	v_cvt_pk_bf16_f32 v29, v26, v27
	ds_write_b64 v186, v[28:29] offset:1632
	ds_read_b32 v26, v187 offset:32
	s_waitcnt lgkmcnt(0)
	v_pk_fma_f32 v[28:29], v[26:27], v[58:59], 0 op_sel_hi:[0,1,0] neg_lo:[1,0,0] neg_hi:[1,0,0]
	v_pk_fma_f32 v[26:27], v[26:27], v[60:61], 0 op_sel_hi:[0,1,0] neg_lo:[1,0,0] neg_hi:[1,0,0]
	v_cvt_pk_bf16_f32 v28, v28, v29
	v_cvt_pk_bf16_f32 v29, v26, v27
	ds_write_b64 v186, v[28:29] offset:2176
	ds_read_b32 v26, v187 offset:40
	s_waitcnt lgkmcnt(0)
	v_pk_fma_f32 v[28:29], v[26:27], v[46:47], 0 op_sel_hi:[0,1,0] neg_lo:[1,0,0] neg_hi:[1,0,0]
	v_pk_fma_f32 v[26:27], v[26:27], v[48:49], 0 op_sel_hi:[0,1,0] neg_lo:[1,0,0] neg_hi:[1,0,0]
	v_cvt_pk_bf16_f32 v28, v28, v29
	v_cvt_pk_bf16_f32 v29, v26, v27
	ds_write_b64 v186, v[28:29] offset:2720
	ds_read_b32 v26, v187 offset:48
	s_waitcnt lgkmcnt(0)
	v_pk_fma_f32 v[28:29], v[26:27], v[42:43], 0 op_sel_hi:[0,1,0] neg_lo:[1,0,0] neg_hi:[1,0,0]
	v_pk_fma_f32 v[26:27], v[26:27], v[44:45], 0 op_sel_hi:[0,1,0] neg_lo:[1,0,0] neg_hi:[1,0,0]
	v_cvt_pk_bf16_f32 v28, v28, v29
	v_cvt_pk_bf16_f32 v29, v26, v27
	ds_write_b64 v186, v[28:29] offset:3264
	ds_read_b32 v26, v187 offset:56
	s_waitcnt lgkmcnt(0)
	v_pk_fma_f32 v[28:29], v[26:27], v[30:31], 0 op_sel_hi:[0,1,0] neg_lo:[1,0,0] neg_hi:[1,0,0]
	v_pk_fma_f32 v[26:27], v[26:27], v[32:33], 0 op_sel_hi:[0,1,0] neg_lo:[1,0,0] neg_hi:[1,0,0]
	v_cvt_pk_bf16_f32 v28, v28, v29
	v_cvt_pk_bf16_f32 v29, v26, v27
	ds_write_b64 v186, v[28:29] offset:3808
	ds_read_b128 a[48:51], v1
	ds_read_b128 a[52:55], v1 offset:64
	ds_read_b128 a[56:59], v1 offset:128
	ds_read_b128 a[60:63], v1 offset:192
	v_lshl_add_u64 v[26:27], v[130:131], 0, s[26:27]
	v_add_co_u32_e32 v28, vcc, s7, v26
	s_nop 1
	v_addc_co_u32_e32 v29, vcc, 0, v27, vcc
	global_load_dwordx4 v[86:89], v[26:27], off nt
	global_load_dwordx4 v[82:85], v[28:29], off nt
	v_add_co_u32_e32 v28, vcc, s36, v26
	s_nop 1
	v_addc_co_u32_e32 v29, vcc, 0, v27, vcc
	v_add_co_u32_e32 v30, vcc, s37, v26
	s_nop 1
	v_addc_co_u32_e32 v31, vcc, 0, v27, vcc
	global_load_dwordx4 v[78:81], v[28:29], off nt
	global_load_dwordx4 v[58:61], v[30:31], off nt
	v_add_co_u32_e32 v28, vcc, s38, v26
	s_nop 1
	v_addc_co_u32_e32 v29, vcc, 0, v27, vcc
	v_add_co_u32_e32 v30, vcc, s39, v26
	s_nop 1
	v_addc_co_u32_e32 v31, vcc, 0, v27, vcc
	global_load_dwordx4 v[46:49], v[28:29], off nt
	global_load_dwordx4 v[42:45], v[30:31], off nt
	v_add_co_u32_e32 v28, vcc, s41, v26
	s_nop 1
	v_addc_co_u32_e32 v29, vcc, 0, v27, vcc
	v_add_co_u32_e32 v26, vcc, s42, v26
	s_nop 1
	v_addc_co_u32_e32 v27, vcc, 0, v27, vcc
	global_load_dwordx4 v[30:33], v[28:29], off nt
	s_nop 0
	global_load_dwordx4 v[26:29], v[26:27], off nt
	v_mov_b32_e32 v62, v197
	s_waitcnt vmcnt(23)
	s_waitcnt vmcnt(22)
	s_waitcnt vmcnt(21)
	s_waitcnt vmcnt(20)
	s_waitcnt vmcnt(19)
	s_waitcnt vmcnt(18)
	s_waitcnt vmcnt(17)
	s_waitcnt vmcnt(16)
	ds_read_b32 v62, v187 offset:64
	s_waitcnt lgkmcnt(0)
	v_pk_fma_f32 v[64:65], v[62:63], v[110:111], 0 op_sel_hi:[0,1,0] neg_lo:[1,0,0] neg_hi:[1,0,0]
	v_pk_fma_f32 v[62:63], v[62:63], v[112:113], 0 op_sel_hi:[0,1,0] neg_lo:[1,0,0] neg_hi:[1,0,0]
	v_cvt_pk_bf16_f32 v64, v64, v65
	v_cvt_pk_bf16_f32 v65, v62, v63
	ds_write_b64 v186, v[64:65]
	ds_read_b32 v62, v187 offset:72
	s_waitcnt lgkmcnt(0)
	v_pk_fma_f32 v[64:65], v[62:63], v[90:91], 0 op_sel_hi:[0,1,0] neg_lo:[1,0,0] neg_hi:[1,0,0]
	v_pk_fma_f32 v[62:63], v[62:63], v[92:93], 0 op_sel_hi:[0,1,0] neg_lo:[1,0,0] neg_hi:[1,0,0]
	v_cvt_pk_bf16_f32 v64, v64, v65
	v_cvt_pk_bf16_f32 v65, v62, v63
	ds_write_b64 v186, v[64:65] offset:544
	ds_read_b32 v62, v187 offset:80
	s_waitcnt lgkmcnt(0)
	v_pk_fma_f32 v[64:65], v[62:63], v[70:71], 0 op_sel_hi:[0,1,0] neg_lo:[1,0,0] neg_hi:[1,0,0]
	v_pk_fma_f32 v[62:63], v[62:63], v[72:73], 0 op_sel_hi:[0,1,0] neg_lo:[1,0,0] neg_hi:[1,0,0]
	v_cvt_pk_bf16_f32 v64, v64, v65
	v_cvt_pk_bf16_f32 v65, v62, v63
	ds_write_b64 v186, v[64:65] offset:1088
	ds_read_b32 v62, v187 offset:88
	s_waitcnt lgkmcnt(0)
	v_pk_fma_f32 v[50:51], v[62:63], v[50:51], 0 op_sel_hi:[0,1,0] neg_lo:[1,0,0] neg_hi:[1,0,0]
	v_pk_fma_f32 v[52:53], v[62:63], v[52:53], 0 op_sel_hi:[0,1,0] neg_lo:[1,0,0] neg_hi:[1,0,0]
	v_cvt_pk_bf16_f32 v50, v50, v51
	v_cvt_pk_bf16_f32 v51, v52, v53
	ds_write_b64 v186, v[50:51] offset:1632
	ds_read_b32 v50, v187 offset:96
	s_waitcnt lgkmcnt(0)
	v_pk_fma_f32 v[34:35], v[50:51], v[34:35], 0 op_sel_hi:[0,1,0] neg_lo:[1,0,0] neg_hi:[1,0,0]
	v_pk_fma_f32 v[36:37], v[50:51], v[36:37], 0 op_sel_hi:[0,1,0] neg_lo:[1,0,0] neg_hi:[1,0,0]
	v_cvt_pk_bf16_f32 v34, v34, v35
	v_cvt_pk_bf16_f32 v35, v36, v37
	ds_write_b64 v186, v[34:35] offset:2176
	ds_read_b32 v34, v187 offset:104
	s_waitcnt lgkmcnt(0)
	v_pk_fma_f32 v[22:23], v[34:35], v[22:23], 0 op_sel_hi:[0,1,0] neg_lo:[1,0,0] neg_hi:[1,0,0]
	v_pk_fma_f32 v[24:25], v[34:35], v[24:25], 0 op_sel_hi:[0,1,0] neg_lo:[1,0,0] neg_hi:[1,0,0]
	v_cvt_pk_bf16_f32 v22, v22, v23
	v_cvt_pk_bf16_f32 v23, v24, v25
	ds_write_b64 v186, v[22:23] offset:2720
	ds_read_b32 v22, v187 offset:112
	s_waitcnt lgkmcnt(0)
	v_pk_fma_f32 v[14:15], v[22:23], v[14:15], 0 op_sel_hi:[0,1,0] neg_lo:[1,0,0] neg_hi:[1,0,0]
	v_pk_fma_f32 v[16:17], v[22:23], v[16:17], 0 op_sel_hi:[0,1,0] neg_lo:[1,0,0] neg_hi:[1,0,0]
	v_cvt_pk_bf16_f32 v14, v14, v15
	v_cvt_pk_bf16_f32 v15, v16, v17
	ds_write_b64 v186, v[14:15] offset:3264
	ds_read_b32 v14, v187 offset:120
	s_waitcnt lgkmcnt(0)
	v_pk_fma_f32 v[6:7], v[14:15], v[6:7], 0 op_sel_hi:[0,1,0] neg_lo:[1,0,0] neg_hi:[1,0,0]
	v_pk_fma_f32 v[8:9], v[14:15], v[8:9], 0 op_sel_hi:[0,1,0] neg_lo:[1,0,0] neg_hi:[1,0,0]
	v_cvt_pk_bf16_f32 v6, v6, v7
	v_cvt_pk_bf16_f32 v7, v8, v9
	ds_write_b64 v186, v[6:7] offset:3808
	ds_read_b128 a[64:67], v1
	ds_read_b128 a[68:71], v1 offset:64
	ds_read_b128 a[72:75], v1 offset:128
	ds_read_b128 a[76:79], v1 offset:192
	v_lshl_add_u64 v[6:7], v[150:151], 0, s[26:27]
	v_lshl_add_u64 v[8:9], v[152:153], 0, s[26:27]
	v_lshl_add_u64 v[14:15], v[156:157], 0, s[26:27]
	v_lshl_add_u64 v[16:17], v[158:159], 0, s[26:27]
	v_lshl_add_u64 v[22:23], v[160:161], 0, s[26:27]
	v_lshl_add_u64 v[24:25], v[162:163], 0, s[26:27]
	v_lshl_add_u64 v[70:71], v[164:165], 0, s[26:27]
	v_lshl_add_u64 v[72:73], v[166:167], 0, s[26:27]
	global_load_dwordx4 v[110:113], v[6:7], off nt
	global_load_dwordx4 v[98:101], v[8:9], off nt
	global_load_dwordx4 v[62:65], v[14:15], off nt
	global_load_dwordx4 v[50:53], v[16:17], off nt
	global_load_dwordx4 v[34:37], v[22:23], off nt
	s_nop 0
	global_load_dwordx4 v[22:25], v[24:25], off nt
	s_nop 0
	global_load_dwordx4 v[14:17], v[70:71], off nt
	global_load_dwordx4 v[6:9], v[72:73], off nt
	s_waitcnt vmcnt(23)
	s_waitcnt vmcnt(22)
	s_waitcnt vmcnt(21)
	s_waitcnt vmcnt(20)
	s_waitcnt vmcnt(19)
	s_waitcnt vmcnt(18)
	s_waitcnt vmcnt(17)
	s_waitcnt vmcnt(16)
	ds_read_b32 v70, v187 offset:128
	s_waitcnt lgkmcnt(0)
	v_pk_fma_f32 v[72:73], v[70:71], v[106:107], 0 op_sel_hi:[0,1,0] neg_lo:[1,0,0] neg_hi:[1,0,0]
	v_pk_fma_f32 v[70:71], v[70:71], v[108:109], 0 op_sel_hi:[0,1,0] neg_lo:[1,0,0] neg_hi:[1,0,0]
	v_cvt_pk_bf16_f32 v72, v72, v73
	v_cvt_pk_bf16_f32 v73, v70, v71
	ds_write_b64 v186, v[72:73]
	ds_read_b32 v70, v187 offset:136
	s_waitcnt lgkmcnt(0)
	v_pk_fma_f32 v[72:73], v[70:71], v[94:95], 0 op_sel_hi:[0,1,0] neg_lo:[1,0,0] neg_hi:[1,0,0]
	v_pk_fma_f32 v[70:71], v[70:71], v[96:97], 0 op_sel_hi:[0,1,0] neg_lo:[1,0,0] neg_hi:[1,0,0]
	v_cvt_pk_bf16_f32 v72, v72, v73
	v_cvt_pk_bf16_f32 v73, v70, v71
	ds_write_b64 v186, v[72:73] offset:544
	ds_read_b32 v70, v187 offset:144
	s_waitcnt lgkmcnt(0)
	v_pk_fma_f32 v[66:67], v[70:71], v[66:67], 0 op_sel_hi:[0,1,0] neg_lo:[1,0,0] neg_hi:[1,0,0]
	v_pk_fma_f32 v[68:69], v[70:71], v[68:69], 0 op_sel_hi:[0,1,0] neg_lo:[1,0,0] neg_hi:[1,0,0]
	v_cvt_pk_bf16_f32 v66, v66, v67
	v_cvt_pk_bf16_f32 v67, v68, v69
	ds_write_b64 v186, v[66:67] offset:1088
	ds_read_b32 v66, v187 offset:152
	s_waitcnt lgkmcnt(0)
	v_pk_fma_f32 v[54:55], v[66:67], v[54:55], 0 op_sel_hi:[0,1,0] neg_lo:[1,0,0] neg_hi:[1,0,0]
	v_pk_fma_f32 v[56:57], v[66:67], v[56:57], 0 op_sel_hi:[0,1,0] neg_lo:[1,0,0] neg_hi:[1,0,0]
	v_cvt_pk_bf16_f32 v54, v54, v55
	v_cvt_pk_bf16_f32 v55, v56, v57
	ds_write_b64 v186, v[54:55] offset:1632
	ds_read_b32 v54, v187 offset:160
	s_waitcnt lgkmcnt(0)
	v_pk_fma_f32 v[38:39], v[54:55], v[38:39], 0 op_sel_hi:[0,1,0] neg_lo:[1,0,0] neg_hi:[1,0,0]
	v_pk_fma_f32 v[40:41], v[54:55], v[40:41], 0 op_sel_hi:[0,1,0] neg_lo:[1,0,0] neg_hi:[1,0,0]
	v_cvt_pk_bf16_f32 v38, v38, v39
	v_cvt_pk_bf16_f32 v39, v40, v41
	ds_write_b64 v186, v[38:39] offset:2176
	ds_read_b32 v38, v187 offset:168
	s_waitcnt lgkmcnt(0)
	v_pk_fma_f32 v[18:19], v[38:39], v[18:19], 0 op_sel_hi:[0,1,0] neg_lo:[1,0,0] neg_hi:[1,0,0]
	v_pk_fma_f32 v[20:21], v[38:39], v[20:21], 0 op_sel_hi:[0,1,0] neg_lo:[1,0,0] neg_hi:[1,0,0]
	v_cvt_pk_bf16_f32 v18, v18, v19
	v_cvt_pk_bf16_f32 v19, v20, v21
	ds_write_b64 v186, v[18:19] offset:2720
	ds_read_b32 v18, v187 offset:176
	s_waitcnt lgkmcnt(0)
	v_pk_fma_f32 v[10:11], v[18:19], v[10:11], 0 op_sel_hi:[0,1,0] neg_lo:[1,0,0] neg_hi:[1,0,0]
	v_pk_fma_f32 v[12:13], v[18:19], v[12:13], 0 op_sel_hi:[0,1,0] neg_lo:[1,0,0] neg_hi:[1,0,0]
	v_cvt_pk_bf16_f32 v10, v10, v11
	v_cvt_pk_bf16_f32 v11, v12, v13
	ds_write_b64 v186, v[10:11] offset:3264
	ds_read_b32 v10, v187 offset:184
	s_waitcnt lgkmcnt(0)
	v_pk_fma_f32 v[2:3], v[10:11], v[2:3], 0 op_sel_hi:[0,1,0] neg_lo:[1,0,0] neg_hi:[1,0,0]
	v_pk_fma_f32 v[4:5], v[10:11], v[4:5], 0 op_sel_hi:[0,1,0] neg_lo:[1,0,0] neg_hi:[1,0,0]
	v_cvt_pk_bf16_f32 v2, v2, v3
	v_cvt_pk_bf16_f32 v3, v4, v5
	ds_write_b64 v186, v[2:3] offset:3808
	ds_read_b128 a[80:83], v1
	ds_read_b128 a[84:87], v1 offset:64
	ds_read_b128 a[88:91], v1 offset:128
	ds_read_b128 a[92:95], v1 offset:192
	v_lshl_add_u64 v[2:3], v[168:169], 0, s[26:27]
	v_lshl_add_u64 v[4:5], v[170:171], 0, s[26:27]
	v_lshl_add_u64 v[10:11], v[172:173], 0, s[26:27]
	v_lshl_add_u64 v[12:13], v[174:175], 0, s[26:27]
	v_lshl_add_u64 v[18:19], v[176:177], 0, s[26:27]
	v_lshl_add_u64 v[20:21], v[178:179], 0, s[26:27]
	v_lshl_add_u64 v[66:67], v[180:181], 0, s[26:27]
	v_lshl_add_u64 v[68:69], v[182:183], 0, s[26:27]
	global_load_dwordx4 v[106:109], v[2:3], off nt
	global_load_dwordx4 v[94:97], v[4:5], off nt
	global_load_dwordx4 v[74:77], v[10:11], off nt
	global_load_dwordx4 v[54:57], v[12:13], off nt
	global_load_dwordx4 v[38:41], v[18:19], off nt
	s_nop 0
	global_load_dwordx4 v[18:21], v[20:21], off nt
	s_nop 0
	global_load_dwordx4 v[10:13], v[66:67], off nt
	global_load_dwordx4 v[2:5], v[68:69], off nt
	v_mov_b32_e32 v66, v196
	s_waitcnt vmcnt(23)
	s_waitcnt vmcnt(22)
	s_waitcnt vmcnt(21)
	s_waitcnt vmcnt(20)
	s_waitcnt vmcnt(19)
	s_waitcnt vmcnt(18)
	s_waitcnt vmcnt(17)
	s_waitcnt vmcnt(16)
	ds_read_b32 v66, v187
	s_waitcnt lgkmcnt(0)
	v_pk_fma_f32 v[68:69], v[66:67], v[86:87], 0 op_sel_hi:[0,1,0] neg_lo:[1,0,0] neg_hi:[1,0,0]
	v_pk_fma_f32 v[66:67], v[66:67], v[88:89], 0 op_sel_hi:[0,1,0] neg_lo:[1,0,0] neg_hi:[1,0,0]
	v_cvt_pk_bf16_f32 v68, v68, v69
	v_cvt_pk_bf16_f32 v69, v66, v67
	ds_write_b64 v186, v[68:69]
	ds_read_b32 v66, v187 offset:8
	s_waitcnt lgkmcnt(0)
	v_pk_fma_f32 v[68:69], v[66:67], v[82:83], 0 op_sel_hi:[0,1,0] neg_lo:[1,0,0] neg_hi:[1,0,0]
	v_pk_fma_f32 v[66:67], v[66:67], v[84:85], 0 op_sel_hi:[0,1,0] neg_lo:[1,0,0] neg_hi:[1,0,0]
	v_cvt_pk_bf16_f32 v68, v68, v69
	v_cvt_pk_bf16_f32 v69, v66, v67
	ds_write_b64 v186, v[68:69] offset:544
	ds_read_b32 v66, v187 offset:16
	s_waitcnt lgkmcnt(0)
	v_pk_fma_f32 v[68:69], v[66:67], v[78:79], 0 op_sel_hi:[0,1,0] neg_lo:[1,0,0] neg_hi:[1,0,0]
	v_pk_fma_f32 v[66:67], v[66:67], v[80:81], 0 op_sel_hi:[0,1,0] neg_lo:[1,0,0] neg_hi:[1,0,0]
	v_cvt_pk_bf16_f32 v68, v68, v69
	v_cvt_pk_bf16_f32 v69, v66, v67
	ds_write_b64 v186, v[68:69] offset:1088
	ds_read_b32 v66, v187 offset:24
	s_waitcnt lgkmcnt(0)
	v_pk_fma_f32 v[58:59], v[66:67], v[58:59], 0 op_sel_hi:[0,1,0] neg_lo:[1,0,0] neg_hi:[1,0,0]
	v_pk_fma_f32 v[60:61], v[66:67], v[60:61], 0 op_sel_hi:[0,1,0] neg_lo:[1,0,0] neg_hi:[1,0,0]
	v_cvt_pk_bf16_f32 v58, v58, v59
	v_cvt_pk_bf16_f32 v59, v60, v61
	ds_write_b64 v186, v[58:59] offset:1632
	ds_read_b32 v58, v187 offset:32
	s_waitcnt lgkmcnt(0)
	v_pk_fma_f32 v[46:47], v[58:59], v[46:47], 0 op_sel_hi:[0,1,0] neg_lo:[1,0,0] neg_hi:[1,0,0]
	v_pk_fma_f32 v[48:49], v[58:59], v[48:49], 0 op_sel_hi:[0,1,0] neg_lo:[1,0,0] neg_hi:[1,0,0]
	v_cvt_pk_bf16_f32 v46, v46, v47
	v_cvt_pk_bf16_f32 v47, v48, v49
	ds_write_b64 v186, v[46:47] offset:2176
	ds_read_b32 v46, v187 offset:40
	s_waitcnt lgkmcnt(0)
	v_pk_fma_f32 v[42:43], v[46:47], v[42:43], 0 op_sel_hi:[0,1,0] neg_lo:[1,0,0] neg_hi:[1,0,0]
	v_pk_fma_f32 v[44:45], v[46:47], v[44:45], 0 op_sel_hi:[0,1,0] neg_lo:[1,0,0] neg_hi:[1,0,0]
	v_cvt_pk_bf16_f32 v42, v42, v43
	v_cvt_pk_bf16_f32 v43, v44, v45
	ds_write_b64 v186, v[42:43] offset:2720
	ds_read_b32 v42, v187 offset:48
	s_waitcnt lgkmcnt(0)
	v_pk_fma_f32 v[30:31], v[42:43], v[30:31], 0 op_sel_hi:[0,1,0] neg_lo:[1,0,0] neg_hi:[1,0,0]
	v_pk_fma_f32 v[32:33], v[42:43], v[32:33], 0 op_sel_hi:[0,1,0] neg_lo:[1,0,0] neg_hi:[1,0,0]
	v_cvt_pk_bf16_f32 v30, v30, v31
	v_cvt_pk_bf16_f32 v31, v32, v33
	ds_write_b64 v186, v[30:31] offset:3264
	ds_read_b32 v30, v187 offset:56
	s_waitcnt lgkmcnt(0)
	v_pk_fma_f32 v[26:27], v[30:31], v[26:27], 0 op_sel_hi:[0,1,0] neg_lo:[1,0,0] neg_hi:[1,0,0]
	v_pk_fma_f32 v[28:29], v[30:31], v[28:29], 0 op_sel_hi:[0,1,0] neg_lo:[1,0,0] neg_hi:[1,0,0]
	v_cvt_pk_bf16_f32 v26, v26, v27
	v_cvt_pk_bf16_f32 v27, v28, v29
	ds_write_b64 v186, v[26:27] offset:3808
	ds_read_b128 a[96:99], v1
	ds_read_b128 a[100:103], v1 offset:64
	ds_read_b128 a[104:107], v1 offset:128
	ds_read_b128 a[108:111], v1 offset:192
	v_lshl_add_u64 v[26:27], v[130:131], 0, s[24:25]
	v_add_co_u32_e32 v28, vcc, s7, v26
	s_nop 1
	v_addc_co_u32_e32 v29, vcc, 0, v27, vcc
	global_load_dwordx4 v[102:105], v[26:27], off nt
	global_load_dwordx4 v[90:93], v[28:29], off nt
	v_add_co_u32_e32 v28, vcc, s36, v26
	s_nop 1
	v_addc_co_u32_e32 v29, vcc, 0, v27, vcc
	v_add_co_u32_e32 v30, vcc, s37, v26
	s_nop 1
	v_addc_co_u32_e32 v31, vcc, 0, v27, vcc
	global_load_dwordx4 v[86:89], v[28:29], off nt
	global_load_dwordx4 v[70:73], v[30:31], off nt
	v_add_co_u32_e32 v28, vcc, s38, v26
	s_nop 1
	v_addc_co_u32_e32 v29, vcc, 0, v27, vcc
	v_add_co_u32_e32 v30, vcc, s39, v26
	s_nop 1
	v_addc_co_u32_e32 v31, vcc, 0, v27, vcc
	global_load_dwordx4 v[66:69], v[28:29], off nt
	global_load_dwordx4 v[46:49], v[30:31], off nt
	v_add_co_u32_e32 v28, vcc, s41, v26
	s_nop 1
	v_addc_co_u32_e32 v29, vcc, 0, v27, vcc
	v_add_co_u32_e32 v26, vcc, s42, v26
	s_nop 1
	v_addc_co_u32_e32 v27, vcc, 0, v27, vcc
	global_load_dwordx4 v[42:45], v[28:29], off nt
	global_load_dwordx4 v[30:33], v[26:27], off nt
	v_mov_b32_e32 v26, v196
	s_waitcnt vmcnt(23)
	s_waitcnt vmcnt(22)
	s_waitcnt vmcnt(21)
	s_waitcnt vmcnt(20)
	s_waitcnt vmcnt(19)
	s_waitcnt vmcnt(18)
	s_waitcnt vmcnt(17)
	s_waitcnt vmcnt(16)
	ds_read_b32 v26, v187 offset:64
	s_waitcnt lgkmcnt(0)
	v_pk_fma_f32 v[28:29], v[26:27], v[110:111], 0 op_sel_hi:[0,1,0] neg_lo:[1,0,0] neg_hi:[1,0,0]
	v_pk_fma_f32 v[26:27], v[26:27], v[112:113], 0 op_sel_hi:[0,1,0] neg_lo:[1,0,0] neg_hi:[1,0,0]
	v_cvt_pk_bf16_f32 v28, v28, v29
	v_cvt_pk_bf16_f32 v29, v26, v27
	ds_write_b64 v186, v[28:29]
	ds_read_b32 v26, v187 offset:72
	s_waitcnt lgkmcnt(0)
	v_pk_fma_f32 v[28:29], v[26:27], v[98:99], 0 op_sel_hi:[0,1,0] neg_lo:[1,0,0] neg_hi:[1,0,0]
	v_pk_fma_f32 v[26:27], v[26:27], v[100:101], 0 op_sel_hi:[0,1,0] neg_lo:[1,0,0] neg_hi:[1,0,0]
	v_cvt_pk_bf16_f32 v28, v28, v29
	v_cvt_pk_bf16_f32 v29, v26, v27
	ds_write_b64 v186, v[28:29] offset:544
	ds_read_b32 v26, v187 offset:80
	s_waitcnt lgkmcnt(0)
	v_pk_fma_f32 v[28:29], v[26:27], v[62:63], 0 op_sel_hi:[0,1,0] neg_lo:[1,0,0] neg_hi:[1,0,0]
	v_pk_fma_f32 v[26:27], v[26:27], v[64:65], 0 op_sel_hi:[0,1,0] neg_lo:[1,0,0] neg_hi:[1,0,0]
	v_cvt_pk_bf16_f32 v28, v28, v29
	v_cvt_pk_bf16_f32 v29, v26, v27
	ds_write_b64 v186, v[28:29] offset:1088
	ds_read_b32 v26, v187 offset:88
	s_waitcnt lgkmcnt(0)
	v_pk_fma_f32 v[28:29], v[26:27], v[50:51], 0 op_sel_hi:[0,1,0] neg_lo:[1,0,0] neg_hi:[1,0,0]
	v_pk_fma_f32 v[26:27], v[26:27], v[52:53], 0 op_sel_hi:[0,1,0] neg_lo:[1,0,0] neg_hi:[1,0,0]
	v_cvt_pk_bf16_f32 v28, v28, v29
	v_cvt_pk_bf16_f32 v29, v26, v27
	ds_write_b64 v186, v[28:29] offset:1632
	ds_read_b32 v26, v187 offset:96
	s_waitcnt lgkmcnt(0)
	v_pk_fma_f32 v[28:29], v[26:27], v[34:35], 0 op_sel_hi:[0,1,0] neg_lo:[1,0,0] neg_hi:[1,0,0]
	v_pk_fma_f32 v[26:27], v[26:27], v[36:37], 0 op_sel_hi:[0,1,0] neg_lo:[1,0,0] neg_hi:[1,0,0]
	v_cvt_pk_bf16_f32 v28, v28, v29
	v_cvt_pk_bf16_f32 v29, v26, v27
	ds_write_b64 v186, v[28:29] offset:2176
	ds_read_b32 v26, v187 offset:104
	s_waitcnt lgkmcnt(0)
	v_pk_fma_f32 v[22:23], v[26:27], v[22:23], 0 op_sel_hi:[0,1,0] neg_lo:[1,0,0] neg_hi:[1,0,0]
	v_pk_fma_f32 v[24:25], v[26:27], v[24:25], 0 op_sel_hi:[0,1,0] neg_lo:[1,0,0] neg_hi:[1,0,0]
	v_cvt_pk_bf16_f32 v22, v22, v23
	v_cvt_pk_bf16_f32 v23, v24, v25
	ds_write_b64 v186, v[22:23] offset:2720
	ds_read_b32 v22, v187 offset:112
	s_waitcnt lgkmcnt(0)
	v_pk_fma_f32 v[14:15], v[22:23], v[14:15], 0 op_sel_hi:[0,1,0] neg_lo:[1,0,0] neg_hi:[1,0,0]
	v_pk_fma_f32 v[16:17], v[22:23], v[16:17], 0 op_sel_hi:[0,1,0] neg_lo:[1,0,0] neg_hi:[1,0,0]
	v_cvt_pk_bf16_f32 v14, v14, v15
	v_cvt_pk_bf16_f32 v15, v16, v17
	ds_write_b64 v186, v[14:15] offset:3264
	ds_read_b32 v14, v187 offset:120
	s_waitcnt lgkmcnt(0)
	v_pk_fma_f32 v[6:7], v[14:15], v[6:7], 0 op_sel_hi:[0,1,0] neg_lo:[1,0,0] neg_hi:[1,0,0]
	v_pk_fma_f32 v[8:9], v[14:15], v[8:9], 0 op_sel_hi:[0,1,0] neg_lo:[1,0,0] neg_hi:[1,0,0]
	v_cvt_pk_bf16_f32 v6, v6, v7
	v_cvt_pk_bf16_f32 v7, v8, v9
	ds_write_b64 v186, v[6:7] offset:3808
	ds_read_b128 a[112:115], v1
	ds_read_b128 a[116:119], v1 offset:64
	ds_read_b128 a[120:123], v1 offset:128
	ds_read_b128 a[124:127], v1 offset:192
	v_lshl_add_u64 v[6:7], v[150:151], 0, s[24:25]
	v_lshl_add_u64 v[8:9], v[152:153], 0, s[24:25]
	v_lshl_add_u64 v[14:15], v[156:157], 0, s[24:25]
	v_lshl_add_u64 v[16:17], v[158:159], 0, s[24:25]
	v_lshl_add_u64 v[22:23], v[160:161], 0, s[24:25]
	v_lshl_add_u64 v[24:25], v[162:163], 0, s[24:25]
	v_lshl_add_u64 v[26:27], v[164:165], 0, s[24:25]
	v_lshl_add_u64 v[28:29], v[166:167], 0, s[24:25]
	global_load_dwordx4 v[110:113], v[6:7], off nt
	global_load_dwordx4 v[98:101], v[8:9], off nt
	global_load_dwordx4 v[78:81], v[14:15], off nt
	global_load_dwordx4 v[58:61], v[16:17], off nt
	global_load_dwordx4 v[34:37], v[22:23], off nt
	s_nop 0
	global_load_dwordx4 v[22:25], v[24:25], off nt
	s_nop 0
	global_load_dwordx4 v[14:17], v[26:27], off nt
	global_load_dwordx4 v[6:9], v[28:29], off nt
	s_waitcnt vmcnt(23)
	s_waitcnt vmcnt(22)
	s_waitcnt vmcnt(21)
	s_waitcnt vmcnt(20)
	s_waitcnt vmcnt(19)
	s_waitcnt vmcnt(18)
	s_waitcnt vmcnt(17)
	s_waitcnt vmcnt(16)
	ds_read_b32 v26, v187 offset:128
	s_waitcnt lgkmcnt(0)
	v_pk_fma_f32 v[28:29], v[26:27], v[106:107], 0 op_sel_hi:[0,1,0] neg_lo:[1,0,0] neg_hi:[1,0,0]
	v_pk_fma_f32 v[26:27], v[26:27], v[108:109], 0 op_sel_hi:[0,1,0] neg_lo:[1,0,0] neg_hi:[1,0,0]
	v_cvt_pk_bf16_f32 v28, v28, v29
	v_cvt_pk_bf16_f32 v29, v26, v27
	ds_write_b64 v186, v[28:29]
	ds_read_b32 v26, v187 offset:136
	s_waitcnt lgkmcnt(0)
	v_pk_fma_f32 v[28:29], v[26:27], v[94:95], 0 op_sel_hi:[0,1,0] neg_lo:[1,0,0] neg_hi:[1,0,0]
	v_pk_fma_f32 v[26:27], v[26:27], v[96:97], 0 op_sel_hi:[0,1,0] neg_lo:[1,0,0] neg_hi:[1,0,0]
	v_cvt_pk_bf16_f32 v28, v28, v29
	v_cvt_pk_bf16_f32 v29, v26, v27
	ds_write_b64 v186, v[28:29] offset:544
	ds_read_b32 v26, v187 offset:144
	s_waitcnt lgkmcnt(0)
	v_pk_fma_f32 v[28:29], v[26:27], v[74:75], 0 op_sel_hi:[0,1,0] neg_lo:[1,0,0] neg_hi:[1,0,0]
	v_pk_fma_f32 v[26:27], v[26:27], v[76:77], 0 op_sel_hi:[0,1,0] neg_lo:[1,0,0] neg_hi:[1,0,0]
	v_cvt_pk_bf16_f32 v28, v28, v29
	v_cvt_pk_bf16_f32 v29, v26, v27
	ds_write_b64 v186, v[28:29] offset:1088
	ds_read_b32 v26, v187 offset:152
	s_waitcnt lgkmcnt(0)
	v_pk_fma_f32 v[28:29], v[26:27], v[54:55], 0 op_sel_hi:[0,1,0] neg_lo:[1,0,0] neg_hi:[1,0,0]
	v_pk_fma_f32 v[26:27], v[26:27], v[56:57], 0 op_sel_hi:[0,1,0] neg_lo:[1,0,0] neg_hi:[1,0,0]
	v_cvt_pk_bf16_f32 v28, v28, v29
	v_cvt_pk_bf16_f32 v29, v26, v27
	ds_write_b64 v186, v[28:29] offset:1632
	ds_read_b32 v26, v187 offset:160
	s_waitcnt lgkmcnt(0)
	v_pk_fma_f32 v[28:29], v[26:27], v[38:39], 0 op_sel_hi:[0,1,0] neg_lo:[1,0,0] neg_hi:[1,0,0]
	v_pk_fma_f32 v[26:27], v[26:27], v[40:41], 0 op_sel_hi:[0,1,0] neg_lo:[1,0,0] neg_hi:[1,0,0]
	v_cvt_pk_bf16_f32 v28, v28, v29
	v_cvt_pk_bf16_f32 v29, v26, v27
	ds_write_b64 v186, v[28:29] offset:2176
	ds_read_b32 v26, v187 offset:168
	s_waitcnt lgkmcnt(0)
	v_pk_fma_f32 v[18:19], v[26:27], v[18:19], 0 op_sel_hi:[0,1,0] neg_lo:[1,0,0] neg_hi:[1,0,0]
	v_pk_fma_f32 v[20:21], v[26:27], v[20:21], 0 op_sel_hi:[0,1,0] neg_lo:[1,0,0] neg_hi:[1,0,0]
	v_cvt_pk_bf16_f32 v18, v18, v19
	v_cvt_pk_bf16_f32 v19, v20, v21
	ds_write_b64 v186, v[18:19] offset:2720
	ds_read_b32 v18, v187 offset:176
	s_waitcnt lgkmcnt(0)
	v_pk_fma_f32 v[10:11], v[18:19], v[10:11], 0 op_sel_hi:[0,1,0] neg_lo:[1,0,0] neg_hi:[1,0,0]
	v_pk_fma_f32 v[12:13], v[18:19], v[12:13], 0 op_sel_hi:[0,1,0] neg_lo:[1,0,0] neg_hi:[1,0,0]
	v_cvt_pk_bf16_f32 v10, v10, v11
	v_cvt_pk_bf16_f32 v11, v12, v13
	ds_write_b64 v186, v[10:11] offset:3264
	ds_read_b32 v10, v187 offset:184
	s_waitcnt lgkmcnt(0)
	v_pk_fma_f32 v[2:3], v[10:11], v[2:3], 0 op_sel_hi:[0,1,0] neg_lo:[1,0,0] neg_hi:[1,0,0]
	v_pk_fma_f32 v[4:5], v[10:11], v[4:5], 0 op_sel_hi:[0,1,0] neg_lo:[1,0,0] neg_hi:[1,0,0]
	v_cvt_pk_bf16_f32 v2, v2, v3
	v_cvt_pk_bf16_f32 v3, v4, v5
	ds_write_b64 v186, v[2:3] offset:3808
	ds_read_b128 a[128:131], v1
	ds_read_b128 a[132:135], v1 offset:64
	ds_read_b128 a[136:139], v1 offset:128
	ds_read_b128 a[140:143], v1 offset:192
	v_lshl_add_u64 v[2:3], v[168:169], 0, s[24:25]
	v_lshl_add_u64 v[4:5], v[170:171], 0, s[24:25]
	v_lshl_add_u64 v[10:11], v[172:173], 0, s[24:25]
	v_lshl_add_u64 v[12:13], v[174:175], 0, s[24:25]
	v_lshl_add_u64 v[18:19], v[176:177], 0, s[24:25]
	v_lshl_add_u64 v[20:21], v[178:179], 0, s[24:25]
	v_lshl_add_u64 v[50:51], v[180:181], 0, s[24:25]
	v_lshl_add_u64 v[52:53], v[182:183], 0, s[24:25]
	global_load_dwordx4 v[114:117], v[2:3], off nt
	global_load_dwordx4 v[94:97], v[4:5], off nt
	global_load_dwordx4 v[82:85], v[10:11], off nt
	global_load_dwordx4 v[62:65], v[12:13], off nt
	global_load_dwordx4 v[38:41], v[18:19], off nt
	global_load_dwordx4 v[26:29], v[20:21], off nt
	s_nop 0
	global_load_dwordx4 v[10:13], v[50:51], off nt
	global_load_dwordx4 v[2:5], v[52:53], off nt
	v_mov_b32_e32 v18, v195
	s_waitcnt vmcnt(23)
	s_waitcnt vmcnt(22)
	s_waitcnt vmcnt(21)
	s_waitcnt vmcnt(20)
	s_waitcnt vmcnt(19)
	s_waitcnt vmcnt(18)
	s_waitcnt vmcnt(17)
	s_waitcnt vmcnt(16)
	ds_read_b32 v18, v187
	s_waitcnt lgkmcnt(0)
	v_pk_fma_f32 v[20:21], v[18:19], v[102:103], 0 op_sel_hi:[0,1,0] neg_lo:[1,0,0] neg_hi:[1,0,0]
	v_pk_fma_f32 v[18:19], v[18:19], v[104:105], 0 op_sel_hi:[0,1,0] neg_lo:[1,0,0] neg_hi:[1,0,0]
	v_cvt_pk_bf16_f32 v20, v20, v21
	v_cvt_pk_bf16_f32 v21, v18, v19
	ds_write_b64 v186, v[20:21]
	ds_read_b32 v18, v187 offset:8
	s_waitcnt lgkmcnt(0)
	v_pk_fma_f32 v[20:21], v[18:19], v[90:91], 0 op_sel_hi:[0,1,0] neg_lo:[1,0,0] neg_hi:[1,0,0]
	v_pk_fma_f32 v[18:19], v[18:19], v[92:93], 0 op_sel_hi:[0,1,0] neg_lo:[1,0,0] neg_hi:[1,0,0]
	v_cvt_pk_bf16_f32 v20, v20, v21
	v_cvt_pk_bf16_f32 v21, v18, v19
	ds_write_b64 v186, v[20:21] offset:544
	ds_read_b32 v18, v187 offset:16
	s_waitcnt lgkmcnt(0)
	v_pk_fma_f32 v[20:21], v[18:19], v[86:87], 0 op_sel_hi:[0,1,0] neg_lo:[1,0,0] neg_hi:[1,0,0]
	v_pk_fma_f32 v[18:19], v[18:19], v[88:89], 0 op_sel_hi:[0,1,0] neg_lo:[1,0,0] neg_hi:[1,0,0]
	v_cvt_pk_bf16_f32 v20, v20, v21
	v_cvt_pk_bf16_f32 v21, v18, v19
	ds_write_b64 v186, v[20:21] offset:1088
	ds_read_b32 v18, v187 offset:24
	s_waitcnt lgkmcnt(0)
	v_pk_fma_f32 v[20:21], v[18:19], v[70:71], 0 op_sel_hi:[0,1,0] neg_lo:[1,0,0] neg_hi:[1,0,0]
	v_pk_fma_f32 v[18:19], v[18:19], v[72:73], 0 op_sel_hi:[0,1,0] neg_lo:[1,0,0] neg_hi:[1,0,0]
	v_cvt_pk_bf16_f32 v20, v20, v21
	v_cvt_pk_bf16_f32 v21, v18, v19
	ds_write_b64 v186, v[20:21] offset:1632
	ds_read_b32 v18, v187 offset:32
	s_waitcnt lgkmcnt(0)
	v_pk_fma_f32 v[20:21], v[18:19], v[66:67], 0 op_sel_hi:[0,1,0] neg_lo:[1,0,0] neg_hi:[1,0,0]
	v_pk_fma_f32 v[18:19], v[18:19], v[68:69], 0 op_sel_hi:[0,1,0] neg_lo:[1,0,0] neg_hi:[1,0,0]
	v_cvt_pk_bf16_f32 v20, v20, v21
	v_cvt_pk_bf16_f32 v21, v18, v19
	ds_write_b64 v186, v[20:21] offset:2176
	ds_read_b32 v18, v187 offset:40
	s_waitcnt lgkmcnt(0)
	v_pk_fma_f32 v[20:21], v[18:19], v[46:47], 0 op_sel_hi:[0,1,0] neg_lo:[1,0,0] neg_hi:[1,0,0]
	v_pk_fma_f32 v[18:19], v[18:19], v[48:49], 0 op_sel_hi:[0,1,0] neg_lo:[1,0,0] neg_hi:[1,0,0]
	v_cvt_pk_bf16_f32 v20, v20, v21
	v_cvt_pk_bf16_f32 v21, v18, v19
	ds_write_b64 v186, v[20:21] offset:2720
	ds_read_b32 v18, v187 offset:48
	s_waitcnt lgkmcnt(0)
	v_pk_fma_f32 v[20:21], v[18:19], v[42:43], 0 op_sel_hi:[0,1,0] neg_lo:[1,0,0] neg_hi:[1,0,0]
	v_pk_fma_f32 v[18:19], v[18:19], v[44:45], 0 op_sel_hi:[0,1,0] neg_lo:[1,0,0] neg_hi:[1,0,0]
	v_cvt_pk_bf16_f32 v20, v20, v21
	v_cvt_pk_bf16_f32 v21, v18, v19
	ds_write_b64 v186, v[20:21] offset:3264
	ds_read_b32 v18, v187 offset:56
	s_waitcnt lgkmcnt(0)
	v_pk_fma_f32 v[20:21], v[18:19], v[30:31], 0 op_sel_hi:[0,1,0] neg_lo:[1,0,0] neg_hi:[1,0,0]
	v_pk_fma_f32 v[18:19], v[18:19], v[32:33], 0 op_sel_hi:[0,1,0] neg_lo:[1,0,0] neg_hi:[1,0,0]
	v_cvt_pk_bf16_f32 v20, v20, v21
	v_cvt_pk_bf16_f32 v21, v18, v19
	ds_write_b64 v186, v[20:21] offset:3808
	ds_read_b128 a[144:147], v1
	ds_read_b128 a[148:151], v1 offset:64
	ds_read_b128 a[152:155], v1 offset:128
	ds_read_b128 a[156:159], v1 offset:192
	v_lshl_add_u64 v[18:19], v[130:131], 0, s[22:23]
	v_add_co_u32_e32 v20, vcc, s7, v18
	s_nop 1
	v_addc_co_u32_e32 v21, vcc, 0, v19, vcc
	global_load_dwordx4 v[106:109], v[18:19], off nt
	global_load_dwordx4 v[90:93], v[20:21], off nt
	v_add_co_u32_e32 v20, vcc, s36, v18
	s_nop 1
	v_addc_co_u32_e32 v21, vcc, 0, v19, vcc
	v_add_co_u32_e32 v30, vcc, s37, v18
	s_nop 1
	v_addc_co_u32_e32 v31, vcc, 0, v19, vcc
	global_load_dwordx4 v[86:89], v[20:21], off nt
	global_load_dwordx4 v[74:77], v[30:31], off nt
	v_add_co_u32_e32 v20, vcc, s38, v18
	s_nop 1
	v_addc_co_u32_e32 v21, vcc, 0, v19, vcc
	v_add_co_u32_e32 v30, vcc, s39, v18
	s_nop 1
	v_addc_co_u32_e32 v31, vcc, 0, v19, vcc
	global_load_dwordx4 v[70:73], v[20:21], off nt
	global_load_dwordx4 v[54:57], v[30:31], off nt
	v_add_co_u32_e32 v20, vcc, s41, v18
	s_nop 1
	v_addc_co_u32_e32 v21, vcc, 0, v19, vcc
	v_add_co_u32_e32 v18, vcc, s42, v18
	s_nop 1
	v_addc_co_u32_e32 v19, vcc, 0, v19, vcc
	global_load_dwordx4 v[50:53], v[20:21], off nt
	global_load_dwordx4 v[46:49], v[18:19], off nt
	v_mov_b32_e32 v18, v195
	s_waitcnt vmcnt(23)
	s_waitcnt vmcnt(22)
	s_waitcnt vmcnt(21)
	s_waitcnt vmcnt(20)
	s_waitcnt vmcnt(19)
	s_waitcnt vmcnt(18)
	s_waitcnt vmcnt(17)
	s_waitcnt vmcnt(16)
	ds_read_b32 v18, v187 offset:64
	s_waitcnt lgkmcnt(0)
	v_pk_fma_f32 v[20:21], v[18:19], v[110:111], 0 op_sel_hi:[0,1,0] neg_lo:[1,0,0] neg_hi:[1,0,0]
	v_pk_fma_f32 v[18:19], v[18:19], v[112:113], 0 op_sel_hi:[0,1,0] neg_lo:[1,0,0] neg_hi:[1,0,0]
	v_cvt_pk_bf16_f32 v20, v20, v21
	v_cvt_pk_bf16_f32 v21, v18, v19
	ds_write_b64 v186, v[20:21]
	ds_read_b32 v18, v187 offset:72
	s_waitcnt lgkmcnt(0)
	v_pk_fma_f32 v[20:21], v[18:19], v[98:99], 0 op_sel_hi:[0,1,0] neg_lo:[1,0,0] neg_hi:[1,0,0]
	v_pk_fma_f32 v[18:19], v[18:19], v[100:101], 0 op_sel_hi:[0,1,0] neg_lo:[1,0,0] neg_hi:[1,0,0]
	v_cvt_pk_bf16_f32 v20, v20, v21
	v_cvt_pk_bf16_f32 v21, v18, v19
	ds_write_b64 v186, v[20:21] offset:544
	ds_read_b32 v18, v187 offset:80
	s_waitcnt lgkmcnt(0)
	v_pk_fma_f32 v[20:21], v[18:19], v[78:79], 0 op_sel_hi:[0,1,0] neg_lo:[1,0,0] neg_hi:[1,0,0]
	v_pk_fma_f32 v[18:19], v[18:19], v[80:81], 0 op_sel_hi:[0,1,0] neg_lo:[1,0,0] neg_hi:[1,0,0]
	v_cvt_pk_bf16_f32 v20, v20, v21
	v_cvt_pk_bf16_f32 v21, v18, v19
	ds_write_b64 v186, v[20:21] offset:1088
	ds_read_b32 v18, v187 offset:88
	s_waitcnt lgkmcnt(0)
	v_pk_fma_f32 v[20:21], v[18:19], v[58:59], 0 op_sel_hi:[0,1,0] neg_lo:[1,0,0] neg_hi:[1,0,0]
	v_pk_fma_f32 v[18:19], v[18:19], v[60:61], 0 op_sel_hi:[0,1,0] neg_lo:[1,0,0] neg_hi:[1,0,0]
	v_cvt_pk_bf16_f32 v20, v20, v21
	v_cvt_pk_bf16_f32 v21, v18, v19
	ds_write_b64 v186, v[20:21] offset:1632
	ds_read_b32 v18, v187 offset:96
	s_waitcnt lgkmcnt(0)
	v_pk_fma_f32 v[20:21], v[18:19], v[34:35], 0 op_sel_hi:[0,1,0] neg_lo:[1,0,0] neg_hi:[1,0,0]
	v_pk_fma_f32 v[18:19], v[18:19], v[36:37], 0 op_sel_hi:[0,1,0] neg_lo:[1,0,0] neg_hi:[1,0,0]
	v_cvt_pk_bf16_f32 v20, v20, v21
	v_cvt_pk_bf16_f32 v21, v18, v19
	ds_write_b64 v186, v[20:21] offset:2176
	ds_read_b32 v18, v187 offset:104
	s_waitcnt lgkmcnt(0)
	v_pk_fma_f32 v[20:21], v[18:19], v[22:23], 0 op_sel_hi:[0,1,0] neg_lo:[1,0,0] neg_hi:[1,0,0]
	v_pk_fma_f32 v[18:19], v[18:19], v[24:25], 0 op_sel_hi:[0,1,0] neg_lo:[1,0,0] neg_hi:[1,0,0]
	v_cvt_pk_bf16_f32 v20, v20, v21
	v_cvt_pk_bf16_f32 v21, v18, v19
	ds_write_b64 v186, v[20:21] offset:2720
	ds_read_b32 v18, v187 offset:112
	s_waitcnt lgkmcnt(0)
	v_pk_fma_f32 v[14:15], v[18:19], v[14:15], 0 op_sel_hi:[0,1,0] neg_lo:[1,0,0] neg_hi:[1,0,0]
	v_pk_fma_f32 v[16:17], v[18:19], v[16:17], 0 op_sel_hi:[0,1,0] neg_lo:[1,0,0] neg_hi:[1,0,0]
	v_cvt_pk_bf16_f32 v14, v14, v15
	v_cvt_pk_bf16_f32 v15, v16, v17
	ds_write_b64 v186, v[14:15] offset:3264
	ds_read_b32 v14, v187 offset:120
	s_waitcnt lgkmcnt(0)
	v_pk_fma_f32 v[6:7], v[14:15], v[6:7], 0 op_sel_hi:[0,1,0] neg_lo:[1,0,0] neg_hi:[1,0,0]
	v_pk_fma_f32 v[8:9], v[14:15], v[8:9], 0 op_sel_hi:[0,1,0] neg_lo:[1,0,0] neg_hi:[1,0,0]
	v_cvt_pk_bf16_f32 v6, v6, v7
	v_cvt_pk_bf16_f32 v7, v8, v9
	ds_write_b64 v186, v[6:7] offset:3808
	ds_read_b128 a[160:163], v1
	ds_read_b128 a[164:167], v1 offset:64
	ds_read_b128 a[168:171], v1 offset:128
	ds_read_b128 a[172:175], v1 offset:192
	v_lshl_add_u64 v[6:7], v[150:151], 0, s[22:23]
	v_lshl_add_u64 v[18:19], v[160:161], 0, s[22:23]
	v_lshl_add_u64 v[20:21], v[162:163], 0, s[22:23]
	v_lshl_add_u64 v[22:23], v[164:165], 0, s[22:23]
	v_lshl_add_u64 v[8:9], v[152:153], 0, s[22:23]
	v_lshl_add_u64 v[14:15], v[156:157], 0, s[22:23]
	v_lshl_add_u64 v[16:17], v[158:159], 0, s[22:23]
	v_lshl_add_u64 v[34:35], v[166:167], 0, s[22:23]
	global_load_dwordx4 v[110:113], v[6:7], off nt
	global_load_dwordx4 v[98:101], v[8:9], off nt
	global_load_dwordx4 v[78:81], v[14:15], off nt
	global_load_dwordx4 v[66:69], v[16:17], off nt
	global_load_dwordx4 v[58:61], v[18:19], off nt
	global_load_dwordx4 v[30:33], v[20:21], off nt
	s_nop 0
	global_load_dwordx4 v[22:25], v[22:23], off nt
	s_nop 0
	global_load_dwordx4 v[18:21], v[34:35], off nt
	s_waitcnt vmcnt(23)
	s_waitcnt vmcnt(22)
	s_waitcnt vmcnt(21)
	s_waitcnt vmcnt(20)
	s_waitcnt vmcnt(19)
	s_waitcnt vmcnt(18)
	s_waitcnt vmcnt(17)
	s_waitcnt vmcnt(16)
	ds_read_b32 v6, v187 offset:128
	s_waitcnt lgkmcnt(0)
	v_pk_fma_f32 v[8:9], v[6:7], v[114:115], 0 op_sel_hi:[0,1,0] neg_lo:[1,0,0] neg_hi:[1,0,0]
	v_pk_fma_f32 v[6:7], v[6:7], v[116:117], 0 op_sel_hi:[0,1,0] neg_lo:[1,0,0] neg_hi:[1,0,0]
	v_cvt_pk_bf16_f32 v8, v8, v9
	v_cvt_pk_bf16_f32 v9, v6, v7
	ds_write_b64 v186, v[8:9]
	ds_read_b32 v6, v187 offset:136
	s_waitcnt lgkmcnt(0)
	v_pk_fma_f32 v[8:9], v[6:7], v[94:95], 0 op_sel_hi:[0,1,0] neg_lo:[1,0,0] neg_hi:[1,0,0]
	v_pk_fma_f32 v[6:7], v[6:7], v[96:97], 0 op_sel_hi:[0,1,0] neg_lo:[1,0,0] neg_hi:[1,0,0]
	v_cvt_pk_bf16_f32 v8, v8, v9
	v_cvt_pk_bf16_f32 v9, v6, v7
	ds_write_b64 v186, v[8:9] offset:544
	ds_read_b32 v6, v187 offset:144
	s_waitcnt lgkmcnt(0)
	v_pk_fma_f32 v[8:9], v[6:7], v[82:83], 0 op_sel_hi:[0,1,0] neg_lo:[1,0,0] neg_hi:[1,0,0]
	v_pk_fma_f32 v[6:7], v[6:7], v[84:85], 0 op_sel_hi:[0,1,0] neg_lo:[1,0,0] neg_hi:[1,0,0]
	v_cvt_pk_bf16_f32 v8, v8, v9
	v_cvt_pk_bf16_f32 v9, v6, v7
	ds_write_b64 v186, v[8:9] offset:1088
	ds_read_b32 v6, v187 offset:152
	s_waitcnt lgkmcnt(0)
	v_pk_fma_f32 v[8:9], v[6:7], v[62:63], 0 op_sel_hi:[0,1,0] neg_lo:[1,0,0] neg_hi:[1,0,0]
	v_pk_fma_f32 v[6:7], v[6:7], v[64:65], 0 op_sel_hi:[0,1,0] neg_lo:[1,0,0] neg_hi:[1,0,0]
	v_cvt_pk_bf16_f32 v8, v8, v9
	v_cvt_pk_bf16_f32 v9, v6, v7
	ds_write_b64 v186, v[8:9] offset:1632
	ds_read_b32 v6, v187 offset:160
	s_waitcnt lgkmcnt(0)
	v_pk_fma_f32 v[8:9], v[6:7], v[38:39], 0 op_sel_hi:[0,1,0] neg_lo:[1,0,0] neg_hi:[1,0,0]
	v_pk_fma_f32 v[6:7], v[6:7], v[40:41], 0 op_sel_hi:[0,1,0] neg_lo:[1,0,0] neg_hi:[1,0,0]
	v_cvt_pk_bf16_f32 v8, v8, v9
	v_cvt_pk_bf16_f32 v9, v6, v7
	ds_write_b64 v186, v[8:9] offset:2176
	ds_read_b32 v6, v187 offset:168
	s_waitcnt lgkmcnt(0)
	v_pk_fma_f32 v[8:9], v[6:7], v[26:27], 0 op_sel_hi:[0,1,0] neg_lo:[1,0,0] neg_hi:[1,0,0]
	v_pk_fma_f32 v[6:7], v[6:7], v[28:29], 0 op_sel_hi:[0,1,0] neg_lo:[1,0,0] neg_hi:[1,0,0]
	v_cvt_pk_bf16_f32 v8, v8, v9
	v_cvt_pk_bf16_f32 v9, v6, v7
	ds_write_b64 v186, v[8:9] offset:2720
	ds_read_b32 v6, v187 offset:176
	s_waitcnt lgkmcnt(0)
	v_pk_fma_f32 v[8:9], v[6:7], v[10:11], 0 op_sel_hi:[0,1,0] neg_lo:[1,0,0] neg_hi:[1,0,0]
	v_pk_fma_f32 v[6:7], v[6:7], v[12:13], 0 op_sel_hi:[0,1,0] neg_lo:[1,0,0] neg_hi:[1,0,0]
	v_cvt_pk_bf16_f32 v8, v8, v9
	v_cvt_pk_bf16_f32 v9, v6, v7
	ds_write_b64 v186, v[8:9] offset:3264
	ds_read_b32 v6, v187 offset:184
	s_waitcnt lgkmcnt(0)
	v_pk_fma_f32 v[2:3], v[6:7], v[2:3], 0 op_sel_hi:[0,1,0] neg_lo:[1,0,0] neg_hi:[1,0,0]
	v_pk_fma_f32 v[4:5], v[6:7], v[4:5], 0 op_sel_hi:[0,1,0] neg_lo:[1,0,0] neg_hi:[1,0,0]
	v_cvt_pk_bf16_f32 v2, v2, v3
	v_cvt_pk_bf16_f32 v3, v4, v5
	ds_write_b64 v186, v[2:3] offset:3808
	ds_read_b128 a[176:179], v1
	ds_read_b128 a[180:183], v1 offset:64
	ds_read_b128 a[184:187], v1 offset:128
	ds_read_b128 a[188:191], v1 offset:192
	v_lshl_add_u64 v[2:3], v[168:169], 0, s[22:23]
	v_lshl_add_u64 v[4:5], v[170:171], 0, s[22:23]
	v_lshl_add_u64 v[6:7], v[172:173], 0, s[22:23]
	v_lshl_add_u64 v[8:9], v[174:175], 0, s[22:23]
	v_lshl_add_u64 v[10:11], v[176:177], 0, s[22:23]
	v_lshl_add_u64 v[12:13], v[178:179], 0, s[22:23]
	v_lshl_add_u64 v[14:15], v[180:181], 0, s[22:23]
	v_lshl_add_u64 v[16:17], v[182:183], 0, s[22:23]
	global_load_dwordx4 v[114:117], v[2:3], off nt
	global_load_dwordx4 v[102:105], v[4:5], off nt
	global_load_dwordx4 v[94:97], v[6:7], off nt
	global_load_dwordx4 v[82:85], v[8:9], off nt
	global_load_dwordx4 v[62:65], v[10:11], off nt
	global_load_dwordx4 v[42:45], v[12:13], off nt
	global_load_dwordx4 v[38:41], v[14:15], off nt
	global_load_dwordx4 v[34:37], v[16:17], off nt
	v_mov_b32_e32 v2, v194
	s_waitcnt vmcnt(23)
	s_waitcnt vmcnt(22)
	s_waitcnt vmcnt(21)
	s_waitcnt vmcnt(20)
	s_waitcnt vmcnt(19)
	s_waitcnt vmcnt(18)
	s_waitcnt vmcnt(17)
	s_waitcnt vmcnt(16)
	ds_read_b32 v2, v187
	s_waitcnt lgkmcnt(0)
	v_pk_fma_f32 v[4:5], v[2:3], v[106:107], 0 op_sel_hi:[0,1,0] neg_lo:[1,0,0] neg_hi:[1,0,0]
	v_pk_fma_f32 v[2:3], v[2:3], v[108:109], 0 op_sel_hi:[0,1,0] neg_lo:[1,0,0] neg_hi:[1,0,0]
	v_cvt_pk_bf16_f32 v4, v4, v5
	v_cvt_pk_bf16_f32 v5, v2, v3
	ds_write_b64 v186, v[4:5]
	ds_read_b32 v2, v187 offset:8
	s_waitcnt lgkmcnt(0)
	v_pk_fma_f32 v[4:5], v[2:3], v[90:91], 0 op_sel_hi:[0,1,0] neg_lo:[1,0,0] neg_hi:[1,0,0]
	v_pk_fma_f32 v[2:3], v[2:3], v[92:93], 0 op_sel_hi:[0,1,0] neg_lo:[1,0,0] neg_hi:[1,0,0]
	v_cvt_pk_bf16_f32 v4, v4, v5
	v_cvt_pk_bf16_f32 v5, v2, v3
	ds_write_b64 v186, v[4:5] offset:544
	ds_read_b32 v2, v187 offset:16
	s_waitcnt lgkmcnt(0)
	v_pk_fma_f32 v[4:5], v[2:3], v[86:87], 0 op_sel_hi:[0,1,0] neg_lo:[1,0,0] neg_hi:[1,0,0]
	v_pk_fma_f32 v[2:3], v[2:3], v[88:89], 0 op_sel_hi:[0,1,0] neg_lo:[1,0,0] neg_hi:[1,0,0]
	v_cvt_pk_bf16_f32 v4, v4, v5
	v_cvt_pk_bf16_f32 v5, v2, v3
	ds_write_b64 v186, v[4:5] offset:1088
	ds_read_b32 v2, v187 offset:24
	s_waitcnt lgkmcnt(0)
	v_pk_fma_f32 v[4:5], v[2:3], v[74:75], 0 op_sel_hi:[0,1,0] neg_lo:[1,0,0] neg_hi:[1,0,0]
	v_pk_fma_f32 v[2:3], v[2:3], v[76:77], 0 op_sel_hi:[0,1,0] neg_lo:[1,0,0] neg_hi:[1,0,0]
	v_cvt_pk_bf16_f32 v4, v4, v5
	v_cvt_pk_bf16_f32 v5, v2, v3
	ds_write_b64 v186, v[4:5] offset:1632
	ds_read_b32 v2, v187 offset:32
	s_waitcnt lgkmcnt(0)
	v_pk_fma_f32 v[4:5], v[2:3], v[70:71], 0 op_sel_hi:[0,1,0] neg_lo:[1,0,0] neg_hi:[1,0,0]
	v_pk_fma_f32 v[2:3], v[2:3], v[72:73], 0 op_sel_hi:[0,1,0] neg_lo:[1,0,0] neg_hi:[1,0,0]
	v_cvt_pk_bf16_f32 v4, v4, v5
	v_cvt_pk_bf16_f32 v5, v2, v3
	ds_write_b64 v186, v[4:5] offset:2176
	ds_read_b32 v2, v187 offset:40
	s_waitcnt lgkmcnt(0)
	v_pk_fma_f32 v[4:5], v[2:3], v[54:55], 0 op_sel_hi:[0,1,0] neg_lo:[1,0,0] neg_hi:[1,0,0]
	v_pk_fma_f32 v[2:3], v[2:3], v[56:57], 0 op_sel_hi:[0,1,0] neg_lo:[1,0,0] neg_hi:[1,0,0]
	v_cvt_pk_bf16_f32 v4, v4, v5
	v_cvt_pk_bf16_f32 v5, v2, v3
	ds_write_b64 v186, v[4:5] offset:2720
	ds_read_b32 v2, v187 offset:48
	s_waitcnt lgkmcnt(0)
	v_pk_fma_f32 v[4:5], v[2:3], v[50:51], 0 op_sel_hi:[0,1,0] neg_lo:[1,0,0] neg_hi:[1,0,0]
	v_pk_fma_f32 v[2:3], v[2:3], v[52:53], 0 op_sel_hi:[0,1,0] neg_lo:[1,0,0] neg_hi:[1,0,0]
	v_cvt_pk_bf16_f32 v4, v4, v5
	v_cvt_pk_bf16_f32 v5, v2, v3
	ds_write_b64 v186, v[4:5] offset:3264
	ds_read_b32 v2, v187 offset:56
	s_waitcnt lgkmcnt(0)
	v_pk_fma_f32 v[4:5], v[2:3], v[46:47], 0 op_sel_hi:[0,1,0] neg_lo:[1,0,0] neg_hi:[1,0,0]
	v_pk_fma_f32 v[2:3], v[2:3], v[48:49], 0 op_sel_hi:[0,1,0] neg_lo:[1,0,0] neg_hi:[1,0,0]
	v_cvt_pk_bf16_f32 v4, v4, v5
	v_cvt_pk_bf16_f32 v5, v2, v3
	ds_write_b64 v186, v[4:5] offset:3808
	ds_read_b128 a[192:195], v1
	ds_read_b128 a[196:199], v1 offset:64
	ds_read_b128 a[200:203], v1 offset:128
	ds_read_b128 a[204:207], v1 offset:192
	v_lshl_add_u64 v[118:119], v[130:131], 0, s[20:21]
	v_add_co_u32_e32 v126, vcc, s7, v118
	s_nop 1
	v_addc_co_u32_e32 v127, vcc, 0, v119, vcc
	v_add_co_u32_e32 v128, vcc, s36, v118
	global_load_dwordx4 v[90:93], v[118:119], off nt
	global_load_dwordx4 v[86:89], v[126:127], off nt
	v_addc_co_u32_e32 v129, vcc, 0, v119, vcc
	v_add_co_u32_e32 v134, vcc, s37, v118
	s_nop 1
	v_addc_co_u32_e32 v135, vcc, 0, v119, vcc
	v_add_co_u32_e32 v136, vcc, s38, v118
	global_load_dwordx4 v[54:57], v[128:129], off nt
	global_load_dwordx4 v[50:53], v[134:135], off nt
	v_addc_co_u32_e32 v137, vcc, 0, v119, vcc
	v_add_co_u32_e32 v138, vcc, s39, v118
	s_nop 1
	v_addc_co_u32_e32 v139, vcc, 0, v119, vcc
	v_add_co_u32_e32 v140, vcc, s41, v118
	global_load_dwordx4 v[14:17], v[136:137], off nt
	global_load_dwordx4 v[10:13], v[138:139], off nt
	v_addc_co_u32_e32 v141, vcc, 0, v119, vcc
	v_add_co_u32_e32 v142, vcc, s42, v118
	s_nop 1
	v_addc_co_u32_e32 v143, vcc, 0, v119, vcc
	global_load_dwordx4 v[6:9], v[140:141], off nt
	global_load_dwordx4 v[2:5], v[142:143], off nt
	v_mov_b32_e32 v26, v194
	s_waitcnt vmcnt(23)
	s_waitcnt vmcnt(22)
	s_waitcnt vmcnt(21)
	s_waitcnt vmcnt(20)
	s_waitcnt vmcnt(19)
	s_waitcnt vmcnt(18)
	s_waitcnt vmcnt(17)
	s_waitcnt vmcnt(16)
	ds_read_b32 v26, v187 offset:64
	s_waitcnt lgkmcnt(0)
	v_pk_fma_f32 v[28:29], v[26:27], v[110:111], 0 op_sel_hi:[0,1,0] neg_lo:[1,0,0] neg_hi:[1,0,0]
	v_pk_fma_f32 v[26:27], v[26:27], v[112:113], 0 op_sel_hi:[0,1,0] neg_lo:[1,0,0] neg_hi:[1,0,0]
	v_cvt_pk_bf16_f32 v28, v28, v29
	v_cvt_pk_bf16_f32 v29, v26, v27
	ds_write_b64 v186, v[28:29]
	ds_read_b32 v26, v187 offset:72
	s_waitcnt lgkmcnt(0)
	v_pk_fma_f32 v[28:29], v[26:27], v[98:99], 0 op_sel_hi:[0,1,0] neg_lo:[1,0,0] neg_hi:[1,0,0]
	v_pk_fma_f32 v[26:27], v[26:27], v[100:101], 0 op_sel_hi:[0,1,0] neg_lo:[1,0,0] neg_hi:[1,0,0]
	v_cvt_pk_bf16_f32 v28, v28, v29
	v_cvt_pk_bf16_f32 v29, v26, v27
	ds_write_b64 v186, v[28:29] offset:544
	ds_read_b32 v26, v187 offset:80
	s_waitcnt lgkmcnt(0)
	v_pk_fma_f32 v[28:29], v[26:27], v[78:79], 0 op_sel_hi:[0,1,0] neg_lo:[1,0,0] neg_hi:[1,0,0]
	v_pk_fma_f32 v[26:27], v[26:27], v[80:81], 0 op_sel_hi:[0,1,0] neg_lo:[1,0,0] neg_hi:[1,0,0]
	v_cvt_pk_bf16_f32 v28, v28, v29
	v_cvt_pk_bf16_f32 v29, v26, v27
	ds_write_b64 v186, v[28:29] offset:1088
	ds_read_b32 v26, v187 offset:88
	s_waitcnt lgkmcnt(0)
	v_pk_fma_f32 v[28:29], v[26:27], v[66:67], 0 op_sel_hi:[0,1,0] neg_lo:[1,0,0] neg_hi:[1,0,0]
	v_pk_fma_f32 v[26:27], v[26:27], v[68:69], 0 op_sel_hi:[0,1,0] neg_lo:[1,0,0] neg_hi:[1,0,0]
	v_cvt_pk_bf16_f32 v28, v28, v29
	v_cvt_pk_bf16_f32 v29, v26, v27
	ds_write_b64 v186, v[28:29] offset:1632
	ds_read_b32 v26, v187 offset:96
	s_waitcnt lgkmcnt(0)
	v_pk_fma_f32 v[28:29], v[26:27], v[58:59], 0 op_sel_hi:[0,1,0] neg_lo:[1,0,0] neg_hi:[1,0,0]
	v_pk_fma_f32 v[26:27], v[26:27], v[60:61], 0 op_sel_hi:[0,1,0] neg_lo:[1,0,0] neg_hi:[1,0,0]
	v_cvt_pk_bf16_f32 v28, v28, v29
	v_cvt_pk_bf16_f32 v29, v26, v27
	ds_write_b64 v186, v[28:29] offset:2176
	ds_read_b32 v26, v187 offset:104
	s_waitcnt lgkmcnt(0)
	v_pk_fma_f32 v[28:29], v[26:27], v[30:31], 0 op_sel_hi:[0,1,0] neg_lo:[1,0,0] neg_hi:[1,0,0]
	v_pk_fma_f32 v[26:27], v[26:27], v[32:33], 0 op_sel_hi:[0,1,0] neg_lo:[1,0,0] neg_hi:[1,0,0]
	v_cvt_pk_bf16_f32 v28, v28, v29
	v_cvt_pk_bf16_f32 v29, v26, v27
	ds_write_b64 v186, v[28:29] offset:2720
	ds_read_b32 v26, v187 offset:112
	s_waitcnt lgkmcnt(0)
	v_pk_fma_f32 v[22:23], v[26:27], v[22:23], 0 op_sel_hi:[0,1,0] neg_lo:[1,0,0] neg_hi:[1,0,0]
	v_pk_fma_f32 v[24:25], v[26:27], v[24:25], 0 op_sel_hi:[0,1,0] neg_lo:[1,0,0] neg_hi:[1,0,0]
	v_cvt_pk_bf16_f32 v22, v22, v23
	v_cvt_pk_bf16_f32 v23, v24, v25
	ds_write_b64 v186, v[22:23] offset:3264
	ds_read_b32 v22, v187 offset:120
	s_waitcnt lgkmcnt(0)
	v_pk_fma_f32 v[18:19], v[22:23], v[18:19], 0 op_sel_hi:[0,1,0] neg_lo:[1,0,0] neg_hi:[1,0,0]
	v_pk_fma_f32 v[20:21], v[22:23], v[20:21], 0 op_sel_hi:[0,1,0] neg_lo:[1,0,0] neg_hi:[1,0,0]
	v_cvt_pk_bf16_f32 v18, v18, v19
	v_cvt_pk_bf16_f32 v19, v20, v21
	ds_write_b64 v186, v[18:19] offset:3808
	ds_read_b128 a[208:211], v1
	ds_read_b128 a[212:215], v1 offset:64
	ds_read_b128 a[216:219], v1 offset:128
	ds_read_b128 a[220:223], v1 offset:192
	v_lshl_add_u64 v[18:19], v[150:151], 0, s[20:21]
	v_lshl_add_u64 v[20:21], v[152:153], 0, s[20:21]
	v_lshl_add_u64 v[22:23], v[156:157], 0, s[20:21]
	v_lshl_add_u64 v[24:25], v[158:159], 0, s[20:21]
	v_lshl_add_u64 v[26:27], v[160:161], 0, s[20:21]
	v_lshl_add_u64 v[28:29], v[162:163], 0, s[20:21]
	v_lshl_add_u64 v[46:47], v[164:165], 0, s[20:21]
	v_lshl_add_u64 v[48:49], v[166:167], 0, s[20:21]
	global_load_dwordx4 v[78:81], v[18:19], off nt
	global_load_dwordx4 v[74:77], v[20:21], off nt
	global_load_dwordx4 v[70:73], v[22:23], off nt
	global_load_dwordx4 v[66:69], v[24:25], off nt
	global_load_dwordx4 v[30:33], v[26:27], off nt
	s_nop 0
	global_load_dwordx4 v[26:29], v[28:29], off nt
	s_nop 0
	global_load_dwordx4 v[22:25], v[46:47], off nt
	global_load_dwordx4 v[18:21], v[48:49], off nt
	s_waitcnt vmcnt(23)
	s_waitcnt vmcnt(22)
	s_waitcnt vmcnt(21)
	s_waitcnt vmcnt(20)
	s_waitcnt vmcnt(19)
	s_waitcnt vmcnt(18)
	s_waitcnt vmcnt(17)
	s_waitcnt vmcnt(16)
	ds_read_b32 v46, v187 offset:128
	s_waitcnt lgkmcnt(0)
	v_pk_fma_f32 v[48:49], v[46:47], v[114:115], 0 op_sel_hi:[0,1,0] neg_lo:[1,0,0] neg_hi:[1,0,0]
	v_pk_fma_f32 v[46:47], v[46:47], v[116:117], 0 op_sel_hi:[0,1,0] neg_lo:[1,0,0] neg_hi:[1,0,0]
	v_cvt_pk_bf16_f32 v48, v48, v49
	v_cvt_pk_bf16_f32 v49, v46, v47
	ds_write_b64 v186, v[48:49]
	ds_read_b32 v46, v187 offset:136
	s_waitcnt lgkmcnt(0)
	v_pk_fma_f32 v[48:49], v[46:47], v[102:103], 0 op_sel_hi:[0,1,0] neg_lo:[1,0,0] neg_hi:[1,0,0]
	v_pk_fma_f32 v[46:47], v[46:47], v[104:105], 0 op_sel_hi:[0,1,0] neg_lo:[1,0,0] neg_hi:[1,0,0]
	v_cvt_pk_bf16_f32 v48, v48, v49
	v_cvt_pk_bf16_f32 v49, v46, v47
	ds_write_b64 v186, v[48:49] offset:544
	ds_read_b32 v46, v187 offset:144
	s_waitcnt lgkmcnt(0)
	v_pk_fma_f32 v[48:49], v[46:47], v[94:95], 0 op_sel_hi:[0,1,0] neg_lo:[1,0,0] neg_hi:[1,0,0]
	v_pk_fma_f32 v[46:47], v[46:47], v[96:97], 0 op_sel_hi:[0,1,0] neg_lo:[1,0,0] neg_hi:[1,0,0]
	v_cvt_pk_bf16_f32 v48, v48, v49
	v_cvt_pk_bf16_f32 v49, v46, v47
	ds_write_b64 v186, v[48:49] offset:1088
	ds_read_b32 v46, v187 offset:152
	s_waitcnt lgkmcnt(0)
	v_pk_fma_f32 v[48:49], v[46:47], v[82:83], 0 op_sel_hi:[0,1,0] neg_lo:[1,0,0] neg_hi:[1,0,0]
	v_pk_fma_f32 v[46:47], v[46:47], v[84:85], 0 op_sel_hi:[0,1,0] neg_lo:[1,0,0] neg_hi:[1,0,0]
	v_cvt_pk_bf16_f32 v48, v48, v49
	v_cvt_pk_bf16_f32 v49, v46, v47
	ds_write_b64 v186, v[48:49] offset:1632
	ds_read_b32 v46, v187 offset:160
	s_waitcnt lgkmcnt(0)
	v_pk_fma_f32 v[48:49], v[46:47], v[62:63], 0 op_sel_hi:[0,1,0] neg_lo:[1,0,0] neg_hi:[1,0,0]
	v_pk_fma_f32 v[46:47], v[46:47], v[64:65], 0 op_sel_hi:[0,1,0] neg_lo:[1,0,0] neg_hi:[1,0,0]
	v_cvt_pk_bf16_f32 v48, v48, v49
	v_cvt_pk_bf16_f32 v49, v46, v47
	ds_write_b64 v186, v[48:49] offset:2176
	ds_read_b32 v46, v187 offset:168
	s_waitcnt lgkmcnt(0)
	v_pk_fma_f32 v[42:43], v[46:47], v[42:43], 0 op_sel_hi:[0,1,0] neg_lo:[1,0,0] neg_hi:[1,0,0]
	v_pk_fma_f32 v[44:45], v[46:47], v[44:45], 0 op_sel_hi:[0,1,0] neg_lo:[1,0,0] neg_hi:[1,0,0]
	v_cvt_pk_bf16_f32 v42, v42, v43
	v_cvt_pk_bf16_f32 v43, v44, v45
	ds_write_b64 v186, v[42:43] offset:2720
	ds_read_b32 v42, v187 offset:176
	s_waitcnt lgkmcnt(0)
	v_pk_fma_f32 v[38:39], v[42:43], v[38:39], 0 op_sel_hi:[0,1,0] neg_lo:[1,0,0] neg_hi:[1,0,0]
	v_pk_fma_f32 v[40:41], v[42:43], v[40:41], 0 op_sel_hi:[0,1,0] neg_lo:[1,0,0] neg_hi:[1,0,0]
	v_cvt_pk_bf16_f32 v38, v38, v39
	v_cvt_pk_bf16_f32 v39, v40, v41
	ds_write_b64 v186, v[38:39] offset:3264
	ds_read_b32 v38, v187 offset:184
	s_waitcnt lgkmcnt(0)
	v_pk_fma_f32 v[34:35], v[38:39], v[34:35], 0 op_sel_hi:[0,1,0] neg_lo:[1,0,0] neg_hi:[1,0,0]
	v_pk_fma_f32 v[36:37], v[38:39], v[36:37], 0 op_sel_hi:[0,1,0] neg_lo:[1,0,0] neg_hi:[1,0,0]
	v_cvt_pk_bf16_f32 v34, v34, v35
	v_cvt_pk_bf16_f32 v35, v36, v37
	ds_write_b64 v186, v[34:35] offset:3808
	ds_read_b128 a[224:227], v1
	ds_read_b128 a[228:231], v1 offset:64
	ds_read_b128 a[232:235], v1 offset:128
	ds_read_b128 a[236:239], v1 offset:192
	v_lshl_add_u64 v[34:35], v[168:169], 0, s[20:21]
	v_lshl_add_u64 v[36:37], v[170:171], 0, s[20:21]
	v_lshl_add_u64 v[38:39], v[172:173], 0, s[20:21]
	v_lshl_add_u64 v[40:41], v[174:175], 0, s[20:21]
	v_lshl_add_u64 v[42:43], v[176:177], 0, s[20:21]
	v_lshl_add_u64 v[44:45], v[178:179], 0, s[20:21]
	v_lshl_add_u64 v[58:59], v[180:181], 0, s[20:21]
	v_lshl_add_u64 v[60:61], v[182:183], 0, s[20:21]
	global_load_dwordx4 v[122:125], v[34:35], off nt
	global_load_dwordx4 v[106:109], v[36:37], off nt
	global_load_dwordx4 v[94:97], v[38:39], off nt
	global_load_dwordx4 v[82:85], v[40:41], off nt
	global_load_dwordx4 v[46:49], v[42:43], off nt
	s_nop 0
	global_load_dwordx4 v[42:45], v[44:45], off nt
	s_nop 0
	global_load_dwordx4 v[38:41], v[58:59], off nt
	global_load_dwordx4 v[34:37], v[60:61], off nt
	v_mov_b32_e32 v98, v133
	s_waitcnt vmcnt(23)
	s_waitcnt vmcnt(22)
	s_waitcnt vmcnt(21)
	s_waitcnt vmcnt(20)
	s_waitcnt vmcnt(19)
	s_waitcnt vmcnt(18)
	s_waitcnt vmcnt(17)
	s_waitcnt vmcnt(16)
	ds_read_b32 v58, v187
	v_add_u32_e32 v99, 1, v98
	v_cmp_eq_u32_e32 vcc, v98, v132
	s_nop 1
	v_cndmask_b32_e64 v60, 0, 1.0, vcc
	v_cmp_eq_u32_e32 vcc, v99, v132
	s_nop 1
	v_cndmask_b32_e64 v61, 0, 1.0, vcc
	s_waitcnt lgkmcnt(0)
	v_pk_fma_f32 v[62:63], v[58:59], v[90:91], v[60:61] op_sel_hi:[0,1,1] neg_lo:[1,0,0] neg_hi:[1,0,0]
	v_add_u32_e32 v90, 3, v98
	v_add_u32_e32 v91, 2, v98
	v_cmp_eq_u32_e32 vcc, v90, v132
	v_cvt_pk_bf16_f32 v62, v62, v63
	s_nop 0
	v_cndmask_b32_e64 v65, 0, 1.0, vcc
	v_cmp_eq_u32_e32 vcc, v91, v132
	s_nop 1
	v_cndmask_b32_e64 v64, 0, 1.0, vcc
	v_pk_fma_f32 v[58:59], v[58:59], v[92:93], v[64:65] op_sel_hi:[0,1,1] neg_lo:[1,0,0] neg_hi:[1,0,0]
	v_cvt_pk_bf16_f32 v63, v58, v59
	ds_write_b64 v186, v[62:63]
	ds_read_b32 v58, v187 offset:8
	v_cmp_eq_u32_e32 vcc, v98, v193
	s_nop 1
	v_cndmask_b32_e64 v62, 0, 1.0, vcc
	v_cmp_eq_u32_e32 vcc, v99, v193
	s_nop 1
	v_cndmask_b32_e64 v63, 0, 1.0, vcc
	v_cmp_eq_u32_e32 vcc, v90, v193
	s_waitcnt lgkmcnt(0)
	v_pk_fma_f32 v[62:63], v[58:59], v[86:87], v[62:63] op_sel_hi:[0,1,1] neg_lo:[1,0,0] neg_hi:[1,0,0]
	v_cvt_pk_bf16_f32 v62, v62, v63
	v_cndmask_b32_e64 v61, 0, 1.0, vcc
	v_pk_fma_f32 v[58:59], v[58:59], v[88:89], v[60:61] op_sel_hi:[0,1,1] neg_lo:[1,0,0] neg_hi:[1,0,0]
	v_cvt_pk_bf16_f32 v63, v58, v59
	ds_write_b64 v186, v[62:63] offset:544
	ds_read_b32 v58, v187 offset:16
	v_cmp_eq_u32_e32 vcc, v98, v192
	s_nop 1
	v_cndmask_b32_e64 v60, 0, 1.0, vcc
	v_cmp_eq_u32_e32 vcc, v99, v192
	s_nop 1
	v_cndmask_b32_e64 v61, 0, 1.0, vcc
	v_cmp_eq_u32_e32 vcc, v90, v192
	s_waitcnt lgkmcnt(0)
	v_pk_fma_f32 v[54:55], v[58:59], v[54:55], v[60:61] op_sel_hi:[0,1,1] neg_lo:[1,0,0] neg_hi:[1,0,0]
	v_cvt_pk_bf16_f32 v54, v54, v55
	v_cndmask_b32_e64 v61, 0, 1.0, vcc
	v_cmp_eq_u32_e32 vcc, v91, v192
	s_nop 1
	v_cndmask_b32_e64 v60, 0, 1.0, vcc
	v_pk_fma_f32 v[56:57], v[58:59], v[56:57], v[60:61] op_sel_hi:[0,1,1] neg_lo:[1,0,0] neg_hi:[1,0,0]
	v_cvt_pk_bf16_f32 v55, v56, v57
	ds_write_b64 v186, v[54:55] offset:1088
	ds_read_b32 v54, v187 offset:24
	v_cmp_eq_u32_e32 vcc, v98, v190
	s_nop 1
	v_cndmask_b32_e64 v56, 0, 1.0, vcc
	v_cmp_eq_u32_e32 vcc, v99, v190
	s_nop 1
	v_cndmask_b32_e64 v57, 0, 1.0, vcc
	v_cmp_eq_u32_e32 vcc, v90, v190
	s_waitcnt lgkmcnt(0)
	v_pk_fma_f32 v[50:51], v[54:55], v[50:51], v[56:57] op_sel_hi:[0,1,1] neg_lo:[1,0,0] neg_hi:[1,0,0]
	v_cvt_pk_bf16_f32 v50, v50, v51
	v_cndmask_b32_e64 v57, 0, 1.0, vcc
	v_cmp_eq_u32_e32 vcc, v91, v190
	s_nop 1
	v_cndmask_b32_e64 v56, 0, 1.0, vcc
	v_pk_fma_f32 v[52:53], v[54:55], v[52:53], v[56:57] op_sel_hi:[0,1,1] neg_lo:[1,0,0] neg_hi:[1,0,0]
	v_cvt_pk_bf16_f32 v51, v52, v53
	ds_write_b64 v186, v[50:51] offset:1632
	ds_read_b32 v50, v187 offset:32
	v_cmp_eq_u32_e32 vcc, v98, v149
	s_nop 1
	v_cndmask_b32_e64 v52, 0, 1.0, vcc
	v_cmp_eq_u32_e32 vcc, v99, v149
	s_nop 1
	v_cndmask_b32_e64 v53, 0, 1.0, vcc
	v_cmp_eq_u32_e32 vcc, v90, v149
	s_waitcnt lgkmcnt(0)
	v_pk_fma_f32 v[14:15], v[50:51], v[14:15], v[52:53] op_sel_hi:[0,1,1] neg_lo:[1,0,0] neg_hi:[1,0,0]
	v_cvt_pk_bf16_f32 v14, v14, v15
	v_cndmask_b32_e64 v53, 0, 1.0, vcc
	v_cmp_eq_u32_e32 vcc, v91, v149
	s_nop 1
	v_cndmask_b32_e64 v52, 0, 1.0, vcc
	v_pk_fma_f32 v[16:17], v[50:51], v[16:17], v[52:53] op_sel_hi:[0,1,1] neg_lo:[1,0,0] neg_hi:[1,0,0]
	v_cvt_pk_bf16_f32 v15, v16, v17
	ds_write_b64 v186, v[14:15] offset:2176
	ds_read_b32 v14, v187 offset:40
	v_cmp_eq_u32_e32 vcc, v98, v148
	s_nop 1
	v_cndmask_b32_e64 v16, 0, 1.0, vcc
	v_cmp_eq_u32_e32 vcc, v99, v148
	s_nop 1
	v_cndmask_b32_e64 v17, 0, 1.0, vcc
	v_cmp_eq_u32_e32 vcc, v90, v148
	s_waitcnt lgkmcnt(0)
	v_pk_fma_f32 v[10:11], v[14:15], v[10:11], v[16:17] op_sel_hi:[0,1,1] neg_lo:[1,0,0] neg_hi:[1,0,0]
	v_cvt_pk_bf16_f32 v10, v10, v11
	v_cndmask_b32_e64 v17, 0, 1.0, vcc
	v_cmp_eq_u32_e32 vcc, v91, v148
	s_nop 1
	v_cndmask_b32_e64 v16, 0, 1.0, vcc
	v_pk_fma_f32 v[12:13], v[14:15], v[12:13], v[16:17] op_sel_hi:[0,1,1] neg_lo:[1,0,0] neg_hi:[1,0,0]
	v_cvt_pk_bf16_f32 v11, v12, v13
	ds_write_b64 v186, v[10:11] offset:2720
	ds_read_b32 v10, v187 offset:48
	v_cmp_eq_u32_e32 vcc, v98, v147
	s_nop 1
	v_cndmask_b32_e64 v12, 0, 1.0, vcc
	v_cmp_eq_u32_e32 vcc, v99, v147
	s_nop 1
	v_cndmask_b32_e64 v13, 0, 1.0, vcc
	v_cmp_eq_u32_e32 vcc, v90, v147
	s_waitcnt lgkmcnt(0)
	v_pk_fma_f32 v[6:7], v[10:11], v[6:7], v[12:13] op_sel_hi:[0,1,1] neg_lo:[1,0,0] neg_hi:[1,0,0]
	v_cvt_pk_bf16_f32 v6, v6, v7
	v_cndmask_b32_e64 v13, 0, 1.0, vcc
	v_cmp_eq_u32_e32 vcc, v91, v147
	s_nop 1
	v_cndmask_b32_e64 v12, 0, 1.0, vcc
	v_pk_fma_f32 v[8:9], v[10:11], v[8:9], v[12:13] op_sel_hi:[0,1,1] neg_lo:[1,0,0] neg_hi:[1,0,0]
	v_cvt_pk_bf16_f32 v7, v8, v9
	ds_write_b64 v186, v[6:7] offset:3264
	ds_read_b32 v6, v187 offset:56
	v_cmp_eq_u32_e32 vcc, v98, v146
	s_nop 1
	v_cndmask_b32_e64 v8, 0, 1.0, vcc
	v_cmp_eq_u32_e32 vcc, v99, v146
	s_nop 1
	v_cndmask_b32_e64 v9, 0, 1.0, vcc
	v_cmp_eq_u32_e32 vcc, v90, v146
	s_waitcnt lgkmcnt(0)
	v_pk_fma_f32 v[2:3], v[6:7], v[2:3], v[8:9] op_sel_hi:[0,1,1] neg_lo:[1,0,0] neg_hi:[1,0,0]
	v_cvt_pk_bf16_f32 v2, v2, v3
	v_cndmask_b32_e64 v9, 0, 1.0, vcc
	v_cmp_eq_u32_e32 vcc, v91, v146
	s_nop 1
	v_cndmask_b32_e64 v8, 0, 1.0, vcc
	v_pk_fma_f32 v[4:5], v[6:7], v[4:5], v[8:9] op_sel_hi:[0,1,1] neg_lo:[1,0,0] neg_hi:[1,0,0]
	v_cvt_pk_bf16_f32 v3, v4, v5
	ds_write_b64 v186, v[2:3] offset:3808
	ds_read_b128 v[2:5], v1
	ds_read_b128 v[6:9], v1 offset:64
	ds_read_b128 v[10:13], v1 offset:128
	ds_read_b128 v[14:17], v1 offset:192
	global_load_dwordx4 v[118:121], v[118:119], off offset:512 nt
	s_nop 0
	global_load_dwordx4 v[110:113], v[126:127], off offset:512 nt
	global_load_dwordx4 v[98:101], v[128:129], off offset:512 nt
	global_load_dwordx4 v[86:89], v[134:135], off offset:512 nt
	global_load_dwordx4 v[62:65], v[136:137], off offset:512 nt
	global_load_dwordx4 v[58:61], v[138:139], off offset:512 nt
	global_load_dwordx4 v[54:57], v[140:141], off offset:512 nt
	global_load_dwordx4 v[50:53], v[142:143], off offset:512 nt
	v_mov_b32_e32 v91, v133
	s_waitcnt vmcnt(23)
	s_waitcnt vmcnt(22)
	s_waitcnt vmcnt(21)
	s_waitcnt vmcnt(20)
	s_waitcnt vmcnt(19)
	s_waitcnt vmcnt(18)
	s_waitcnt vmcnt(17)
	s_waitcnt vmcnt(16)
	ds_read_b32 v90, v187 offset:64
	v_or_b32_e32 v138, 16, v132
	v_add_u32_e32 v102, 1, v91
	v_cmp_eq_u32_e32 vcc, v91, v138
	v_add_u32_e32 v103, 3, v91
	v_add_u32_e32 v104, 2, v91
	v_cndmask_b32_e64 v92, 0, 1.0, vcc
	v_cmp_eq_u32_e32 vcc, v102, v138
	v_or_b32_e32 v139, 18, v132
	v_or_b32_e32 v140, 20, v132
	v_cndmask_b32_e64 v93, 0, 1.0, vcc
	v_cmp_eq_u32_e32 vcc, v103, v138
	s_waitcnt lgkmcnt(0)
	v_pk_fma_f32 v[78:79], v[90:91], v[78:79], v[92:93] op_sel_hi:[0,1,1] neg_lo:[1,0,0] neg_hi:[1,0,0]
	v_cvt_pk_bf16_f32 v78, v78, v79
	v_cndmask_b32_e64 v93, 0, 1.0, vcc
	v_cmp_eq_u32_e32 vcc, v104, v138
	v_or_b32_e32 v141, 22, v132
	v_or_b32_e32 v142, 24, v132
	v_cndmask_b32_e64 v92, 0, 1.0, vcc
	v_pk_fma_f32 v[80:81], v[90:91], v[80:81], v[92:93] op_sel_hi:[0,1,1] neg_lo:[1,0,0] neg_hi:[1,0,0]
	v_cvt_pk_bf16_f32 v79, v80, v81
	ds_write_b64 v186, v[78:79]
	ds_read_b32 v78, v187 offset:72
	v_cmp_eq_u32_e32 vcc, v91, v139
	v_or_b32_e32 v143, 26, v132
	v_or_b32_e32 v144, 28, v132
	v_cndmask_b32_e64 v80, 0, 1.0, vcc
	v_cmp_eq_u32_e32 vcc, v102, v139
	v_or_b32_e32 v145, 30, v132
	s_nop 0
	v_cndmask_b32_e64 v81, 0, 1.0, vcc
	v_cmp_eq_u32_e32 vcc, v103, v139
	s_waitcnt lgkmcnt(0)
	v_pk_fma_f32 v[74:75], v[78:79], v[74:75], v[80:81] op_sel_hi:[0,1,1] neg_lo:[1,0,0] neg_hi:[1,0,0]
	v_cvt_pk_bf16_f32 v74, v74, v75
	v_cndmask_b32_e64 v81, 0, 1.0, vcc
	v_cmp_eq_u32_e32 vcc, v104, v139
	s_nop 1
	v_cndmask_b32_e64 v80, 0, 1.0, vcc
	v_pk_fma_f32 v[76:77], v[78:79], v[76:77], v[80:81] op_sel_hi:[0,1,1] neg_lo:[1,0,0] neg_hi:[1,0,0]
	v_cvt_pk_bf16_f32 v75, v76, v77
	ds_write_b64 v186, v[74:75] offset:544
	ds_read_b32 v74, v187 offset:80
	v_cmp_eq_u32_e32 vcc, v91, v140
	s_nop 1
	v_cndmask_b32_e64 v76, 0, 1.0, vcc
	v_cmp_eq_u32_e32 vcc, v102, v140
	s_nop 1
	v_cndmask_b32_e64 v77, 0, 1.0, vcc
	v_cmp_eq_u32_e32 vcc, v103, v140
	s_waitcnt lgkmcnt(0)
	v_pk_fma_f32 v[70:71], v[74:75], v[70:71], v[76:77] op_sel_hi:[0,1,1] neg_lo:[1,0,0] neg_hi:[1,0,0]
	v_cvt_pk_bf16_f32 v70, v70, v71
	v_cndmask_b32_e64 v77, 0, 1.0, vcc
	v_cmp_eq_u32_e32 vcc, v104, v140
	s_nop 1
	v_cndmask_b32_e64 v76, 0, 1.0, vcc
	v_pk_fma_f32 v[72:73], v[74:75], v[72:73], v[76:77] op_sel_hi:[0,1,1] neg_lo:[1,0,0] neg_hi:[1,0,0]
	v_cvt_pk_bf16_f32 v71, v72, v73
	ds_write_b64 v186, v[70:71] offset:1088
	ds_read_b32 v70, v187 offset:88
	v_cmp_eq_u32_e32 vcc, v91, v141
	s_nop 1
	v_cndmask_b32_e64 v72, 0, 1.0, vcc
	v_cmp_eq_u32_e32 vcc, v102, v141
	s_nop 1
	v_cndmask_b32_e64 v73, 0, 1.0, vcc
	v_cmp_eq_u32_e32 vcc, v103, v141
	s_waitcnt lgkmcnt(0)
	v_pk_fma_f32 v[66:67], v[70:71], v[66:67], v[72:73] op_sel_hi:[0,1,1] neg_lo:[1,0,0] neg_hi:[1,0,0]
	v_cvt_pk_bf16_f32 v66, v66, v67
	v_cndmask_b32_e64 v73, 0, 1.0, vcc
	v_cmp_eq_u32_e32 vcc, v104, v141
	s_nop 1
	v_cndmask_b32_e64 v72, 0, 1.0, vcc
	v_pk_fma_f32 v[68:69], v[70:71], v[68:69], v[72:73] op_sel_hi:[0,1,1] neg_lo:[1,0,0] neg_hi:[1,0,0]
	v_cvt_pk_bf16_f32 v67, v68, v69
	ds_write_b64 v186, v[66:67] offset:1632
	ds_read_b32 v66, v187 offset:96
	v_cmp_eq_u32_e32 vcc, v91, v142
	s_nop 1
	v_cndmask_b32_e64 v68, 0, 1.0, vcc
	v_cmp_eq_u32_e32 vcc, v102, v142
	s_nop 1
	v_cndmask_b32_e64 v69, 0, 1.0, vcc
	v_cmp_eq_u32_e32 vcc, v103, v142
	s_waitcnt lgkmcnt(0)
	v_pk_fma_f32 v[30:31], v[66:67], v[30:31], v[68:69] op_sel_hi:[0,1,1] neg_lo:[1,0,0] neg_hi:[1,0,0]
	v_cvt_pk_bf16_f32 v30, v30, v31
	v_cndmask_b32_e64 v69, 0, 1.0, vcc
	v_cmp_eq_u32_e32 vcc, v104, v142
	s_nop 1
	v_cndmask_b32_e64 v68, 0, 1.0, vcc
	v_pk_fma_f32 v[32:33], v[66:67], v[32:33], v[68:69] op_sel_hi:[0,1,1] neg_lo:[1,0,0] neg_hi:[1,0,0]
	v_cvt_pk_bf16_f32 v31, v32, v33
	ds_write_b64 v186, v[30:31] offset:2176
	ds_read_b32 v30, v187 offset:104
	v_cmp_eq_u32_e32 vcc, v91, v143
	s_nop 1
	v_cndmask_b32_e64 v32, 0, 1.0, vcc
	v_cmp_eq_u32_e32 vcc, v102, v143
	s_nop 1
	v_cndmask_b32_e64 v33, 0, 1.0, vcc
	v_cmp_eq_u32_e32 vcc, v103, v143
	s_waitcnt lgkmcnt(0)
	v_pk_fma_f32 v[26:27], v[30:31], v[26:27], v[32:33] op_sel_hi:[0,1,1] neg_lo:[1,0,0] neg_hi:[1,0,0]
	v_cvt_pk_bf16_f32 v26, v26, v27
	v_cndmask_b32_e64 v33, 0, 1.0, vcc
	v_cmp_eq_u32_e32 vcc, v104, v143
	s_nop 1
	v_cndmask_b32_e64 v32, 0, 1.0, vcc
	v_pk_fma_f32 v[28:29], v[30:31], v[28:29], v[32:33] op_sel_hi:[0,1,1] neg_lo:[1,0,0] neg_hi:[1,0,0]
	v_cvt_pk_bf16_f32 v27, v28, v29
	ds_write_b64 v186, v[26:27] offset:2720
	ds_read_b32 v26, v187 offset:112
	v_cmp_eq_u32_e32 vcc, v91, v144
	s_nop 1
	v_cndmask_b32_e64 v28, 0, 1.0, vcc
	v_cmp_eq_u32_e32 vcc, v102, v144
	s_nop 1
	v_cndmask_b32_e64 v29, 0, 1.0, vcc
	v_cmp_eq_u32_e32 vcc, v103, v144
	s_waitcnt lgkmcnt(0)
	v_pk_fma_f32 v[22:23], v[26:27], v[22:23], v[28:29] op_sel_hi:[0,1,1] neg_lo:[1,0,0] neg_hi:[1,0,0]
	v_cvt_pk_bf16_f32 v22, v22, v23
	v_cndmask_b32_e64 v29, 0, 1.0, vcc
	v_cmp_eq_u32_e32 vcc, v104, v144
	s_nop 1
	v_cndmask_b32_e64 v28, 0, 1.0, vcc
	v_pk_fma_f32 v[24:25], v[26:27], v[24:25], v[28:29] op_sel_hi:[0,1,1] neg_lo:[1,0,0] neg_hi:[1,0,0]
	v_cvt_pk_bf16_f32 v23, v24, v25
	ds_write_b64 v186, v[22:23] offset:3264
	ds_read_b32 v22, v187 offset:120
	v_cmp_eq_u32_e32 vcc, v91, v145
	s_nop 1
	v_cndmask_b32_e64 v24, 0, 1.0, vcc
	v_cmp_eq_u32_e32 vcc, v102, v145
	s_nop 1
	v_cndmask_b32_e64 v25, 0, 1.0, vcc
	v_cmp_eq_u32_e32 vcc, v103, v145
	s_waitcnt lgkmcnt(0)
	v_pk_fma_f32 v[18:19], v[22:23], v[18:19], v[24:25] op_sel_hi:[0,1,1] neg_lo:[1,0,0] neg_hi:[1,0,0]
	v_cvt_pk_bf16_f32 v18, v18, v19
	v_cndmask_b32_e64 v25, 0, 1.0, vcc
	v_cmp_eq_u32_e32 vcc, v104, v145
	s_nop 1
	v_cndmask_b32_e64 v24, 0, 1.0, vcc
	v_pk_fma_f32 v[20:21], v[22:23], v[20:21], v[24:25] op_sel_hi:[0,1,1] neg_lo:[1,0,0] neg_hi:[1,0,0]
	v_cvt_pk_bf16_f32 v19, v20, v21
	ds_write_b64 v186, v[18:19] offset:3808
	ds_read_b128 v[18:21], v1
	ds_read_b128 v[22:25], v1 offset:64
	ds_read_b128 v[26:29], v1 offset:128
	ds_read_b128 v[30:33], v1 offset:192
	v_lshl_add_u64 v[66:67], v[150:151], 0, s[8:9]
	v_lshl_add_u64 v[68:69], v[152:153], 0, s[8:9]
	v_lshl_add_u64 v[70:71], v[156:157], 0, s[8:9]
	v_lshl_add_u64 v[72:73], v[158:159], 0, s[8:9]
	v_lshl_add_u64 v[74:75], v[160:161], 0, s[8:9]
	v_lshl_add_u64 v[76:77], v[162:163], 0, s[8:9]
	v_lshl_add_u64 v[134:135], v[164:165], 0, s[8:9]
	v_lshl_add_u64 v[136:137], v[166:167], 0, s[8:9]
	global_load_dwordx4 v[126:129], v[66:67], off nt
	global_load_dwordx4 v[114:117], v[68:69], off nt
	global_load_dwordx4 v[102:105], v[70:71], off nt
	global_load_dwordx4 v[90:93], v[72:73], off nt
	global_load_dwordx4 v[78:81], v[74:75], off nt
	s_nop 0
	global_load_dwordx4 v[74:77], v[76:77], off nt
	s_nop 0
	global_load_dwordx4 v[70:73], v[134:135], off nt
	global_load_dwordx4 v[66:69], v[136:137], off nt
	s_waitcnt vmcnt(23)
	s_waitcnt vmcnt(22)
	s_waitcnt vmcnt(21)
	s_waitcnt vmcnt(20)
	s_waitcnt vmcnt(19)
	s_waitcnt vmcnt(18)
	s_waitcnt vmcnt(17)
	s_waitcnt vmcnt(16)
	ds_read_b32 v134, v187 offset:128
	v_or_b32_e32 v194, 32, v132
	v_add_u32_e32 v135, 1, v133
	v_cmp_eq_u32_e32 vcc, v133, v194
	v_add_u32_e32 v202, 3, v133
	v_add_u32_e32 v203, 2, v133
	v_cndmask_b32_e64 v136, 0, 1.0, vcc
	v_cmp_eq_u32_e32 vcc, v135, v194
	v_or_b32_e32 v195, 34, v132
	v_or_b32_e32 v196, 36, v132
	v_cndmask_b32_e64 v137, 0, 1.0, vcc
	v_cmp_eq_u32_e32 vcc, v202, v194
	s_waitcnt lgkmcnt(0)
	v_pk_fma_f32 v[122:123], v[134:135], v[122:123], v[136:137] op_sel_hi:[0,1,1] neg_lo:[1,0,0] neg_hi:[1,0,0]
	v_cvt_pk_bf16_f32 v122, v122, v123
	v_cndmask_b32_e64 v137, 0, 1.0, vcc
	v_cmp_eq_u32_e32 vcc, v203, v194
	v_or_b32_e32 v197, 38, v132
	v_or_b32_e32 v198, 40, v132
	v_cndmask_b32_e64 v136, 0, 1.0, vcc
	v_pk_fma_f32 v[124:125], v[134:135], v[124:125], v[136:137] op_sel_hi:[0,1,1] neg_lo:[1,0,0] neg_hi:[1,0,0]
	v_cvt_pk_bf16_f32 v123, v124, v125
	ds_write_b64 v186, v[122:123]
	ds_read_b32 v122, v187 offset:136
	v_cmp_eq_u32_e32 vcc, v133, v195
	v_or_b32_e32 v199, 42, v132
	v_or_b32_e32 v200, 44, v132
	v_cndmask_b32_e64 v124, 0, 1.0, vcc
	v_cmp_eq_u32_e32 vcc, v135, v195
	v_or_b32_e32 v201, 46, v132
	s_nop 0
	v_cndmask_b32_e64 v125, 0, 1.0, vcc
	v_cmp_eq_u32_e32 vcc, v202, v195
	s_waitcnt lgkmcnt(0)
	v_pk_fma_f32 v[106:107], v[122:123], v[106:107], v[124:125] op_sel_hi:[0,1,1] neg_lo:[1,0,0] neg_hi:[1,0,0]
	v_cvt_pk_bf16_f32 v106, v106, v107
	v_cndmask_b32_e64 v125, 0, 1.0, vcc
	v_cmp_eq_u32_e32 vcc, v203, v195
	s_nop 1
	v_cndmask_b32_e64 v124, 0, 1.0, vcc
	v_pk_fma_f32 v[108:109], v[122:123], v[108:109], v[124:125] op_sel_hi:[0,1,1] neg_lo:[1,0,0] neg_hi:[1,0,0]
	v_cvt_pk_bf16_f32 v107, v108, v109
	ds_write_b64 v186, v[106:107] offset:544
	ds_read_b32 v106, v187 offset:144
	v_cmp_eq_u32_e32 vcc, v133, v196
	s_nop 1
	v_cndmask_b32_e64 v108, 0, 1.0, vcc
	v_cmp_eq_u32_e32 vcc, v135, v196
	s_nop 1
	v_cndmask_b32_e64 v109, 0, 1.0, vcc
	v_cmp_eq_u32_e32 vcc, v202, v196
	s_waitcnt lgkmcnt(0)
	v_pk_fma_f32 v[94:95], v[106:107], v[94:95], v[108:109] op_sel_hi:[0,1,1] neg_lo:[1,0,0] neg_hi:[1,0,0]
	v_cvt_pk_bf16_f32 v94, v94, v95
	v_cndmask_b32_e64 v109, 0, 1.0, vcc
	v_cmp_eq_u32_e32 vcc, v203, v196
	s_nop 1
	v_cndmask_b32_e64 v108, 0, 1.0, vcc
	v_pk_fma_f32 v[96:97], v[106:107], v[96:97], v[108:109] op_sel_hi:[0,1,1] neg_lo:[1,0,0] neg_hi:[1,0,0]
	v_cvt_pk_bf16_f32 v95, v96, v97
	ds_write_b64 v186, v[94:95] offset:1088
	ds_read_b32 v94, v187 offset:152
	v_cmp_eq_u32_e32 vcc, v133, v197
	s_nop 1
	v_cndmask_b32_e64 v96, 0, 1.0, vcc
	v_cmp_eq_u32_e32 vcc, v135, v197
	s_nop 1
	v_cndmask_b32_e64 v97, 0, 1.0, vcc
	v_cmp_eq_u32_e32 vcc, v202, v197
	s_waitcnt lgkmcnt(0)
	v_pk_fma_f32 v[82:83], v[94:95], v[82:83], v[96:97] op_sel_hi:[0,1,1] neg_lo:[1,0,0] neg_hi:[1,0,0]
	v_cvt_pk_bf16_f32 v82, v82, v83
	v_cndmask_b32_e64 v97, 0, 1.0, vcc
	v_cmp_eq_u32_e32 vcc, v203, v197
	s_nop 1
	v_cndmask_b32_e64 v96, 0, 1.0, vcc
	v_pk_fma_f32 v[84:85], v[94:95], v[84:85], v[96:97] op_sel_hi:[0,1,1] neg_lo:[1,0,0] neg_hi:[1,0,0]
	v_cvt_pk_bf16_f32 v83, v84, v85
	ds_write_b64 v186, v[82:83] offset:1632
	ds_read_b32 v82, v187 offset:160
	v_cmp_eq_u32_e32 vcc, v133, v198
	s_nop 1
	v_cndmask_b32_e64 v84, 0, 1.0, vcc
	v_cmp_eq_u32_e32 vcc, v135, v198
	s_nop 1
	v_cndmask_b32_e64 v85, 0, 1.0, vcc
	v_cmp_eq_u32_e32 vcc, v202, v198
	s_waitcnt lgkmcnt(0)
	v_pk_fma_f32 v[46:47], v[82:83], v[46:47], v[84:85] op_sel_hi:[0,1,1] neg_lo:[1,0,0] neg_hi:[1,0,0]
	v_cvt_pk_bf16_f32 v46, v46, v47
	v_cndmask_b32_e64 v85, 0, 1.0, vcc
	v_cmp_eq_u32_e32 vcc, v203, v198
	s_nop 1
	v_cndmask_b32_e64 v84, 0, 1.0, vcc
	v_pk_fma_f32 v[48:49], v[82:83], v[48:49], v[84:85] op_sel_hi:[0,1,1] neg_lo:[1,0,0] neg_hi:[1,0,0]
	v_cvt_pk_bf16_f32 v47, v48, v49
	ds_write_b64 v186, v[46:47] offset:2176
	ds_read_b32 v46, v187 offset:168
	v_cmp_eq_u32_e32 vcc, v133, v199
	s_nop 1
	v_cndmask_b32_e64 v48, 0, 1.0, vcc
	v_cmp_eq_u32_e32 vcc, v135, v199
	s_nop 1
	v_cndmask_b32_e64 v49, 0, 1.0, vcc
	v_cmp_eq_u32_e32 vcc, v202, v199
	s_waitcnt lgkmcnt(0)
	v_pk_fma_f32 v[42:43], v[46:47], v[42:43], v[48:49] op_sel_hi:[0,1,1] neg_lo:[1,0,0] neg_hi:[1,0,0]
	v_cvt_pk_bf16_f32 v42, v42, v43
	v_cndmask_b32_e64 v49, 0, 1.0, vcc
	v_cmp_eq_u32_e32 vcc, v203, v199
	s_nop 1
	v_cndmask_b32_e64 v48, 0, 1.0, vcc
	v_pk_fma_f32 v[44:45], v[46:47], v[44:45], v[48:49] op_sel_hi:[0,1,1] neg_lo:[1,0,0] neg_hi:[1,0,0]
	v_cvt_pk_bf16_f32 v43, v44, v45
	ds_write_b64 v186, v[42:43] offset:2720
	ds_read_b32 v42, v187 offset:176
	v_cmp_eq_u32_e32 vcc, v133, v200
	s_nop 1
	v_cndmask_b32_e64 v44, 0, 1.0, vcc
	v_cmp_eq_u32_e32 vcc, v135, v200
	s_nop 1
	v_cndmask_b32_e64 v45, 0, 1.0, vcc
	v_cmp_eq_u32_e32 vcc, v202, v200
	s_waitcnt lgkmcnt(0)
	v_pk_fma_f32 v[38:39], v[42:43], v[38:39], v[44:45] op_sel_hi:[0,1,1] neg_lo:[1,0,0] neg_hi:[1,0,0]
	v_cvt_pk_bf16_f32 v38, v38, v39
	v_cndmask_b32_e64 v45, 0, 1.0, vcc
	v_cmp_eq_u32_e32 vcc, v203, v200
	s_nop 1
	v_cndmask_b32_e64 v44, 0, 1.0, vcc
	v_pk_fma_f32 v[40:41], v[42:43], v[40:41], v[44:45] op_sel_hi:[0,1,1] neg_lo:[1,0,0] neg_hi:[1,0,0]
	v_cvt_pk_bf16_f32 v39, v40, v41
	ds_write_b64 v186, v[38:39] offset:3264
	ds_read_b32 v38, v187 offset:184
	v_cmp_eq_u32_e32 vcc, v133, v201
	s_nop 1
	v_cndmask_b32_e64 v40, 0, 1.0, vcc
	v_cmp_eq_u32_e32 vcc, v135, v201
	s_nop 1
	v_cndmask_b32_e64 v41, 0, 1.0, vcc
	v_cmp_eq_u32_e32 vcc, v202, v201
	s_waitcnt lgkmcnt(0)
	v_pk_fma_f32 v[34:35], v[38:39], v[34:35], v[40:41] op_sel_hi:[0,1,1] neg_lo:[1,0,0] neg_hi:[1,0,0]
	v_cvt_pk_bf16_f32 v34, v34, v35
	v_cndmask_b32_e64 v41, 0, 1.0, vcc
	v_cmp_eq_u32_e32 vcc, v203, v201
	s_nop 1
	v_cndmask_b32_e64 v40, 0, 1.0, vcc
	v_pk_fma_f32 v[36:37], v[38:39], v[36:37], v[40:41] op_sel_hi:[0,1,1] neg_lo:[1,0,0] neg_hi:[1,0,0]
	v_cvt_pk_bf16_f32 v35, v36, v37
	ds_write_b64 v186, v[34:35] offset:3808
	ds_read_b128 v[34:37], v1
	ds_read_b128 v[38:41], v1 offset:64
	ds_read_b128 v[42:45], v1 offset:128
	ds_read_b128 v[46:49], v1 offset:192
	v_mov_b32_e32 v106, v189
	s_waitcnt vmcnt(15)
	s_waitcnt vmcnt(14)
	s_waitcnt vmcnt(13)
	s_waitcnt vmcnt(12)
	s_waitcnt vmcnt(11)
	s_waitcnt vmcnt(10)
	s_waitcnt vmcnt(9)
	s_waitcnt vmcnt(8)
	ds_read_b32 v82, v187
	v_add_u32_e32 v107, 1, v106
	v_cmp_eq_u32_e32 vcc, v106, v132
	v_add_u32_e32 v108, 3, v106
	v_add_u32_e32 v109, 2, v106
	v_cndmask_b32_e64 v84, 0, 1.0, vcc
	v_cmp_eq_u32_e32 vcc, v107, v132
	s_nop 1
	v_cndmask_b32_e64 v85, 0, 1.0, vcc
	v_cmp_eq_u32_e32 vcc, v108, v132
	s_waitcnt lgkmcnt(0)
	v_pk_fma_f32 v[94:95], v[82:83], v[118:119], v[84:85] op_sel_hi:[0,1,1] neg_lo:[1,0,0] neg_hi:[1,0,0]
	v_cvt_pk_bf16_f32 v94, v94, v95
	v_cndmask_b32_e64 v97, 0, 1.0, vcc
	v_cmp_eq_u32_e32 vcc, v109, v132
	s_nop 1
	v_cndmask_b32_e64 v96, 0, 1.0, vcc
	v_pk_fma_f32 v[82:83], v[82:83], v[120:121], v[96:97] op_sel_hi:[0,1,1] neg_lo:[1,0,0] neg_hi:[1,0,0]
	v_cvt_pk_bf16_f32 v95, v82, v83
	ds_write_b64 v186, v[94:95]
	ds_read_b32 v82, v187 offset:8
	v_cmp_eq_u32_e32 vcc, v106, v193
	s_nop 1
	v_cndmask_b32_e64 v94, 0, 1.0, vcc
	v_cmp_eq_u32_e32 vcc, v107, v193
	s_nop 1
	v_cndmask_b32_e64 v95, 0, 1.0, vcc
	v_cmp_eq_u32_e32 vcc, v108, v193
	s_waitcnt lgkmcnt(0)
	v_pk_fma_f32 v[94:95], v[82:83], v[110:111], v[94:95] op_sel_hi:[0,1,1] neg_lo:[1,0,0] neg_hi:[1,0,0]
	v_cvt_pk_bf16_f32 v94, v94, v95
	v_cndmask_b32_e64 v85, 0, 1.0, vcc
	v_pk_fma_f32 v[82:83], v[82:83], v[112:113], v[84:85] op_sel_hi:[0,1,1] neg_lo:[1,0,0] neg_hi:[1,0,0]
	v_cvt_pk_bf16_f32 v95, v82, v83
	ds_write_b64 v186, v[94:95] offset:544
	ds_read_b32 v82, v187 offset:16
	v_cmp_eq_u32_e32 vcc, v106, v192
	s_nop 1
	v_cndmask_b32_e64 v84, 0, 1.0, vcc
	v_cmp_eq_u32_e32 vcc, v107, v192
	s_nop 1
	v_cndmask_b32_e64 v85, 0, 1.0, vcc
	v_cmp_eq_u32_e32 vcc, v108, v192
	s_waitcnt lgkmcnt(0)
	v_pk_fma_f32 v[84:85], v[82:83], v[98:99], v[84:85] op_sel_hi:[0,1,1] neg_lo:[1,0,0] neg_hi:[1,0,0]
	v_cvt_pk_bf16_f32 v84, v84, v85
	v_cndmask_b32_e64 v95, 0, 1.0, vcc
	v_cmp_eq_u32_e32 vcc, v109, v192
	s_nop 1
	v_cndmask_b32_e64 v94, 0, 1.0, vcc
	v_pk_fma_f32 v[82:83], v[82:83], v[100:101], v[94:95] op_sel_hi:[0,1,1] neg_lo:[1,0,0] neg_hi:[1,0,0]
	v_cvt_pk_bf16_f32 v85, v82, v83
	ds_write_b64 v186, v[84:85] offset:1088
	ds_read_b32 v82, v187 offset:24
	v_cmp_eq_u32_e32 vcc, v106, v190
	s_nop 1
	v_cndmask_b32_e64 v84, 0, 1.0, vcc
	v_cmp_eq_u32_e32 vcc, v107, v190
	s_nop 1
	v_cndmask_b32_e64 v85, 0, 1.0, vcc
	v_cmp_eq_u32_e32 vcc, v108, v190
	s_waitcnt lgkmcnt(0)
	v_pk_fma_f32 v[84:85], v[82:83], v[86:87], v[84:85] op_sel_hi:[0,1,1] neg_lo:[1,0,0] neg_hi:[1,0,0]
	v_cvt_pk_bf16_f32 v84, v84, v85
	v_cndmask_b32_e64 v87, 0, 1.0, vcc
	v_cmp_eq_u32_e32 vcc, v109, v190
	s_nop 1
	v_cndmask_b32_e64 v86, 0, 1.0, vcc
	v_pk_fma_f32 v[82:83], v[82:83], v[88:89], v[86:87] op_sel_hi:[0,1,1] neg_lo:[1,0,0] neg_hi:[1,0,0]
	v_cvt_pk_bf16_f32 v85, v82, v83
	ds_write_b64 v186, v[84:85] offset:1632
	ds_read_b32 v82, v187 offset:32
	v_cmp_eq_u32_e32 vcc, v106, v149
	s_nop 1
	v_cndmask_b32_e64 v84, 0, 1.0, vcc
	v_cmp_eq_u32_e32 vcc, v107, v149
	s_nop 1
	v_cndmask_b32_e64 v85, 0, 1.0, vcc
	v_cmp_eq_u32_e32 vcc, v108, v149
	s_waitcnt lgkmcnt(0)
	v_pk_fma_f32 v[62:63], v[82:83], v[62:63], v[84:85] op_sel_hi:[0,1,1] neg_lo:[1,0,0] neg_hi:[1,0,0]
	v_cvt_pk_bf16_f32 v62, v62, v63
	v_cndmask_b32_e64 v85, 0, 1.0, vcc
	v_cmp_eq_u32_e32 vcc, v109, v149
	s_nop 1
	v_cndmask_b32_e64 v84, 0, 1.0, vcc
	v_pk_fma_f32 v[64:65], v[82:83], v[64:65], v[84:85] op_sel_hi:[0,1,1] neg_lo:[1,0,0] neg_hi:[1,0,0]
	v_cvt_pk_bf16_f32 v63, v64, v65
	ds_write_b64 v186, v[62:63] offset:2176
	ds_read_b32 v62, v187 offset:40
	v_cmp_eq_u32_e32 vcc, v106, v148
	s_nop 1
	v_cndmask_b32_e64 v64, 0, 1.0, vcc
	v_cmp_eq_u32_e32 vcc, v107, v148
	s_nop 1
	v_cndmask_b32_e64 v65, 0, 1.0, vcc
	v_cmp_eq_u32_e32 vcc, v108, v148
	s_waitcnt lgkmcnt(0)
	v_pk_fma_f32 v[58:59], v[62:63], v[58:59], v[64:65] op_sel_hi:[0,1,1] neg_lo:[1,0,0] neg_hi:[1,0,0]
	v_cvt_pk_bf16_f32 v58, v58, v59
	v_cndmask_b32_e64 v65, 0, 1.0, vcc
	v_cmp_eq_u32_e32 vcc, v109, v148
	s_nop 1
	v_cndmask_b32_e64 v64, 0, 1.0, vcc
	v_pk_fma_f32 v[60:61], v[62:63], v[60:61], v[64:65] op_sel_hi:[0,1,1] neg_lo:[1,0,0] neg_hi:[1,0,0]
	v_cvt_pk_bf16_f32 v59, v60, v61
	ds_write_b64 v186, v[58:59] offset:2720
	ds_read_b32 v58, v187 offset:48
	v_cmp_eq_u32_e32 vcc, v106, v147
	s_nop 1
	v_cndmask_b32_e64 v60, 0, 1.0, vcc
	v_cmp_eq_u32_e32 vcc, v107, v147
	s_nop 1
	v_cndmask_b32_e64 v61, 0, 1.0, vcc
	v_cmp_eq_u32_e32 vcc, v108, v147
	s_waitcnt lgkmcnt(0)
	v_pk_fma_f32 v[54:55], v[58:59], v[54:55], v[60:61] op_sel_hi:[0,1,1] neg_lo:[1,0,0] neg_hi:[1,0,0]
	v_cvt_pk_bf16_f32 v54, v54, v55
	v_cndmask_b32_e64 v61, 0, 1.0, vcc
	v_cmp_eq_u32_e32 vcc, v109, v147
	s_nop 1
	v_cndmask_b32_e64 v60, 0, 1.0, vcc
	v_pk_fma_f32 v[56:57], v[58:59], v[56:57], v[60:61] op_sel_hi:[0,1,1] neg_lo:[1,0,0] neg_hi:[1,0,0]
	v_cvt_pk_bf16_f32 v55, v56, v57
	ds_write_b64 v186, v[54:55] offset:3264
	ds_read_b32 v54, v187 offset:56
	v_cmp_eq_u32_e32 vcc, v106, v146
	s_nop 1
	v_cndmask_b32_e64 v56, 0, 1.0, vcc
	v_cmp_eq_u32_e32 vcc, v107, v146
	s_nop 1
	v_cndmask_b32_e64 v57, 0, 1.0, vcc
	v_cmp_eq_u32_e32 vcc, v108, v146
	s_waitcnt lgkmcnt(0)
	v_pk_fma_f32 v[50:51], v[54:55], v[50:51], v[56:57] op_sel_hi:[0,1,1] neg_lo:[1,0,0] neg_hi:[1,0,0]
	v_cvt_pk_bf16_f32 v50, v50, v51
	v_cndmask_b32_e64 v57, 0, 1.0, vcc
	v_cmp_eq_u32_e32 vcc, v109, v146
	s_nop 1
	v_cndmask_b32_e64 v56, 0, 1.0, vcc
	v_pk_fma_f32 v[52:53], v[54:55], v[52:53], v[56:57] op_sel_hi:[0,1,1] neg_lo:[1,0,0] neg_hi:[1,0,0]
	v_cvt_pk_bf16_f32 v51, v52, v53
	ds_write_b64 v186, v[50:51] offset:3808
	ds_read_b128 v[50:53], v1
	ds_read_b128 v[54:57], v1 offset:64
	ds_read_b128 v[58:61], v1 offset:128
	ds_read_b128 v[62:65], v1 offset:192
	v_lshl_add_u64 v[82:83], v[168:169], 0, s[8:9]
	v_lshl_add_u64 v[84:85], v[170:171], 0, s[8:9]
	v_lshl_add_u64 v[86:87], v[172:173], 0, s[8:9]
	v_lshl_add_u64 v[88:89], v[174:175], 0, s[8:9]
	v_lshl_add_u64 v[94:95], v[176:177], 0, s[8:9]
	v_lshl_add_u64 v[96:97], v[178:179], 0, s[8:9]
	v_lshl_add_u64 v[122:123], v[180:181], 0, s[8:9]
	v_lshl_add_u64 v[124:125], v[182:183], 0, s[8:9]
	global_load_dwordx4 v[134:137], v[82:83], off nt
	global_load_dwordx4 v[118:121], v[84:85], off nt
	global_load_dwordx4 v[110:113], v[86:87], off nt
	global_load_dwordx4 v[106:109], v[88:89], off nt
	global_load_dwordx4 v[98:101], v[94:95], off nt
	s_nop 0
	global_load_dwordx4 v[94:97], v[96:97], off nt
	s_nop 0
	global_load_dwordx4 v[86:89], v[122:123], off nt
	global_load_dwordx4 v[82:85], v[124:125], off nt
	v_mov_b32_e32 v132, v189
	s_waitcnt vmcnt(15)
	s_waitcnt vmcnt(14)
	s_waitcnt vmcnt(13)
	s_waitcnt vmcnt(12)
	s_waitcnt vmcnt(11)
	s_waitcnt vmcnt(10)
	s_waitcnt vmcnt(9)
	s_waitcnt vmcnt(8)
	ds_read_b32 v122, v187 offset:64
	v_add_u32_e32 v133, 1, v132
	v_cmp_eq_u32_e32 vcc, v132, v138
	v_add_u32_e32 v146, 3, v132
	v_add_u32_e32 v147, 2, v132
	v_cndmask_b32_e64 v124, 0, 1.0, vcc
	v_cmp_eq_u32_e32 vcc, v133, v138
	s_nop 1
	v_cndmask_b32_e64 v125, 0, 1.0, vcc
	v_cmp_eq_u32_e32 vcc, v146, v138
	s_waitcnt lgkmcnt(0)
	v_pk_fma_f32 v[124:125], v[122:123], v[126:127], v[124:125] op_sel_hi:[0,1,1] neg_lo:[1,0,0] neg_hi:[1,0,0]
	v_cvt_pk_bf16_f32 v124, v124, v125
	v_cndmask_b32_e64 v127, 0, 1.0, vcc
	v_cmp_eq_u32_e32 vcc, v147, v138
	s_nop 1
	v_cndmask_b32_e64 v126, 0, 1.0, vcc
	v_pk_fma_f32 v[122:123], v[122:123], v[128:129], v[126:127] op_sel_hi:[0,1,1] neg_lo:[1,0,0] neg_hi:[1,0,0]
	v_cvt_pk_bf16_f32 v125, v122, v123
	ds_write_b64 v186, v[124:125]
	ds_read_b32 v122, v187 offset:72
	v_cmp_eq_u32_e32 vcc, v132, v139
	s_nop 1
	v_cndmask_b32_e64 v124, 0, 1.0, vcc
	v_cmp_eq_u32_e32 vcc, v133, v139
	s_nop 1
	v_cndmask_b32_e64 v125, 0, 1.0, vcc
	v_cmp_eq_u32_e32 vcc, v146, v139
	s_waitcnt lgkmcnt(0)
	v_pk_fma_f32 v[114:115], v[122:123], v[114:115], v[124:125] op_sel_hi:[0,1,1] neg_lo:[1,0,0] neg_hi:[1,0,0]
	v_cvt_pk_bf16_f32 v114, v114, v115
	v_cndmask_b32_e64 v125, 0, 1.0, vcc
	v_cmp_eq_u32_e32 vcc, v147, v139
	s_nop 1
	v_cndmask_b32_e64 v124, 0, 1.0, vcc
	v_pk_fma_f32 v[116:117], v[122:123], v[116:117], v[124:125] op_sel_hi:[0,1,1] neg_lo:[1,0,0] neg_hi:[1,0,0]
	v_cvt_pk_bf16_f32 v115, v116, v117
	ds_write_b64 v186, v[114:115] offset:544
	ds_read_b32 v114, v187 offset:80
	v_cmp_eq_u32_e32 vcc, v132, v140
	s_nop 1
	v_cndmask_b32_e64 v116, 0, 1.0, vcc
	v_cmp_eq_u32_e32 vcc, v133, v140
	s_nop 1
	v_cndmask_b32_e64 v117, 0, 1.0, vcc
	v_cmp_eq_u32_e32 vcc, v146, v140
	s_waitcnt lgkmcnt(0)
	v_pk_fma_f32 v[102:103], v[114:115], v[102:103], v[116:117] op_sel_hi:[0,1,1] neg_lo:[1,0,0] neg_hi:[1,0,0]
	v_cvt_pk_bf16_f32 v102, v102, v103
	v_cndmask_b32_e64 v117, 0, 1.0, vcc
	v_cmp_eq_u32_e32 vcc, v147, v140
	s_nop 1
	v_cndmask_b32_e64 v116, 0, 1.0, vcc
	v_pk_fma_f32 v[104:105], v[114:115], v[104:105], v[116:117] op_sel_hi:[0,1,1] neg_lo:[1,0,0] neg_hi:[1,0,0]
	v_cvt_pk_bf16_f32 v103, v104, v105
	ds_write_b64 v186, v[102:103] offset:1088
	ds_read_b32 v102, v187 offset:88
	v_cmp_eq_u32_e32 vcc, v132, v141
	s_nop 1
	v_cndmask_b32_e64 v104, 0, 1.0, vcc
	v_cmp_eq_u32_e32 vcc, v133, v141
	s_nop 1
	v_cndmask_b32_e64 v105, 0, 1.0, vcc
	v_cmp_eq_u32_e32 vcc, v146, v141
	s_waitcnt lgkmcnt(0)
	v_pk_fma_f32 v[90:91], v[102:103], v[90:91], v[104:105] op_sel_hi:[0,1,1] neg_lo:[1,0,0] neg_hi:[1,0,0]
	v_cvt_pk_bf16_f32 v90, v90, v91
	v_cndmask_b32_e64 v105, 0, 1.0, vcc
	v_cmp_eq_u32_e32 vcc, v147, v141
	s_nop 1
	v_cndmask_b32_e64 v104, 0, 1.0, vcc
	v_pk_fma_f32 v[92:93], v[102:103], v[92:93], v[104:105] op_sel_hi:[0,1,1] neg_lo:[1,0,0] neg_hi:[1,0,0]
	v_cvt_pk_bf16_f32 v91, v92, v93
	ds_write_b64 v186, v[90:91] offset:1632
	ds_read_b32 v90, v187 offset:96
	v_cmp_eq_u32_e32 vcc, v132, v142
	s_nop 1
	v_cndmask_b32_e64 v92, 0, 1.0, vcc
	v_cmp_eq_u32_e32 vcc, v133, v142
	s_nop 1
	v_cndmask_b32_e64 v93, 0, 1.0, vcc
	v_cmp_eq_u32_e32 vcc, v146, v142
	s_waitcnt lgkmcnt(0)
	v_pk_fma_f32 v[78:79], v[90:91], v[78:79], v[92:93] op_sel_hi:[0,1,1] neg_lo:[1,0,0] neg_hi:[1,0,0]
	v_cvt_pk_bf16_f32 v78, v78, v79
	v_cndmask_b32_e64 v93, 0, 1.0, vcc
	v_cmp_eq_u32_e32 vcc, v147, v142
	s_nop 1
	v_cndmask_b32_e64 v92, 0, 1.0, vcc
	v_pk_fma_f32 v[80:81], v[90:91], v[80:81], v[92:93] op_sel_hi:[0,1,1] neg_lo:[1,0,0] neg_hi:[1,0,0]
	v_cvt_pk_bf16_f32 v79, v80, v81
	ds_write_b64 v186, v[78:79] offset:2176
	ds_read_b32 v78, v187 offset:104
	v_cmp_eq_u32_e32 vcc, v132, v143
	s_nop 1
	v_cndmask_b32_e64 v80, 0, 1.0, vcc
	v_cmp_eq_u32_e32 vcc, v133, v143
	s_nop 1
	v_cndmask_b32_e64 v81, 0, 1.0, vcc
	v_cmp_eq_u32_e32 vcc, v146, v143
	s_waitcnt lgkmcnt(0)
	v_pk_fma_f32 v[74:75], v[78:79], v[74:75], v[80:81] op_sel_hi:[0,1,1] neg_lo:[1,0,0] neg_hi:[1,0,0]
	v_cvt_pk_bf16_f32 v74, v74, v75
	v_cndmask_b32_e64 v81, 0, 1.0, vcc
	v_cmp_eq_u32_e32 vcc, v147, v143
	s_nop 1
	v_cndmask_b32_e64 v80, 0, 1.0, vcc
	v_pk_fma_f32 v[76:77], v[78:79], v[76:77], v[80:81] op_sel_hi:[0,1,1] neg_lo:[1,0,0] neg_hi:[1,0,0]
	v_cvt_pk_bf16_f32 v75, v76, v77
	ds_write_b64 v186, v[74:75] offset:2720
	ds_read_b32 v74, v187 offset:112
	v_cmp_eq_u32_e32 vcc, v132, v144
	s_nop 1
	v_cndmask_b32_e64 v76, 0, 1.0, vcc
	v_cmp_eq_u32_e32 vcc, v133, v144
	s_nop 1
	v_cndmask_b32_e64 v77, 0, 1.0, vcc
	v_cmp_eq_u32_e32 vcc, v146, v144
	s_waitcnt lgkmcnt(0)
	v_pk_fma_f32 v[70:71], v[74:75], v[70:71], v[76:77] op_sel_hi:[0,1,1] neg_lo:[1,0,0] neg_hi:[1,0,0]
	v_cvt_pk_bf16_f32 v70, v70, v71
	v_cndmask_b32_e64 v77, 0, 1.0, vcc
	v_cmp_eq_u32_e32 vcc, v147, v144
	s_nop 1
	v_cndmask_b32_e64 v76, 0, 1.0, vcc
	v_pk_fma_f32 v[72:73], v[74:75], v[72:73], v[76:77] op_sel_hi:[0,1,1] neg_lo:[1,0,0] neg_hi:[1,0,0]
	v_cvt_pk_bf16_f32 v71, v72, v73
	ds_write_b64 v186, v[70:71] offset:3264
	ds_read_b32 v70, v187 offset:120
	v_cmp_eq_u32_e32 vcc, v132, v145
	s_nop 1
	v_cndmask_b32_e64 v72, 0, 1.0, vcc
	v_cmp_eq_u32_e32 vcc, v133, v145
	s_nop 1
	v_cndmask_b32_e64 v73, 0, 1.0, vcc
	v_cmp_eq_u32_e32 vcc, v146, v145
	s_waitcnt lgkmcnt(0)
	v_pk_fma_f32 v[66:67], v[70:71], v[66:67], v[72:73] op_sel_hi:[0,1,1] neg_lo:[1,0,0] neg_hi:[1,0,0]
	v_cvt_pk_bf16_f32 v66, v66, v67
	v_cndmask_b32_e64 v73, 0, 1.0, vcc
	v_cmp_eq_u32_e32 vcc, v147, v145
	s_nop 1
	v_cndmask_b32_e64 v72, 0, 1.0, vcc
	v_pk_fma_f32 v[68:69], v[70:71], v[68:69], v[72:73] op_sel_hi:[0,1,1] neg_lo:[1,0,0] neg_hi:[1,0,0]
	v_cvt_pk_bf16_f32 v67, v68, v69
	ds_write_b64 v186, v[66:67] offset:3808
	ds_read_b128 v[66:69], v1
	ds_read_b128 v[70:73], v1 offset:64
	ds_read_b128 v[74:77], v1 offset:128
	ds_read_b128 v[78:81], v1 offset:192
	v_lshl_add_u64 v[90:91], v[130:131], 0, s[0:1]
	v_add_co_u32_e32 v92, vcc, s7, v90
	s_nop 1
	v_addc_co_u32_e32 v93, vcc, 0, v91, vcc
	global_load_dwordx4 v[146:149], v[90:91], off nt
	global_load_dwordx4 v[142:145], v[92:93], off nt
	v_add_co_u32_e32 v92, vcc, s36, v90
	s_nop 1
	v_addc_co_u32_e32 v93, vcc, 0, v91, vcc
	v_add_co_u32_e32 v102, vcc, s37, v90
	s_nop 1
	v_addc_co_u32_e32 v103, vcc, 0, v91, vcc
	global_load_dwordx4 v[138:141], v[92:93], off nt
	global_load_dwordx4 v[130:133], v[102:103], off nt
	v_add_co_u32_e32 v92, vcc, s38, v90
	s_nop 1
	v_addc_co_u32_e32 v93, vcc, 0, v91, vcc
	v_add_co_u32_e32 v102, vcc, s39, v90
	s_nop 1
	v_addc_co_u32_e32 v103, vcc, 0, v91, vcc
	global_load_dwordx4 v[126:129], v[92:93], off nt
	global_load_dwordx4 v[122:125], v[102:103], off nt
	v_add_co_u32_e32 v92, vcc, s41, v90
	s_nop 1
	v_addc_co_u32_e32 v93, vcc, 0, v91, vcc
	v_add_co_u32_e32 v90, vcc, s42, v90
	s_nop 1
	v_addc_co_u32_e32 v91, vcc, 0, v91, vcc
	global_load_dwordx4 v[114:117], v[92:93], off nt
	global_load_dwordx4 v[102:105], v[90:91], off nt
	s_waitcnt vmcnt(15)
	s_waitcnt vmcnt(14)
	s_waitcnt vmcnt(13)
	s_waitcnt vmcnt(12)
	s_waitcnt vmcnt(11)
	s_waitcnt vmcnt(10)
	s_waitcnt vmcnt(9)
	s_waitcnt vmcnt(8)
	ds_read_b32 v90, v187 offset:128
	v_add_u32_e32 v190, 1, v189
	v_cmp_eq_u32_e32 vcc, v189, v194
	v_add_u32_e32 v192, 3, v189
	v_add_u32_e32 v193, 2, v189
	v_cndmask_b32_e64 v92, 0, 1.0, vcc
	v_cmp_eq_u32_e32 vcc, v190, v194
	s_nop 1
	v_cndmask_b32_e64 v93, 0, 1.0, vcc
	v_cmp_eq_u32_e32 vcc, v192, v194
	s_waitcnt lgkmcnt(0)
	v_pk_fma_f32 v[92:93], v[90:91], v[134:135], v[92:93] op_sel_hi:[0,1,1] neg_lo:[1,0,0] neg_hi:[1,0,0]
	v_cvt_pk_bf16_f32 v92, v92, v93
	v_cndmask_b32_e64 v135, 0, 1.0, vcc
	v_cmp_eq_u32_e32 vcc, v193, v194
	s_nop 1
	v_cndmask_b32_e64 v134, 0, 1.0, vcc
	v_pk_fma_f32 v[90:91], v[90:91], v[136:137], v[134:135] op_sel_hi:[0,1,1] neg_lo:[1,0,0] neg_hi:[1,0,0]
	v_cvt_pk_bf16_f32 v93, v90, v91
	ds_write_b64 v186, v[92:93]
	ds_read_b32 v90, v187 offset:136
	v_cmp_eq_u32_e32 vcc, v189, v195
	s_nop 1
	v_cndmask_b32_e64 v92, 0, 1.0, vcc
	v_cmp_eq_u32_e32 vcc, v190, v195
	s_nop 1
	v_cndmask_b32_e64 v93, 0, 1.0, vcc
	v_cmp_eq_u32_e32 vcc, v192, v195
	s_waitcnt lgkmcnt(0)
	v_pk_fma_f32 v[92:93], v[90:91], v[118:119], v[92:93] op_sel_hi:[0,1,1] neg_lo:[1,0,0] neg_hi:[1,0,0]
	v_cvt_pk_bf16_f32 v92, v92, v93
	v_cndmask_b32_e64 v119, 0, 1.0, vcc
	v_cmp_eq_u32_e32 vcc, v193, v195
	s_nop 1
	v_cndmask_b32_e64 v118, 0, 1.0, vcc
	v_pk_fma_f32 v[90:91], v[90:91], v[120:121], v[118:119] op_sel_hi:[0,1,1] neg_lo:[1,0,0] neg_hi:[1,0,0]
	v_cvt_pk_bf16_f32 v93, v90, v91
	ds_write_b64 v186, v[92:93] offset:544
	ds_read_b32 v90, v187 offset:144
	v_cmp_eq_u32_e32 vcc, v189, v196
	s_nop 1
	v_cndmask_b32_e64 v92, 0, 1.0, vcc
	v_cmp_eq_u32_e32 vcc, v190, v196
	s_nop 1
	v_cndmask_b32_e64 v93, 0, 1.0, vcc
	v_cmp_eq_u32_e32 vcc, v192, v196
	s_waitcnt lgkmcnt(0)
	v_pk_fma_f32 v[92:93], v[90:91], v[110:111], v[92:93] op_sel_hi:[0,1,1] neg_lo:[1,0,0] neg_hi:[1,0,0]
	v_cvt_pk_bf16_f32 v92, v92, v93
	v_cndmask_b32_e64 v111, 0, 1.0, vcc
	v_cmp_eq_u32_e32 vcc, v193, v196
	s_nop 1
	v_cndmask_b32_e64 v110, 0, 1.0, vcc
	v_pk_fma_f32 v[90:91], v[90:91], v[112:113], v[110:111] op_sel_hi:[0,1,1] neg_lo:[1,0,0] neg_hi:[1,0,0]
	v_cvt_pk_bf16_f32 v93, v90, v91
	ds_write_b64 v186, v[92:93] offset:1088
	ds_read_b32 v90, v187 offset:152
	v_cmp_eq_u32_e32 vcc, v189, v197
	s_nop 1
	v_cndmask_b32_e64 v92, 0, 1.0, vcc
	v_cmp_eq_u32_e32 vcc, v190, v197
	s_nop 1
	v_cndmask_b32_e64 v93, 0, 1.0, vcc
	v_cmp_eq_u32_e32 vcc, v192, v197
	s_waitcnt lgkmcnt(0)
	v_pk_fma_f32 v[92:93], v[90:91], v[106:107], v[92:93] op_sel_hi:[0,1,1] neg_lo:[1,0,0] neg_hi:[1,0,0]
	v_cvt_pk_bf16_f32 v92, v92, v93
	v_cndmask_b32_e64 v107, 0, 1.0, vcc
	v_cmp_eq_u32_e32 vcc, v193, v197
	s_nop 1
	v_cndmask_b32_e64 v106, 0, 1.0, vcc
	v_pk_fma_f32 v[90:91], v[90:91], v[108:109], v[106:107] op_sel_hi:[0,1,1] neg_lo:[1,0,0] neg_hi:[1,0,0]
	v_cvt_pk_bf16_f32 v93, v90, v91
	ds_write_b64 v186, v[92:93] offset:1632
	ds_read_b32 v90, v187 offset:160
	v_cmp_eq_u32_e32 vcc, v189, v198
	s_nop 1
	v_cndmask_b32_e64 v92, 0, 1.0, vcc
	v_cmp_eq_u32_e32 vcc, v190, v198
	s_nop 1
	v_cndmask_b32_e64 v93, 0, 1.0, vcc
	v_cmp_eq_u32_e32 vcc, v192, v198
	s_waitcnt lgkmcnt(0)
	v_pk_fma_f32 v[92:93], v[90:91], v[98:99], v[92:93] op_sel_hi:[0,1,1] neg_lo:[1,0,0] neg_hi:[1,0,0]
	v_cvt_pk_bf16_f32 v92, v92, v93
	v_cndmask_b32_e64 v99, 0, 1.0, vcc
	v_cmp_eq_u32_e32 vcc, v193, v198
	s_nop 1
	v_cndmask_b32_e64 v98, 0, 1.0, vcc
	v_pk_fma_f32 v[90:91], v[90:91], v[100:101], v[98:99] op_sel_hi:[0,1,1] neg_lo:[1,0,0] neg_hi:[1,0,0]
	v_cvt_pk_bf16_f32 v93, v90, v91
	ds_write_b64 v186, v[92:93] offset:2176
	ds_read_b32 v90, v187 offset:168
	v_cmp_eq_u32_e32 vcc, v189, v199
	s_nop 1
	v_cndmask_b32_e64 v92, 0, 1.0, vcc
	v_cmp_eq_u32_e32 vcc, v190, v199
	s_nop 1
	v_cndmask_b32_e64 v93, 0, 1.0, vcc
	v_cmp_eq_u32_e32 vcc, v192, v199
	s_waitcnt lgkmcnt(0)
	v_pk_fma_f32 v[92:93], v[90:91], v[94:95], v[92:93] op_sel_hi:[0,1,1] neg_lo:[1,0,0] neg_hi:[1,0,0]
	v_cvt_pk_bf16_f32 v92, v92, v93
	v_cndmask_b32_e64 v95, 0, 1.0, vcc
	v_cmp_eq_u32_e32 vcc, v193, v199
	s_nop 1
	v_cndmask_b32_e64 v94, 0, 1.0, vcc
	v_pk_fma_f32 v[90:91], v[90:91], v[96:97], v[94:95] op_sel_hi:[0,1,1] neg_lo:[1,0,0] neg_hi:[1,0,0]
	v_cvt_pk_bf16_f32 v93, v90, v91
	ds_write_b64 v186, v[92:93] offset:2720
	ds_read_b32 v90, v187 offset:176
	v_cmp_eq_u32_e32 vcc, v189, v200
	s_nop 1
	v_cndmask_b32_e64 v92, 0, 1.0, vcc
	v_cmp_eq_u32_e32 vcc, v190, v200
	s_nop 1
	v_cndmask_b32_e64 v93, 0, 1.0, vcc
	v_cmp_eq_u32_e32 vcc, v192, v200
	s_waitcnt lgkmcnt(0)
	v_pk_fma_f32 v[86:87], v[90:91], v[86:87], v[92:93] op_sel_hi:[0,1,1] neg_lo:[1,0,0] neg_hi:[1,0,0]
	v_cvt_pk_bf16_f32 v86, v86, v87
	v_cndmask_b32_e64 v93, 0, 1.0, vcc
	v_cmp_eq_u32_e32 vcc, v193, v200
	s_nop 1
	v_cndmask_b32_e64 v92, 0, 1.0, vcc
	v_pk_fma_f32 v[88:89], v[90:91], v[88:89], v[92:93] op_sel_hi:[0,1,1] neg_lo:[1,0,0] neg_hi:[1,0,0]
	v_cvt_pk_bf16_f32 v87, v88, v89
	ds_write_b64 v186, v[86:87] offset:3264
	ds_read_b32 v86, v187 offset:184
	v_cmp_eq_u32_e32 vcc, v189, v201
	s_nop 1
	v_cndmask_b32_e64 v88, 0, 1.0, vcc
	v_cmp_eq_u32_e32 vcc, v190, v201
	s_nop 1
	v_cndmask_b32_e64 v89, 0, 1.0, vcc
	v_cmp_eq_u32_e32 vcc, v192, v201
	s_waitcnt lgkmcnt(0)
	v_pk_fma_f32 v[82:83], v[86:87], v[82:83], v[88:89] op_sel_hi:[0,1,1] neg_lo:[1,0,0] neg_hi:[1,0,0]
	v_cvt_pk_bf16_f32 v82, v82, v83
	v_cndmask_b32_e64 v89, 0, 1.0, vcc
	v_cmp_eq_u32_e32 vcc, v193, v201
	s_nop 1
	v_cndmask_b32_e64 v88, 0, 1.0, vcc
	v_pk_fma_f32 v[84:85], v[86:87], v[84:85], v[88:89] op_sel_hi:[0,1,1] neg_lo:[1,0,0] neg_hi:[1,0,0]
	v_cvt_pk_bf16_f32 v83, v84, v85
	ds_write_b64 v186, v[82:83] offset:3808
	ds_read_b128 v[82:85], v1
	ds_read_b128 v[86:89], v1 offset:64
	ds_read_b128 v[90:93], v1 offset:128
	ds_read_b128 v[94:97], v1 offset:192
	v_lshl_add_u64 v[98:99], v[150:151], 0, s[0:1]
	v_lshl_add_u64 v[192:193], v[164:165], 0, s[0:1]
	v_lshl_add_u64 v[196:197], v[166:167], 0, s[0:1]
	v_lshl_add_u64 v[100:101], v[152:153], 0, s[0:1]
	v_lshl_add_u64 v[106:107], v[156:157], 0, s[0:1]
	v_lshl_add_u64 v[108:109], v[158:159], 0, s[0:1]
	v_lshl_add_u64 v[110:111], v[160:161], 0, s[0:1]
	v_lshl_add_u64 v[112:113], v[162:163], 0, s[0:1]
	global_load_dwordx4 v[118:121], v[98:99], off nt
	global_load_dwordx4 v[134:137], v[100:101], off nt
	global_load_dwordx4 v[150:153], v[106:107], off nt
	global_load_dwordx4 v[156:159], v[108:109], off nt
	global_load_dwordx4 v[160:163], v[110:111], off nt
	global_load_dwordx4 v[164:167], v[112:113], off nt
	s_nop 0
	global_load_dwordx4 v[192:195], v[192:193], off nt
	s_nop 0
	global_load_dwordx4 v[196:199], v[196:197], off nt
	v_mov_b32_e32 v98, v188
	s_waitcnt vmcnt(15)
	s_waitcnt vmcnt(14)
	s_waitcnt vmcnt(13)
	s_waitcnt vmcnt(12)
	s_waitcnt vmcnt(11)
	s_waitcnt vmcnt(10)
	s_waitcnt vmcnt(9)
	s_waitcnt vmcnt(8)
	ds_read_b32 v98, v187
	s_waitcnt lgkmcnt(0)
	v_pk_fma_f32 v[100:101], v[98:99], v[146:147], 0 op_sel_hi:[0,1,0] neg_lo:[1,0,0] neg_hi:[1,0,0]
	v_pk_fma_f32 v[98:99], v[98:99], v[148:149], 0 op_sel_hi:[0,1,0] neg_lo:[1,0,0] neg_hi:[1,0,0]
	v_cvt_pk_bf16_f32 v100, v100, v101
	v_cvt_pk_bf16_f32 v101, v98, v99
	ds_write_b64 v186, v[100:101]
	ds_read_b32 v98, v187 offset:8
	s_waitcnt lgkmcnt(0)
	v_pk_fma_f32 v[100:101], v[98:99], v[142:143], 0 op_sel_hi:[0,1,0] neg_lo:[1,0,0] neg_hi:[1,0,0]
	v_pk_fma_f32 v[98:99], v[98:99], v[144:145], 0 op_sel_hi:[0,1,0] neg_lo:[1,0,0] neg_hi:[1,0,0]
	v_cvt_pk_bf16_f32 v100, v100, v101
	v_cvt_pk_bf16_f32 v101, v98, v99
	ds_write_b64 v186, v[100:101] offset:544
	ds_read_b32 v98, v187 offset:16
	s_waitcnt lgkmcnt(0)
	v_pk_fma_f32 v[100:101], v[98:99], v[138:139], 0 op_sel_hi:[0,1,0] neg_lo:[1,0,0] neg_hi:[1,0,0]
	v_pk_fma_f32 v[98:99], v[98:99], v[140:141], 0 op_sel_hi:[0,1,0] neg_lo:[1,0,0] neg_hi:[1,0,0]
	v_cvt_pk_bf16_f32 v100, v100, v101
	v_cvt_pk_bf16_f32 v101, v98, v99
	ds_write_b64 v186, v[100:101] offset:1088
	ds_read_b32 v98, v187 offset:24
	s_waitcnt lgkmcnt(0)
	v_pk_fma_f32 v[100:101], v[98:99], v[130:131], 0 op_sel_hi:[0,1,0] neg_lo:[1,0,0] neg_hi:[1,0,0]
	v_pk_fma_f32 v[98:99], v[98:99], v[132:133], 0 op_sel_hi:[0,1,0] neg_lo:[1,0,0] neg_hi:[1,0,0]
	v_cvt_pk_bf16_f32 v100, v100, v101
	v_cvt_pk_bf16_f32 v101, v98, v99
	ds_write_b64 v186, v[100:101] offset:1632
	ds_read_b32 v98, v187 offset:32
	s_waitcnt lgkmcnt(0)
	v_pk_fma_f32 v[100:101], v[98:99], v[126:127], 0 op_sel_hi:[0,1,0] neg_lo:[1,0,0] neg_hi:[1,0,0]
	v_pk_fma_f32 v[98:99], v[98:99], v[128:129], 0 op_sel_hi:[0,1,0] neg_lo:[1,0,0] neg_hi:[1,0,0]
	v_cvt_pk_bf16_f32 v100, v100, v101
	v_cvt_pk_bf16_f32 v101, v98, v99
	ds_write_b64 v186, v[100:101] offset:2176
	ds_read_b32 v98, v187 offset:40
	s_waitcnt lgkmcnt(0)
	v_pk_fma_f32 v[100:101], v[98:99], v[122:123], 0 op_sel_hi:[0,1,0] neg_lo:[1,0,0] neg_hi:[1,0,0]
	v_pk_fma_f32 v[98:99], v[98:99], v[124:125], 0 op_sel_hi:[0,1,0] neg_lo:[1,0,0] neg_hi:[1,0,0]
	v_cvt_pk_bf16_f32 v100, v100, v101
	v_cvt_pk_bf16_f32 v101, v98, v99
	ds_write_b64 v186, v[100:101] offset:2720
	ds_read_b32 v98, v187 offset:48
	s_waitcnt lgkmcnt(0)
	v_pk_fma_f32 v[100:101], v[98:99], v[114:115], 0 op_sel_hi:[0,1,0] neg_lo:[1,0,0] neg_hi:[1,0,0]
	v_pk_fma_f32 v[98:99], v[98:99], v[116:117], 0 op_sel_hi:[0,1,0] neg_lo:[1,0,0] neg_hi:[1,0,0]
	v_cvt_pk_bf16_f32 v100, v100, v101
	v_cvt_pk_bf16_f32 v101, v98, v99
	ds_write_b64 v186, v[100:101] offset:3264
	ds_read_b32 v98, v187 offset:56
	s_waitcnt lgkmcnt(0)
	v_pk_fma_f32 v[100:101], v[98:99], v[102:103], 0 op_sel_hi:[0,1,0] neg_lo:[1,0,0] neg_hi:[1,0,0]
	v_pk_fma_f32 v[98:99], v[98:99], v[104:105], 0 op_sel_hi:[0,1,0] neg_lo:[1,0,0] neg_hi:[1,0,0]
	v_cvt_pk_bf16_f32 v100, v100, v101
	v_cvt_pk_bf16_f32 v101, v98, v99
	ds_write_b64 v186, v[100:101] offset:3808
	ds_read_b128 v[98:101], v1
	ds_read_b128 v[102:105], v1 offset:64
	ds_read_b128 v[106:109], v1 offset:128
	ds_read_b128 v[110:113], v1 offset:192
	v_lshl_add_u64 v[114:115], v[168:169], 0, s[0:1]
	v_lshl_add_u64 v[126:127], v[176:177], 0, s[0:1]
	v_lshl_add_u64 v[176:177], v[180:181], 0, s[0:1]
	v_lshl_add_u64 v[180:181], v[182:183], 0, s[0:1]
	v_lshl_add_u64 v[116:117], v[170:171], 0, s[0:1]
	v_lshl_add_u64 v[122:123], v[172:173], 0, s[0:1]
	v_lshl_add_u64 v[124:125], v[174:175], 0, s[0:1]
	v_lshl_add_u64 v[128:129], v[178:179], 0, s[0:1]
	global_load_dwordx4 v[130:133], v[114:115], off nt
	global_load_dwordx4 v[138:141], v[116:117], off nt
	global_load_dwordx4 v[142:145], v[122:123], off nt
	global_load_dwordx4 v[146:149], v[124:125], off nt
	global_load_dwordx4 v[168:171], v[126:127], off nt
	global_load_dwordx4 v[172:175], v[128:129], off nt
	s_nop 0
	global_load_dwordx4 v[176:179], v[176:177], off nt
	s_nop 0
	global_load_dwordx4 v[180:183], v[180:181], off nt
	v_mov_b32_e32 v114, v188
	s_waitcnt vmcnt(15)
	s_waitcnt vmcnt(14)
	s_waitcnt vmcnt(13)
	s_waitcnt vmcnt(12)
	s_waitcnt vmcnt(11)
	s_waitcnt vmcnt(10)
	s_waitcnt vmcnt(9)
	s_waitcnt vmcnt(8)
	ds_read_b32 v114, v187 offset:64
	s_waitcnt lgkmcnt(0)
	v_pk_fma_f32 v[116:117], v[114:115], v[118:119], 0 op_sel_hi:[0,1,0] neg_lo:[1,0,0] neg_hi:[1,0,0]
	v_pk_fma_f32 v[114:115], v[114:115], v[120:121], 0 op_sel_hi:[0,1,0] neg_lo:[1,0,0] neg_hi:[1,0,0]
	v_cvt_pk_bf16_f32 v116, v116, v117
	v_cvt_pk_bf16_f32 v117, v114, v115
	ds_write_b64 v186, v[116:117]
	ds_read_b32 v114, v187 offset:72
	s_waitcnt lgkmcnt(0)
	v_pk_fma_f32 v[116:117], v[114:115], v[134:135], 0 op_sel_hi:[0,1,0] neg_lo:[1,0,0] neg_hi:[1,0,0]
	v_pk_fma_f32 v[114:115], v[114:115], v[136:137], 0 op_sel_hi:[0,1,0] neg_lo:[1,0,0] neg_hi:[1,0,0]
	v_cvt_pk_bf16_f32 v116, v116, v117
	v_cvt_pk_bf16_f32 v117, v114, v115
	ds_write_b64 v186, v[116:117] offset:544
	ds_read_b32 v114, v187 offset:80
	s_waitcnt lgkmcnt(0)
	v_pk_fma_f32 v[116:117], v[114:115], v[150:151], 0 op_sel_hi:[0,1,0] neg_lo:[1,0,0] neg_hi:[1,0,0]
	v_pk_fma_f32 v[114:115], v[114:115], v[152:153], 0 op_sel_hi:[0,1,0] neg_lo:[1,0,0] neg_hi:[1,0,0]
	v_cvt_pk_bf16_f32 v116, v116, v117
	v_cvt_pk_bf16_f32 v117, v114, v115
	ds_write_b64 v186, v[116:117] offset:1088
	ds_read_b32 v114, v187 offset:88
	s_waitcnt lgkmcnt(0)
	v_pk_fma_f32 v[116:117], v[114:115], v[156:157], 0 op_sel_hi:[0,1,0] neg_lo:[1,0,0] neg_hi:[1,0,0]
	v_pk_fma_f32 v[114:115], v[114:115], v[158:159], 0 op_sel_hi:[0,1,0] neg_lo:[1,0,0] neg_hi:[1,0,0]
	v_cvt_pk_bf16_f32 v116, v116, v117
	v_cvt_pk_bf16_f32 v117, v114, v115
	ds_write_b64 v186, v[116:117] offset:1632
	ds_read_b32 v114, v187 offset:96
	s_waitcnt lgkmcnt(0)
	v_pk_fma_f32 v[116:117], v[114:115], v[160:161], 0 op_sel_hi:[0,1,0] neg_lo:[1,0,0] neg_hi:[1,0,0]
	v_pk_fma_f32 v[114:115], v[114:115], v[162:163], 0 op_sel_hi:[0,1,0] neg_lo:[1,0,0] neg_hi:[1,0,0]
	v_cvt_pk_bf16_f32 v116, v116, v117
	v_cvt_pk_bf16_f32 v117, v114, v115
	ds_write_b64 v186, v[116:117] offset:2176
	ds_read_b32 v114, v187 offset:104
	s_waitcnt lgkmcnt(0)
	v_pk_fma_f32 v[116:117], v[114:115], v[164:165], 0 op_sel_hi:[0,1,0] neg_lo:[1,0,0] neg_hi:[1,0,0]
	v_pk_fma_f32 v[114:115], v[114:115], v[166:167], 0 op_sel_hi:[0,1,0] neg_lo:[1,0,0] neg_hi:[1,0,0]
	v_cvt_pk_bf16_f32 v116, v116, v117
	v_cvt_pk_bf16_f32 v117, v114, v115
	ds_write_b64 v186, v[116:117] offset:2720
	ds_read_b32 v114, v187 offset:112
	s_waitcnt lgkmcnt(0)
	v_pk_fma_f32 v[116:117], v[114:115], v[192:193], 0 op_sel_hi:[0,1,0] neg_lo:[1,0,0] neg_hi:[1,0,0]
	v_pk_fma_f32 v[114:115], v[114:115], v[194:195], 0 op_sel_hi:[0,1,0] neg_lo:[1,0,0] neg_hi:[1,0,0]
	v_cvt_pk_bf16_f32 v116, v116, v117
	v_cvt_pk_bf16_f32 v117, v114, v115
	ds_write_b64 v186, v[116:117] offset:3264
	ds_read_b32 v114, v187 offset:120
	s_waitcnt lgkmcnt(0)
	v_pk_fma_f32 v[116:117], v[114:115], v[196:197], 0 op_sel_hi:[0,1,0] neg_lo:[1,0,0] neg_hi:[1,0,0]
	v_pk_fma_f32 v[114:115], v[114:115], v[198:199], 0 op_sel_hi:[0,1,0] neg_lo:[1,0,0] neg_hi:[1,0,0]
	v_cvt_pk_bf16_f32 v116, v116, v117
	v_cvt_pk_bf16_f32 v117, v114, v115
	ds_write_b64 v186, v[116:117] offset:3808
	ds_read_b128 v[114:117], v1
	ds_read_b128 v[118:121], v1 offset:64
	ds_read_b128 v[122:125], v1 offset:128
	ds_read_b128 v[126:129], v1 offset:192
	s_waitcnt vmcnt(7)
	s_waitcnt vmcnt(6)
	s_waitcnt vmcnt(5)
	s_waitcnt vmcnt(4)
	s_waitcnt vmcnt(3)
	s_waitcnt vmcnt(2)
	s_waitcnt vmcnt(1)
	s_waitcnt vmcnt(0)
	ds_read_b32 v134, v187 offset:128
	s_waitcnt lgkmcnt(0)
	v_pk_fma_f32 v[130:131], v[134:135], v[130:131], 0 op_sel_hi:[0,1,0] neg_lo:[1,0,0] neg_hi:[1,0,0]
	v_pk_fma_f32 v[132:133], v[134:135], v[132:133], 0 op_sel_hi:[0,1,0] neg_lo:[1,0,0] neg_hi:[1,0,0]
	v_cvt_pk_bf16_f32 v130, v130, v131
	v_cvt_pk_bf16_f32 v131, v132, v133
	ds_write_b64 v186, v[130:131]
	ds_read_b32 v130, v187 offset:136
	s_waitcnt lgkmcnt(0)
	v_pk_fma_f32 v[132:133], v[130:131], v[138:139], 0 op_sel_hi:[0,1,0] neg_lo:[1,0,0] neg_hi:[1,0,0]
	v_pk_fma_f32 v[130:131], v[130:131], v[140:141], 0 op_sel_hi:[0,1,0] neg_lo:[1,0,0] neg_hi:[1,0,0]
	v_cvt_pk_bf16_f32 v132, v132, v133
	v_cvt_pk_bf16_f32 v133, v130, v131
	ds_write_b64 v186, v[132:133] offset:544
	ds_read_b32 v130, v187 offset:144
	s_waitcnt lgkmcnt(0)
	v_pk_fma_f32 v[132:133], v[130:131], v[142:143], 0 op_sel_hi:[0,1,0] neg_lo:[1,0,0] neg_hi:[1,0,0]
	v_pk_fma_f32 v[130:131], v[130:131], v[144:145], 0 op_sel_hi:[0,1,0] neg_lo:[1,0,0] neg_hi:[1,0,0]
	v_cvt_pk_bf16_f32 v132, v132, v133
	v_cvt_pk_bf16_f32 v133, v130, v131
	ds_write_b64 v186, v[132:133] offset:1088
	ds_read_b32 v130, v187 offset:152
	s_waitcnt lgkmcnt(0)
	v_pk_fma_f32 v[132:133], v[130:131], v[146:147], 0 op_sel_hi:[0,1,0] neg_lo:[1,0,0] neg_hi:[1,0,0]
	v_pk_fma_f32 v[130:131], v[130:131], v[148:149], 0 op_sel_hi:[0,1,0] neg_lo:[1,0,0] neg_hi:[1,0,0]
	v_cvt_pk_bf16_f32 v132, v132, v133
	v_cvt_pk_bf16_f32 v133, v130, v131
	ds_write_b64 v186, v[132:133] offset:1632
	ds_read_b32 v130, v187 offset:160
	s_waitcnt lgkmcnt(0)
	v_pk_fma_f32 v[132:133], v[130:131], v[168:169], 0 op_sel_hi:[0,1,0] neg_lo:[1,0,0] neg_hi:[1,0,0]
	v_pk_fma_f32 v[130:131], v[130:131], v[170:171], 0 op_sel_hi:[0,1,0] neg_lo:[1,0,0] neg_hi:[1,0,0]
	v_cvt_pk_bf16_f32 v132, v132, v133
	v_cvt_pk_bf16_f32 v133, v130, v131
	ds_write_b64 v186, v[132:133] offset:2176
	ds_read_b32 v130, v187 offset:168
	s_waitcnt lgkmcnt(0)
	v_pk_fma_f32 v[132:133], v[130:131], v[172:173], 0 op_sel_hi:[0,1,0] neg_lo:[1,0,0] neg_hi:[1,0,0]
	v_pk_fma_f32 v[130:131], v[130:131], v[174:175], 0 op_sel_hi:[0,1,0] neg_lo:[1,0,0] neg_hi:[1,0,0]
	v_cvt_pk_bf16_f32 v132, v132, v133
	v_cvt_pk_bf16_f32 v133, v130, v131
	ds_write_b64 v186, v[132:133] offset:2720
	ds_read_b32 v130, v187 offset:176
	s_waitcnt lgkmcnt(0)
	v_pk_fma_f32 v[132:133], v[130:131], v[176:177], 0 op_sel_hi:[0,1,0] neg_lo:[1,0,0] neg_hi:[1,0,0]
	v_pk_fma_f32 v[130:131], v[130:131], v[178:179], 0 op_sel_hi:[0,1,0] neg_lo:[1,0,0] neg_hi:[1,0,0]
	v_cvt_pk_bf16_f32 v132, v132, v133
	v_cvt_pk_bf16_f32 v133, v130, v131
	ds_write_b64 v186, v[132:133] offset:3264
	ds_read_b32 v130, v187 offset:184
	s_waitcnt lgkmcnt(0)
	v_pk_fma_f32 v[132:133], v[130:131], v[180:181], 0 op_sel_hi:[0,1,0] neg_lo:[1,0,0] neg_hi:[1,0,0]
	v_pk_fma_f32 v[130:131], v[130:131], v[182:183], 0 op_sel_hi:[0,1,0] neg_lo:[1,0,0] neg_hi:[1,0,0]
	v_cvt_pk_bf16_f32 v132, v132, v133
	v_cvt_pk_bf16_f32 v133, v130, v131
	ds_write_b64 v186, v[132:133] offset:3808
	ds_read_b128 v[130:133], v1
	ds_read_b128 v[134:137], v1 offset:64
	ds_read_b128 v[138:141], v1 offset:128
	ds_read_b128 v[142:145], v1 offset:192
	s_ashr_i32 s7, s6, 31
	s_lshl_b64 s[0:1], s[6:7], 2
	s_add_u32 s0, s4, s0
	s_addc_u32 s1, s5, s1
	v_lshlrev_b32_e32 v1, 4, v0
	s_add_i32 s20, s34, 1
	s_add_i32 s34, s34, -1
	v_or_b32_e32 v153, s10, v206
	s_xor_b32 s26, s3, 2
	s_lshl_b64 s[10:11], s[10:11], 3
	s_and_b32 s20, s20, 3
	s_and_b32 s27, s34, 3
	s_add_u32 s10, s14, s10
	s_addc_u32 s11, s15, s11
	s_lshl_b32 s42, s35, 2
	s_add_i32 s41, s42, 0x26a20
	s_add_i32 s42, s42, 0x26a00
	v_lshlrev_b32_e32 v190, 3, v206
	s_cmp_eq_u32 s35, 3
	v_lshlrev_b32_e32 v150, 3, v0
	v_and_b32_e32 v151, 1, v0
	v_lshl_add_u64 v[0:1], v[154:155], 3, s[14:15]
	v_lshl_add_u64 v[192:193], s[10:11], 0, v[190:191]
	s_cselect_b64 s[10:11], -1, 0
	s_lshl_b32 s14, s3, 2
	s_add_u32 s24, s16, s14
	v_or_b32_e32 v155, 0x20000, v150
	v_add_u32_e32 v156, 0x20880, v150
	v_lshlrev_b32_e32 v150, 1, v153
	s_addc_u32 s25, s17, 0
	s_lshl_b32 s43, s3, 9
	v_lshl_add_u32 v212, s26, 9, v150
	s_lshl_b32 s15, s26, 8
	s_add_i32 s26, s43, 0x200
	v_mov_b32_e32 v152, 0x880
	v_cmp_lt_u32_e64 s[0:1], 15, v206
	v_cmp_eq_u32_e32 vcc, 1, v151
	s_and_b32 s45, s26, 0x600
	s_add_i32 s26, s43, 0x500
	v_cndmask_b32_e32 v211, 0, v152, vcc
	s_and_b32 s56, s26, 0x700
	s_add_i32 s26, s43, 0x540
	v_lshl_add_u32 v213, s20, 9, v150
	v_lshl_add_u32 v214, s27, 9, v150
	s_and_b32 s57, s26, 0x740
	s_add_i32 s26, s43, 0x580
	s_and_b32 s58, s26, 0x780
	s_add_i32 s26, s43, 0x5c0
	s_and_b32 s59, s26, 0x7c0
	s_add_i32 s26, s43, 0x600
	s_and_b32 s60, s26, 0x600
	s_add_i32 s26, s43, 0x640
	s_and_b32 s61, s26, 0x640
	s_add_i32 s26, s43, 0x680
	s_and_b32 s62, s26, 0x680
	s_add_i32 s26, s43, 0x6c0
	s_and_b32 s63, s26, 0x6c0
	s_add_i32 s26, s43, 0x700
	s_and_b32 s64, s26, 0x700
	s_add_i32 s26, s43, 0x740
	s_and_b32 s65, s26, 0x740
	s_add_i32 s26, s43, 0x780
	s_lshl_b32 s14, s27, 8
	s_lshl_b32 s20, s20, 8
	s_add_i32 s27, s43, 0x240
	s_add_i32 s28, s43, 0x280
	s_add_i32 s29, s43, 0x2c0
	s_add_i32 s30, s43, 0x300
	s_add_i32 s31, s43, 0x340
	s_add_i32 s34, s43, 0x380
	s_add_i32 s35, s43, 0x3c0
	s_add_i32 s36, s43, 0x440
	s_add_i32 s37, s43, 0x480
	s_add_i32 s38, s43, 0x4c0
	s_and_b32 s66, s26, 0x780
	s_add_i32 s26, s43, 0x7c0
	s_mul_hi_i32 s23, s18, 0x65
	s_mul_i32 s22, s18, 0x65
	v_cmp_eq_u32_e64 s[4:5], 1, v185
	v_cmp_eq_u32_e64 s[6:7], 2, v185
	v_cmp_eq_u32_e64 s[8:9], 63, v206
	s_xor_b32 s44, s43, 0x400
	s_and_b32 s46, s27, 0x640
	s_and_b32 s47, s28, 0x680
	s_waitcnt lgkmcnt(0)
	v_mov_b32_e32 v146, 0x20000
	s_and_b32 s48, s29, 0x6c0
	s_and_b32 s49, s30, 0x700
	s_and_b32 s50, s31, 0x740
	s_and_b32 s51, s34, 0x780
	s_and_b32 s52, s35, 0x7c0
	s_and_b32 s53, s36, 0x640
	s_and_b32 s54, s37, 0x680
	s_and_b32 s55, s38, 0x6c0
	s_and_b32 s67, s26, 0x7c0
	s_and_b64 s[26:27], s[10:11], s[12:13]
	v_lshl_add_u32 v215, v154, 1, v146
	v_mov_b32_e32 v216, 1
	s_lshl_b32 s28, s14, 3
	s_lshl_b32 s30, s15, 3
	s_lshl_b32 s34, s20, 3
	s_movk_i32 s68, 0x7fff
	s_mov_b32 s69, 0
	v_and_b32_e32 v220, 24, v206
	v_lshlrev_b32_e32 v220, 2, v220
	v_and_b32_e32 v221, 2, v206
	v_lshl_or_b32 v220, v221, 3, v220
	v_and_b32_e32 v221, 32, v206
	v_lshrrev_b32_e32 v221, 2, v221
	v_or_b32_e32 v220, v220, v221
	v_and_b32_e32 v221, 4, v206
	v_or_b32_e32 v220, v220, v221
	v_and_b32_e32 v221, 1, v206
	v_lshl_or_b32 v220, v221, 1, v220
	v_mov_b32_e32 v220, v254
	s_lshr_b32 s76, s19, 8
	s_add_i32 s76, s76, 0x20000
	v_add_u32_e32 v220, s76, v220
	v_add_u32_e32 v225, s45, v220
	v_add_u32_e32 v226, s44, v220
	v_add_u32_e32 v227, s60, v220
	v_add_u32_e32 v228, s43, v220
	v_and_b32_e32 v221, 1, v206
	v_mul_u32_u24_e32 v221, 0x880, v221
	v_lshrrev_b32_e32 v220, 4, v206
	v_lshl_add_u32 v221, v220, 5, v221
	v_and_b32_e32 v220, 2, v206
	v_lshl_add_u32 v221, v220, 3, v221
	v_add_u32_e32 v222, 0x20000, v221
	v_cmp_ne_u32_e32 vcc, 0, v220
	v_mov_b32_e32 v220, 0x44444444
	v_mov_b32_e32 v221, 0xeeeeeeee
	s_nop 1
	v_cndmask_b32_e32 v223, v220, v221, vcc
	v_cmp_lt_u32_e64 s[74:75], 47, v206
	v_mov_b32_e32 v224, v184
	ds_read_b128 v[166:169], v224 offset:0
	ds_read_b128 v[170:173], v224 offset:1024
	ds_read_b128 v[174:177], v224 offset:2048
	ds_read_b128 v[178:181], v224 offset:3072
	ds_read_b128 v[182:185], v224 offset:4096
	ds_read_b128 v[186:189], v224 offset:5120
	s_mov_b32 s20, 0
